# v40 + P2a A-row gather DMA issued two steps ahead (into the stage just consumed) instead of one; W load timing unchanged
# baseline (speedup 1.0000x reference)
.LBB0_263:
	s_sub_i32 s7, s62, s64
	v_mov_b32_e32 v162, v0
	s_min_i32 s7, s7, 0x200
	s_add_i32 s8, s7, 0x7f
	v_readfirstlane_b32 s6, v162
	s_lshr_b32 s66, s8, 7
	s_ashr_i32 s8, s6, 2
	s_and_b32 s8, s8, -16
	s_mul_i32 s8, s8, s66
	s_add_i32 s8, s8, s64
	v_bfe_u32 v2, v162, 3, 3
	v_or_b32_e32 v10, s8, v2
	s_add_i32 s65, s7, s64
	v_mov_b32_e32 v11, s64
	v_cmp_gt_i32_e32 vcc, s65, v10
	v_or_b32_e32 v4, 8, v10
	v_add_u32_e32 v6, 16, v10
	v_cndmask_b32_e32 v2, v11, v10, vcc
	v_cmp_gt_i32_e32 vcc, s65, v4
	s_cmpk_gt_u32 s7, 0x80
	s_cselect_b64 s[46:47], -1, 0
	v_cndmask_b32_e32 v4, v11, v4, vcc
	v_cmp_gt_i32_e32 vcc, s65, v6
	s_and_b64 vcc, s[46:47], vcc
	v_add_u32_e32 v8, 24, v10
	v_cndmask_b32_e32 v6, v11, v6, vcc
	v_cmp_gt_i32_e32 vcc, s65, v8
	s_and_b64 vcc, s[46:47], vcc
	v_ashrrev_i32_e32 v3, 31, v2
	v_ashrrev_i32_e32 v7, 31, v6
	v_cndmask_b32_e32 v8, v11, v8, vcc
	v_lshl_add_u64 v[2:3], v[2:3], 2, s[24:25]
	v_ashrrev_i32_e32 v5, 31, v4
	v_lshl_add_u64 v[6:7], v[6:7], 2, s[24:25]
	v_ashrrev_i32_e32 v9, 31, v8
	v_lshl_add_u64 v[4:5], v[4:5], 2, s[24:25]
	v_lshl_add_u64 v[8:9], v[8:9], 2, s[24:25]
	global_load_dword v12, v[2:3], off
	global_load_dword v13, v[4:5], off
	s_nop 0
	global_load_dword v6, v[6:7], off
	s_nop 0
	global_load_dword v7, v[8:9], off
	v_add_u32_e32 v2, 32, v10
	s_cmpk_gt_u32 s7, 0x100
	s_cselect_b64 s[44:45], -1, 0
	v_cmp_gt_i32_e32 vcc, s65, v2
	s_and_b64 vcc, s[44:45], vcc
	v_add_u32_e32 v4, 40, v10
	v_cndmask_b32_e32 v2, v11, v2, vcc
	v_cmp_gt_i32_e32 vcc, s65, v4
	s_and_b64 vcc, s[44:45], vcc
	v_ashrrev_i32_e32 v3, 31, v2
	v_cndmask_b32_e32 v4, v11, v4, vcc
	v_lshl_add_u64 v[2:3], v[2:3], 2, s[24:25]
	v_ashrrev_i32_e32 v5, 31, v4
	v_lshl_add_u64 v[4:5], v[4:5], 2, s[24:25]
	global_load_dword v8, v[2:3], off
	global_load_dword v9, v[4:5], off
	v_add_u32_e32 v2, 48, v10
	s_cmpk_gt_u32 s7, 0x180
	s_cselect_b64 s[42:43], -1, 0
	v_cmp_gt_i32_e32 vcc, s65, v2
	s_and_b64 vcc, s[42:43], vcc
	v_add_u32_e32 v4, 56, v10
	v_cndmask_b32_e32 v2, v11, v2, vcc
	v_cmp_gt_i32_e32 vcc, s65, v4
	s_and_b64 vcc, s[42:43], vcc
	v_ashrrev_i32_e32 v3, 31, v2
	v_cndmask_b32_e32 v4, v11, v4, vcc
	v_lshl_add_u64 v[2:3], v[2:3], 2, s[24:25]
	v_ashrrev_i32_e32 v5, 31, v4
	v_lshl_add_u64 v[4:5], v[4:5], 2, s[24:25]
	global_load_dword v131, v[2:3], off
	global_load_dword v130, v[4:5], off
	v_and_b32_e32 v10, 31, v162
	v_and_b32_e32 v2, 7, v162
	v_bfe_u32 v3, v162, 4, 2
	v_cmp_gt_u32_e32 vcc, 16, v10
	v_bitop3_b32 v2, v3, v2, 4 bitop3:0x36
	v_ashrrev_i32_e32 v11, 5, v162
	v_cndmask_b32_e32 v15, v166, v167, vcc
	v_bitop3_b32 v14, v3, v162, 7 bitop3:0x78
	v_lshlrev_b32_e32 v132, 4, v2
	v_lshl_add_u32 v2, v10, 4, v15
	v_lshlrev_b32_e32 v133, 4, v14
	v_lshl_or_b32 v168, v11, 13, v2
	global_load_dwordx4 v[228:231], v168, s[22:23]
	global_load_dwordx4 v[232:235], v168, s[22:23] offset:2048
	global_load_dwordx4 v[236:239], v168, s[28:29]
	global_load_dwordx4 v[240:243], v168, s[28:29] offset:2048
	global_load_dwordx4 v[60:63], v168, s[30:31]
	global_load_dwordx4 v[64:67], v168, s[30:31] offset:2048
	global_load_dwordx4 v[68:71], v168, s[34:35]
	global_load_dwordx4 v[72:75], v168, s[34:35] offset:2048
	v_lshrrev_b32_e32 v5, 4, v162
	v_lshlrev_b32_e32 v3, 11, v3
	s_lshl_b32 s6, s6, 8
	s_and_b32 s6, s6, 0xffffc000
	v_and_b32_e32 v4, 15, v162
	s_add_i32 s67, s6, 0
	s_add_i32 s68, s67, 0x400
	s_mov_b64 s[6:7], -1
	s_mov_b64 s[8:9], 0
	s_cmp_lt_i32 s66, 2
	s_mov_b64 s[10:11], 0
	s_waitcnt vmcnt(15)
	v_lshlrev_b32_e32 v2, 8, v12
	v_and_or_b32 v169, v2, s60, v133
	s_waitcnt vmcnt(14)
	v_lshlrev_b32_e32 v2, 8, v13
	v_and_or_b32 v170, v2, s60, v132
	s_waitcnt vmcnt(13)
	v_lshlrev_b32_e32 v2, 8, v6
	s_waitcnt vmcnt(12)
	v_lshlrev_b32_e32 v6, 8, v7
	v_and_or_b32 v175, v6, s60, v132
	v_and_or_b32 v174, v2, s60, v133
	s_waitcnt vmcnt(11)
	v_lshlrev_b32_e32 v2, 8, v8
	s_waitcnt vmcnt(10)
	v_lshlrev_b32_e32 v6, 8, v9
	v_and_or_b32 v177, v6, s60, v132
	v_lshlrev_b32_e32 v6, 3, v162
	v_and_or_b32 v176, v2, s60, v133
	v_lshlrev_b32_e32 v2, 10, v11
	v_and_b32_e32 v6, 24, v6
	v_add3_u32 v173, s61, v2, v6
	v_bfe_u32 v2, v162, 2, 3
	v_bitop3_b32 v134, v2, v5, 4 bitop3:0x78
	v_bfe_u32 v2, v162, 2, 2
	v_lshlrev_b32_e32 v7, 8, v2
	v_add3_u32 v3, s61, v3, v7
	v_lshrrev_b32_e32 v7, 2, v162
	v_and_or_b32 v2, v7, 4, v2
	v_lshlrev_b32_e32 v2, 5, v2
	v_add3_u32 v171, v3, v6, v2
	v_bfe_u32 v3, v162, 1, 3
	v_bitop3_b32 v3, v5, v3, 3 bitop3:0x6c
	v_lshlrev_b32_e32 v2, 7, v4
	v_lshlrev_b32_e32 v3, 4, v3
	v_add3_u32 v172, s67, v2, v3
	s_cbranch_scc1 .LBB0_275
	s_cmp_gt_i32 s66, 2
	s_cbranch_scc0 .LBB0_269
	s_cmp_eq_u32 s66, 3
	s_mov_b64 s[10:11], -1
	s_cbranch_scc0 .LBB0_270
	s_mov_b32 s6, m0
	s_mov_b32 m0, s67
	s_nop 0
	global_load_lds_dwordx4 v169, s[18:19]
	s_mov_b32 m0, s6
	s_add_i32 s52, s67, 0x800
	s_mov_b32 s6, m0
	s_mov_b32 m0, s68
	s_nop 0
	global_load_lds_dwordx4 v170, s[18:19]
	s_mov_b32 m0, s6
	s_add_i32 s53, s67, 0xc00
	s_mov_b32 s6, m0
	s_mov_b32 m0, s52
	s_nop 0
	global_load_lds_dwordx4 v174, s[18:19]
	s_mov_b32 m0, s6
	s_add_i32 s69, s67, 0x1000
	s_mov_b32 s6, m0
	s_mov_b32 m0, s53
	s_nop 0
	global_load_lds_dwordx4 v175, s[18:19]
	s_mov_b32 m0, s6
	s_add_i32 s70, s67, 0x1400
	s_mov_b32 s6, m0
	s_mov_b32 m0, s69
	s_nop 0
	global_load_lds_dwordx4 v176, s[18:19]
	s_mov_b32 m0, s6
	v_mov_b32_e32 v26, 0
	s_mov_b32 s6, m0
	s_mov_b32 m0, s70
	s_nop 0
	global_load_lds_dwordx4 v177, s[18:19]
	s_mov_b32 m0, s6
	s_waitcnt vmcnt(6)
	v_mov_b32_e32 v106, v60
	v_mov_b32_e32 v107, v61
	v_mov_b32_e32 v108, v62
	v_mov_b32_e32 v109, v63
	v_mov_b32_e32 v102, v64
	v_mov_b32_e32 v103, v65
	v_mov_b32_e32 v104, v66
	v_mov_b32_e32 v105, v67
	v_mov_b32_e32 v110, v68
	v_mov_b32_e32 v111, v69
	v_mov_b32_e32 v112, v70
	v_mov_b32_e32 v113, v71
	v_mov_b32_e32 v98, v72
	v_mov_b32_e32 v99, v73
	v_mov_b32_e32 v100, v74
	v_mov_b32_e32 v101, v75
	v_xor_b32_e32 v139, 64, v172
	v_cvt_pk_bf16_f32 v2, v228, v229
	v_cvt_pk_bf16_f32 v3, v230, v231
	v_lshlrev_b32_e32 v4, 5, v134
	v_add_u32_e32 v135, v173, v4
	v_xor_b32_e32 v5, 32, v4
	ds_write_b64 v135, v[2:3]
	v_cvt_pk_bf16_f32 v2, v232, v233
	v_cvt_pk_bf16_f32 v3, v234, v235
	v_add_u32_e32 v136, v173, v5
	v_xor_b32_e32 v5, 64, v4
	ds_write_b64 v136, v[2:3] offset:256
	v_cvt_pk_bf16_f32 v2, v236, v237
	v_cvt_pk_bf16_f32 v3, v238, v239
	v_add_u32_e32 v137, v173, v5
	v_xor_b32_e32 v4, 0x60, v4
	ds_write_b64 v137, v[2:3] offset:512
	v_cvt_pk_bf16_f32 v2, v240, v241
	v_cvt_pk_bf16_f32 v3, v242, v243
	v_add_u32_e32 v138, v173, v4
	ds_write_b64 v138, v[2:3] offset:768
	global_load_dwordx4 v[122:125], v168, s[38:39]
	global_load_dwordx4 v[118:121], v168, s[38:39] offset:2048
	global_load_dwordx4 v[126:129], v168, s[40:41]
	global_load_dwordx4 v[114:117], v168, s[40:41] offset:2048
	s_waitcnt lgkmcnt(0)
	s_barrier
	v_add_u32_e32 v2, 0x2000, v172
	s_add_i32 s71, s67, 0x2000
	v_xor_b32_e32 v140, 64, v2
	v_xor_b32_e32 v141, 32, v171
	v_xor_b32_e32 v142, 64, v171
	v_xor_b32_e32 v143, 0x60, v171
	v_xor_b32_e32 v144, 0x80, v171
	v_xor_b32_e32 v145, 0xa0, v171
	v_xor_b32_e32 v146, 0xc0, v171
	s_add_i32 s72, s67, 0x2400
	v_xor_b32_e32 v147, 0xe0, v171
	s_add_i32 s73, s67, 0x2800
	s_add_i32 s74, s67, 0x2c00
	s_add_i32 s75, s67, 0x3000
	s_add_i32 s76, s67, 0x3400
	s_mov_b32 s50, 0
	s_mov_b64 s[10:11], 0
	v_mov_b32_e32 v27, v26
	v_mov_b32_e32 v28, v26
	v_mov_b32_e32 v29, v26
	v_mov_b32_e32 v2, v26
	v_mov_b32_e32 v3, v26
	v_mov_b32_e32 v4, v26
	v_mov_b32_e32 v5, v26
	v_mov_b32_e32 v10, v26
	v_mov_b32_e32 v11, v26
	v_mov_b32_e32 v12, v26
	v_mov_b32_e32 v13, v26
	v_mov_b32_e32 v50, v26
	v_mov_b32_e32 v51, v26
	v_mov_b32_e32 v52, v26
	v_mov_b32_e32 v53, v26
	v_mov_b32_e32 v14, v26
	v_mov_b32_e32 v15, v26
	v_mov_b32_e32 v16, v26
	v_mov_b32_e32 v17, v26
	v_mov_b32_e32 v30, v26
	v_mov_b32_e32 v31, v26
	v_mov_b32_e32 v32, v26
	v_mov_b32_e32 v33, v26
	v_mov_b32_e32 v66, v26
	v_mov_b32_e32 v67, v26
	v_mov_b32_e32 v68, v26
	v_mov_b32_e32 v69, v26
	v_mov_b32_e32 v34, v26
	v_mov_b32_e32 v35, v26
	v_mov_b32_e32 v36, v26
	v_mov_b32_e32 v37, v26
	v_mov_b32_e32 v62, v26
	v_mov_b32_e32 v63, v26
	v_mov_b32_e32 v64, v26
	v_mov_b32_e32 v65, v26
	v_mov_b32_e32 v82, v26
	v_mov_b32_e32 v83, v26
	v_mov_b32_e32 v84, v26
	v_mov_b32_e32 v85, v26
	v_mov_b32_e32 v54, v26
	v_mov_b32_e32 v55, v26
	v_mov_b32_e32 v56, v26
	v_mov_b32_e32 v57, v26
	v_mov_b32_e32 v86, v26
	v_mov_b32_e32 v87, v26
	v_mov_b32_e32 v88, v26
	v_mov_b32_e32 v89, v26
	v_mov_b32_e32 v22, v26
	v_mov_b32_e32 v23, v26
	v_mov_b32_e32 v24, v26
	v_mov_b32_e32 v25, v26
	v_mov_b32_e32 v6, v26
	v_mov_b32_e32 v7, v26
	v_mov_b32_e32 v8, v26
	v_mov_b32_e32 v9, v26
	v_mov_b32_e32 v42, v26
	v_mov_b32_e32 v43, v26
	v_mov_b32_e32 v44, v26
	v_mov_b32_e32 v45, v26
	v_mov_b32_e32 v38, v26
	v_mov_b32_e32 v39, v26
	v_mov_b32_e32 v40, v26
	v_mov_b32_e32 v41, v26
	v_mov_b32_e32 v18, v26
	v_mov_b32_e32 v19, v26
	v_mov_b32_e32 v20, v26
	v_mov_b32_e32 v21, v26
	v_mov_b32_e32 v70, v26
	v_mov_b32_e32 v71, v26
	v_mov_b32_e32 v72, v26
	v_mov_b32_e32 v73, v26
	v_mov_b32_e32 v58, v26
	v_mov_b32_e32 v59, v26
	v_mov_b32_e32 v60, v26
	v_mov_b32_e32 v61, v26
	v_mov_b32_e32 v46, v26
	v_mov_b32_e32 v47, v26
	v_mov_b32_e32 v48, v26
	v_mov_b32_e32 v49, v26
	v_mov_b32_e32 v90, v26
	v_mov_b32_e32 v91, v26
	v_mov_b32_e32 v92, v26
	v_mov_b32_e32 v93, v26
	v_mov_b32_e32 v78, v26
	v_mov_b32_e32 v79, v26
	v_mov_b32_e32 v80, v26
	v_mov_b32_e32 v81, v26
	v_mov_b32_e32 v74, v26
	v_mov_b32_e32 v75, v26
	v_mov_b32_e32 v76, v26
	v_mov_b32_e32 v77, v26
	v_mov_b32_e32 v94, v26
	v_mov_b32_e32 v95, v26
	v_mov_b32_e32 v96, v26
	v_mov_b32_e32 v97, v26
	s_add_u32 s48, s18, 0x80
	s_addc_u32 s49, s19, 0
	s_mov_b32 s78, m0
	s_mov_b32 m0, s71
	s_nop 0
	global_load_lds_dwordx4 v169, s[48:49]
	s_mov_b32 m0, s78
	s_mov_b32 s78, m0
	s_mov_b32 m0, s72
	s_nop 0
	global_load_lds_dwordx4 v170, s[48:49]
	s_mov_b32 m0, s78
	s_mov_b32 s78, m0
	s_mov_b32 m0, s73
	s_nop 0
	global_load_lds_dwordx4 v174, s[48:49]
	s_mov_b32 m0, s78
	s_mov_b32 s78, m0
	s_mov_b32 m0, s74
	s_nop 0
	global_load_lds_dwordx4 v175, s[48:49]
	s_mov_b32 m0, s78
	s_mov_b32 s78, m0
	s_mov_b32 m0, s75
	s_nop 0
	global_load_lds_dwordx4 v176, s[48:49]
	s_mov_b32 m0, s78
	s_mov_b32 s78, m0
	s_mov_b32 m0, s76
	s_nop 0
	global_load_lds_dwordx4 v177, s[48:49]
	s_mov_b32 m0, s78
.LBB0_267:
	s_waitcnt vmcnt(10)
	s_min_u32 s6, s50, 12
	ds_read_b128 v[148:151], v172
	ds_read_b128 v[152:155], v172 offset:2048
	ds_read_b128 v[156:159], v172 offset:4096
	ds_read_b64_tr_b16 v[178:179], v171
	ds_read_b64_tr_b16 v[180:181], v171 offset:1024
	s_cmp_lt_u32 s50, 13
	s_cselect_b64 vcc, -1, 0
	s_lshl_b32 s6, s6, 17
	s_add_u32 s51, s22, s6
	s_addc_u32 s77, s23, 0
	s_add_u32 s6, s51, 0x60000
	ds_read_b64_tr_b16 v[182:183], v141
	ds_read_b64_tr_b16 v[184:185], v141 offset:1024
	s_addc_u32 s7, s77, 0
	s_waitcnt lgkmcnt(2)
	v_mfma_f32_16x16x32_bf16 v[94:97], v[178:181], v[148:151], v[94:97]
	s_add_u32 s48, s10, 0x100
	s_min_u32 s48, s48, 0x780
	s_add_u32 s48, s18, s48
	v_mfma_f32_16x16x32_bf16 v[74:77], v[178:181], v[152:155], v[74:77]
	v_cvt_pk_bf16_f32 v106, v106, v107
	v_cvt_pk_bf16_f32 v107, v108, v109
	v_cndmask_b32_e32 v160, 0, v168, vcc
	v_mfma_f32_16x16x32_bf16 v[78:81], v[178:181], v[156:159], v[78:81]
	s_addc_u32 s49, s19, 0
	ds_write_b64 v135, v[106:107] offset:16384
	ds_read_b64_tr_b16 v[106:107], v142
	ds_read_b64_tr_b16 v[108:109], v142 offset:1024
	s_waitcnt lgkmcnt(3)
	v_mfma_f32_16x16x32_bf16 v[90:93], v[182:185], v[148:151], v[90:93]
	v_cvt_pk_bf16_f32 v102, v102, v103
	v_cvt_pk_bf16_f32 v103, v104, v105
	ds_write_b64 v136, v[102:103] offset:16640
	v_mfma_f32_16x16x32_bf16 v[46:49], v[182:185], v[152:155], v[46:49]
	v_mfma_f32_16x16x32_bf16 v[58:61], v[182:185], v[156:159], v[58:61]
	ds_read_b64_tr_b16 v[102:103], v143
	ds_read_b64_tr_b16 v[104:105], v143 offset:1024
	s_waitcnt lgkmcnt(3)
	v_mfma_f32_16x16x32_bf16 v[70:73], v[106:109], v[148:151], v[70:73]
	v_cvt_pk_bf16_f32 v110, v110, v111
	v_cvt_pk_bf16_f32 v111, v112, v113
	ds_write_b64 v137, v[110:111] offset:16896
	v_mfma_f32_16x16x32_bf16 v[18:21], v[106:109], v[152:155], v[18:21]
	v_mfma_f32_16x16x32_bf16 v[38:41], v[106:109], v[156:159], v[38:41]
	ds_read_b64_tr_b16 v[106:107], v144
	ds_read_b64_tr_b16 v[108:109], v144 offset:1024
	s_waitcnt lgkmcnt(3)
	v_mfma_f32_16x16x32_bf16 v[42:45], v[102:105], v[148:151], v[42:45]
	v_cvt_pk_bf16_f32 v98, v98, v99
	v_cvt_pk_bf16_f32 v99, v100, v101
	ds_write_b64 v138, v[98:99] offset:17152
	v_mfma_f32_16x16x32_bf16 v[6:9], v[102:105], v[152:155], v[6:9]
	v_mfma_f32_16x16x32_bf16 v[22:25], v[102:105], v[156:159], v[22:25]
	ds_read_b64_tr_b16 v[98:99], v145
	ds_read_b64_tr_b16 v[100:101], v145 offset:1024
	s_waitcnt lgkmcnt(3)
	v_mfma_f32_16x16x32_bf16 v[86:89], v[106:109], v[148:151], v[86:89]
	v_mfma_f32_16x16x32_bf16 v[54:57], v[106:109], v[152:155], v[54:57]
	v_mfma_f32_16x16x32_bf16 v[82:85], v[106:109], v[156:159], v[82:85]
	ds_read_b64_tr_b16 v[102:103], v146
	ds_read_b64_tr_b16 v[104:105], v146 offset:1024
	s_waitcnt lgkmcnt(2)
	v_mfma_f32_16x16x32_bf16 v[62:65], v[98:101], v[148:151], v[62:65]
	v_mfma_f32_16x16x32_bf16 v[34:37], v[98:101], v[152:155], v[34:37]
	v_mfma_f32_16x16x32_bf16 v[66:69], v[98:101], v[156:159], v[66:69]
	ds_read_b64_tr_b16 v[98:99], v147
	ds_read_b64_tr_b16 v[100:101], v147 offset:1024
	s_waitcnt lgkmcnt(2)
	v_mfma_f32_16x16x32_bf16 v[30:33], v[102:105], v[148:151], v[30:33]
	v_mfma_f32_16x16x32_bf16 v[14:17], v[102:105], v[152:155], v[14:17]
	v_mfma_f32_16x16x32_bf16 v[50:53], v[102:105], v[156:159], v[50:53]
	s_waitcnt lgkmcnt(0)
	v_mfma_f32_16x16x32_bf16 v[10:13], v[98:101], v[148:151], v[10:13]
	ds_read_b64_tr_b16 v[102:103], v171 offset:8192
	ds_read_b64_tr_b16 v[104:105], v171 offset:9216
	v_mfma_f32_16x16x32_bf16 v[2:5], v[98:101], v[152:155], v[2:5]
	ds_read_b128 v[148:151], v139
	ds_read_b128 v[152:155], v139 offset:2048
	ds_read_b128 v[178:181], v139 offset:4096
	v_mfma_f32_16x16x32_bf16 v[26:29], v[98:101], v[156:159], v[26:29]
	ds_read_b64_tr_b16 v[98:99], v141 offset:8192
	ds_read_b64_tr_b16 v[100:101], v141 offset:9216
	s_waitcnt lgkmcnt(4)
	v_mfma_f32_16x16x32_bf16 v[94:97], v[102:105], v[148:151], v[94:97]
	s_waitcnt lgkmcnt(3)
	v_mfma_f32_16x16x32_bf16 v[74:77], v[102:105], v[152:155], v[74:77]
	s_waitcnt lgkmcnt(2)
	v_mfma_f32_16x16x32_bf16 v[78:81], v[102:105], v[178:181], v[78:81]
	s_mov_b32 s78, m0
	s_mov_b32 m0, s67
	s_nop 0
	global_load_lds_dwordx4 v169, s[48:49]
	s_mov_b32 m0, s78
	ds_read_b64_tr_b16 v[102:103], v142 offset:8192
	ds_read_b64_tr_b16 v[104:105], v142 offset:9216
	s_waitcnt lgkmcnt(2)
	v_mfma_f32_16x16x32_bf16 v[90:93], v[98:101], v[148:151], v[90:93]
	s_mov_b32 s78, m0
	s_mov_b32 m0, s68
	s_nop 0
	global_load_lds_dwordx4 v170, s[48:49]
	s_mov_b32 m0, s78
	v_mfma_f32_16x16x32_bf16 v[46:49], v[98:101], v[152:155], v[46:49]
	v_mfma_f32_16x16x32_bf16 v[58:61], v[98:101], v[178:181], v[58:61]
	ds_read_b64_tr_b16 v[98:99], v143 offset:8192
	ds_read_b64_tr_b16 v[100:101], v143 offset:9216
	s_waitcnt lgkmcnt(2)
	v_mfma_f32_16x16x32_bf16 v[70:73], v[102:105], v[148:151], v[70:73]
	s_mov_b32 s78, m0
	s_mov_b32 m0, s52
	s_nop 0
	global_load_lds_dwordx4 v174, s[48:49]
	s_mov_b32 m0, s78
	v_mfma_f32_16x16x32_bf16 v[18:21], v[102:105], v[152:155], v[18:21]
	v_mfma_f32_16x16x32_bf16 v[38:41], v[102:105], v[178:181], v[38:41]
	ds_read_b64_tr_b16 v[102:103], v144 offset:8192
	ds_read_b64_tr_b16 v[104:105], v144 offset:9216
	s_waitcnt lgkmcnt(2)
	v_mfma_f32_16x16x32_bf16 v[42:45], v[98:101], v[148:151], v[42:45]
	s_mov_b32 s78, m0
	s_mov_b32 m0, s53
	s_nop 0
	global_load_lds_dwordx4 v175, s[48:49]
	s_mov_b32 m0, s78
	v_mfma_f32_16x16x32_bf16 v[6:9], v[98:101], v[152:155], v[6:9]
	v_mfma_f32_16x16x32_bf16 v[22:25], v[98:101], v[178:181], v[22:25]
	ds_read_b64_tr_b16 v[98:99], v145 offset:8192
	ds_read_b64_tr_b16 v[100:101], v145 offset:9216
	s_waitcnt lgkmcnt(2)
	v_mfma_f32_16x16x32_bf16 v[86:89], v[102:105], v[148:151], v[86:89]
	s_mov_b32 s78, m0
	s_mov_b32 m0, s69
	s_nop 0
	global_load_lds_dwordx4 v176, s[48:49]
	s_mov_b32 m0, s78
	global_load_dwordx4 v[106:109], v160, s[6:7]
	v_mfma_f32_16x16x32_bf16 v[54:57], v[102:105], v[152:155], v[54:57]
	v_mfma_f32_16x16x32_bf16 v[82:85], v[102:105], v[178:181], v[82:85]
	ds_read_b64_tr_b16 v[156:157], v146 offset:8192
	ds_read_b64_tr_b16 v[158:159], v146 offset:9216
	s_waitcnt lgkmcnt(2)
	v_mfma_f32_16x16x32_bf16 v[62:65], v[98:101], v[148:151], v[62:65]
	s_mov_b32 s78, m0
	s_mov_b32 m0, s70
	s_nop 0
	global_load_lds_dwordx4 v177, s[48:49]
	s_mov_b32 m0, s78
	global_load_dwordx4 v[102:105], v160, s[6:7] offset:2048
	v_mfma_f32_16x16x32_bf16 v[34:37], v[98:101], v[152:155], v[34:37]
	v_mfma_f32_16x16x32_bf16 v[66:69], v[98:101], v[178:181], v[66:69]
	ds_read_b64_tr_b16 v[182:183], v147 offset:8192
	ds_read_b64_tr_b16 v[184:185], v147 offset:9216
	s_waitcnt lgkmcnt(2)
	v_mfma_f32_16x16x32_bf16 v[30:33], v[156:159], v[148:151], v[30:33]
	s_add_u32 s6, s51, 0x61000
	s_addc_u32 s7, s77, 0
	global_load_dwordx4 v[110:113], v160, s[6:7]
	v_mfma_f32_16x16x32_bf16 v[14:17], v[156:159], v[152:155], v[14:17]
	v_mfma_f32_16x16x32_bf16 v[50:53], v[156:159], v[178:181], v[50:53]
	s_waitcnt lgkmcnt(0)
	v_mfma_f32_16x16x32_bf16 v[10:13], v[182:185], v[148:151], v[10:13]
	global_load_dwordx4 v[98:101], v160, s[6:7] offset:2048
	v_mfma_f32_16x16x32_bf16 v[2:5], v[182:185], v[152:155], v[2:5]
	v_mfma_f32_16x16x32_bf16 v[26:29], v[182:185], v[178:181], v[26:29]
	s_min_u32 s6, s50, 11
	s_add_i32 s77, s50, 2
	s_cmp_lt_u32 s50, 12
	s_cselect_b64 vcc, -1, 0
	s_lshl_b32 s6, s6, 17
	s_waitcnt lgkmcnt(0)
	s_barrier
	s_add_u32 s78, s22, s6
	s_waitcnt vmcnt(10)
	s_addc_u32 s79, s23, 0
	s_add_u32 s48, s78, 0x80000
	ds_read_b64_tr_b16 v[148:149], v171 offset:16384
	ds_read_b64_tr_b16 v[150:151], v171 offset:17408
	ds_read_b128 v[152:155], v172 offset:8192
	ds_read_b128 v[156:159], v172 offset:10240
	ds_read_b128 v[178:181], v172 offset:12288
	s_addc_u32 s49, s79, 0
	s_add_u32 s10, s10, 0x100
	s_addc_u32 s11, s11, 0
	s_cmp_lt_u32 s50, 14
	ds_read_b64_tr_b16 v[182:183], v141 offset:16384
	ds_read_b64_tr_b16 v[184:185], v141 offset:17408
	s_cselect_b64 s[6:7], -1, 0
	s_waitcnt lgkmcnt(4)
	v_mfma_f32_16x16x32_bf16 v[94:97], v[148:151], v[152:155], v[94:97]
	v_cndmask_b32_e32 v160, 0, v168, vcc
	s_and_b64 vcc, s[6:7], exec
	s_add_i32 s50, s10, 0x80
	s_min_u32 s50, s50, 0x780
	s_waitcnt lgkmcnt(3)
	v_mfma_f32_16x16x32_bf16 v[74:77], v[148:151], v[156:159], v[74:77]
	s_add_u32 s50, s18, s50
	v_cvt_pk_bf16_f32 v122, v122, v123
	v_cvt_pk_bf16_f32 v123, v124, v125
	s_waitcnt lgkmcnt(2)
	v_mfma_f32_16x16x32_bf16 v[78:81], v[148:151], v[178:181], v[78:81]
	s_addc_u32 s51, s19, 0
	ds_write_b64 v135, v[122:123]
	ds_read_b64_tr_b16 v[122:123], v142 offset:16384
	ds_read_b64_tr_b16 v[124:125], v142 offset:17408
	s_waitcnt lgkmcnt(3)
	v_mfma_f32_16x16x32_bf16 v[90:93], v[182:185], v[152:155], v[90:93]
	v_cvt_pk_bf16_f32 v118, v118, v119
	v_cvt_pk_bf16_f32 v119, v120, v121
	ds_write_b64 v136, v[118:119] offset:256
	v_mfma_f32_16x16x32_bf16 v[46:49], v[182:185], v[156:159], v[46:49]
	v_mfma_f32_16x16x32_bf16 v[58:61], v[182:185], v[178:181], v[58:61]
	ds_read_b64_tr_b16 v[118:119], v143 offset:16384
	ds_read_b64_tr_b16 v[120:121], v143 offset:17408
	s_waitcnt lgkmcnt(3)
	v_mfma_f32_16x16x32_bf16 v[70:73], v[122:125], v[152:155], v[70:73]
	v_cvt_pk_bf16_f32 v126, v126, v127
	v_cvt_pk_bf16_f32 v127, v128, v129
	ds_write_b64 v137, v[126:127] offset:512
	v_mfma_f32_16x16x32_bf16 v[18:21], v[122:125], v[156:159], v[18:21]
	v_mfma_f32_16x16x32_bf16 v[38:41], v[122:125], v[178:181], v[38:41]
	ds_read_b64_tr_b16 v[122:123], v144 offset:16384
	ds_read_b64_tr_b16 v[124:125], v144 offset:17408
	s_waitcnt lgkmcnt(3)
	v_mfma_f32_16x16x32_bf16 v[42:45], v[118:121], v[152:155], v[42:45]
	v_cvt_pk_bf16_f32 v114, v114, v115
	v_cvt_pk_bf16_f32 v115, v116, v117
	ds_write_b64 v138, v[114:115] offset:768
	v_mfma_f32_16x16x32_bf16 v[6:9], v[118:121], v[156:159], v[6:9]
	v_mfma_f32_16x16x32_bf16 v[22:25], v[118:121], v[178:181], v[22:25]
	ds_read_b64_tr_b16 v[114:115], v145 offset:16384
	ds_read_b64_tr_b16 v[116:117], v145 offset:17408
	s_waitcnt lgkmcnt(3)
	v_mfma_f32_16x16x32_bf16 v[86:89], v[122:125], v[152:155], v[86:89]
	v_mfma_f32_16x16x32_bf16 v[54:57], v[122:125], v[156:159], v[54:57]
	v_mfma_f32_16x16x32_bf16 v[82:85], v[122:125], v[178:181], v[82:85]
	ds_read_b64_tr_b16 v[118:119], v146 offset:16384
	ds_read_b64_tr_b16 v[120:121], v146 offset:17408
	s_waitcnt lgkmcnt(2)
	v_mfma_f32_16x16x32_bf16 v[62:65], v[114:117], v[152:155], v[62:65]
	v_mfma_f32_16x16x32_bf16 v[34:37], v[114:117], v[156:159], v[34:37]
	v_mfma_f32_16x16x32_bf16 v[66:69], v[114:117], v[178:181], v[66:69]
	ds_read_b64_tr_b16 v[114:115], v147 offset:16384
	ds_read_b64_tr_b16 v[116:117], v147 offset:17408
	s_waitcnt lgkmcnt(2)
	v_mfma_f32_16x16x32_bf16 v[30:33], v[118:121], v[152:155], v[30:33]
	v_mfma_f32_16x16x32_bf16 v[14:17], v[118:121], v[156:159], v[14:17]
	v_mfma_f32_16x16x32_bf16 v[50:53], v[118:121], v[178:181], v[50:53]
	s_waitcnt lgkmcnt(0)
	v_mfma_f32_16x16x32_bf16 v[10:13], v[114:117], v[152:155], v[10:13]
	ds_read_b64_tr_b16 v[118:119], v171 offset:24576
	ds_read_b64_tr_b16 v[120:121], v171 offset:25600
	v_mfma_f32_16x16x32_bf16 v[2:5], v[114:117], v[156:159], v[2:5]
	ds_read_b128 v[148:151], v140
	ds_read_b128 v[152:155], v140 offset:2048
	ds_read_b128 v[156:159], v140 offset:4096
	v_mfma_f32_16x16x32_bf16 v[26:29], v[114:117], v[178:181], v[26:29]
	ds_read_b64_tr_b16 v[114:115], v141 offset:24576
	ds_read_b64_tr_b16 v[116:117], v141 offset:25600
	s_waitcnt lgkmcnt(4)
	v_mfma_f32_16x16x32_bf16 v[94:97], v[118:121], v[148:151], v[94:97]
	s_waitcnt lgkmcnt(3)
	v_mfma_f32_16x16x32_bf16 v[74:77], v[118:121], v[152:155], v[74:77]
	s_waitcnt lgkmcnt(2)
	v_mfma_f32_16x16x32_bf16 v[78:81], v[118:121], v[156:159], v[78:81]
	s_mov_b32 s80, m0
	s_mov_b32 m0, s71
	s_nop 0
	global_load_lds_dwordx4 v169, s[50:51]
	s_mov_b32 m0, s80
	ds_read_b64_tr_b16 v[118:119], v142 offset:24576
	ds_read_b64_tr_b16 v[120:121], v142 offset:25600
	s_waitcnt lgkmcnt(2)
	v_mfma_f32_16x16x32_bf16 v[90:93], v[114:117], v[148:151], v[90:93]
	s_mov_b32 s80, m0
	s_mov_b32 m0, s72
	s_nop 0
	global_load_lds_dwordx4 v170, s[50:51]
	s_mov_b32 m0, s80
	v_mfma_f32_16x16x32_bf16 v[46:49], v[114:117], v[152:155], v[46:49]
	v_mfma_f32_16x16x32_bf16 v[58:61], v[114:117], v[156:159], v[58:61]
	ds_read_b64_tr_b16 v[114:115], v143 offset:24576
	ds_read_b64_tr_b16 v[116:117], v143 offset:25600
	s_waitcnt lgkmcnt(2)
	v_mfma_f32_16x16x32_bf16 v[70:73], v[118:121], v[148:151], v[70:73]
	s_mov_b32 s80, m0
	s_mov_b32 m0, s73
	s_nop 0
	global_load_lds_dwordx4 v174, s[50:51]
	s_mov_b32 m0, s80
	v_mfma_f32_16x16x32_bf16 v[18:21], v[118:121], v[152:155], v[18:21]
	v_mfma_f32_16x16x32_bf16 v[38:41], v[118:121], v[156:159], v[38:41]
	ds_read_b64_tr_b16 v[118:119], v144 offset:24576
	ds_read_b64_tr_b16 v[120:121], v144 offset:25600
	s_waitcnt lgkmcnt(2)
	v_mfma_f32_16x16x32_bf16 v[42:45], v[114:117], v[148:151], v[42:45]
	s_mov_b32 s80, m0
	s_mov_b32 m0, s74
	s_nop 0
	global_load_lds_dwordx4 v175, s[50:51]
	s_mov_b32 m0, s80
	v_mfma_f32_16x16x32_bf16 v[6:9], v[114:117], v[152:155], v[6:9]
	v_mfma_f32_16x16x32_bf16 v[22:25], v[114:117], v[156:159], v[22:25]
	ds_read_b64_tr_b16 v[114:115], v145 offset:24576
	ds_read_b64_tr_b16 v[116:117], v145 offset:25600
	s_waitcnt lgkmcnt(2)
	v_mfma_f32_16x16x32_bf16 v[86:89], v[118:121], v[148:151], v[86:89]
	s_mov_b32 s80, m0
	s_mov_b32 m0, s75
	s_nop 0
	global_load_lds_dwordx4 v176, s[50:51]
	s_mov_b32 m0, s80
	s_cbranch_vccz .Lmy_tl_267_0
	global_load_dwordx4 v[122:125], v160, s[48:49]
.Lmy_tl_267_0:
	v_mfma_f32_16x16x32_bf16 v[54:57], v[118:121], v[152:155], v[54:57]
	v_mfma_f32_16x16x32_bf16 v[82:85], v[118:121], v[156:159], v[82:85]
	ds_read_b64_tr_b16 v[178:179], v146 offset:24576
	ds_read_b64_tr_b16 v[180:181], v146 offset:25600
	s_waitcnt lgkmcnt(2)
	v_mfma_f32_16x16x32_bf16 v[62:65], v[114:117], v[148:151], v[62:65]
	s_mov_b32 s80, m0
	s_mov_b32 m0, s76
	s_nop 0
	global_load_lds_dwordx4 v177, s[50:51]
	s_mov_b32 m0, s80
	s_cbranch_vccz .Lmy_tl_267_1
	global_load_dwordx4 v[118:121], v160, s[48:49] offset:2048

.LBB0_271:
	s_mov_b32 s6, m0
	s_mov_b32 m0, s67
	s_nop 0
	global_load_lds_dwordx4 v169, s[18:19]
	s_mov_b32 m0, s6
	s_add_i32 s69, s67, 0x800
	s_mov_b32 s6, m0
	s_mov_b32 m0, s68
	s_nop 0
	global_load_lds_dwordx4 v170, s[18:19]
	s_mov_b32 m0, s6
	s_add_i32 s70, s67, 0xc00
	s_mov_b32 s6, m0
	s_mov_b32 m0, s69
	s_nop 0
	global_load_lds_dwordx4 v174, s[18:19]
	s_mov_b32 m0, s6
	v_xor_b32_e32 v102, 64, v172
	s_mov_b32 s6, m0
	s_mov_b32 m0, s70
	s_nop 0
	global_load_lds_dwordx4 v175, s[18:19]
	s_mov_b32 m0, s6
	s_waitcnt vmcnt(4)
	v_mov_b32_e32 v38, v60
	v_mov_b32_e32 v39, v61
	v_mov_b32_e32 v40, v62
	v_mov_b32_e32 v41, v63
	v_mov_b32_e32 v26, v64
	v_mov_b32_e32 v27, v65
	v_mov_b32_e32 v28, v66
	v_mov_b32_e32 v29, v67
	v_mov_b32_e32 v50, v68
	v_mov_b32_e32 v51, v69
	v_mov_b32_e32 v52, v70
	v_mov_b32_e32 v53, v71
	v_mov_b32_e32 v22, v72
	v_mov_b32_e32 v23, v73
	v_mov_b32_e32 v24, v74
	v_mov_b32_e32 v25, v75
	s_add_i32 s71, s67, 0x2000
	v_cvt_pk_bf16_f32 v2, v228, v229
	v_cvt_pk_bf16_f32 v3, v230, v231
	v_lshlrev_b32_e32 v4, 5, v134
	v_add_u32_e32 v98, v173, v4
	v_xor_b32_e32 v5, 32, v4
	ds_write_b64 v98, v[2:3]
	v_cvt_pk_bf16_f32 v2, v232, v233
	v_cvt_pk_bf16_f32 v3, v234, v235
	v_add_u32_e32 v99, v173, v5
	v_xor_b32_e32 v5, 64, v4
	ds_write_b64 v99, v[2:3] offset:256
	v_cvt_pk_bf16_f32 v2, v236, v237
	v_cvt_pk_bf16_f32 v3, v238, v239
	v_add_u32_e32 v100, v173, v5
	v_xor_b32_e32 v4, 0x60, v4
	ds_write_b64 v100, v[2:3] offset:512
	v_cvt_pk_bf16_f32 v2, v240, v241
	v_cvt_pk_bf16_f32 v3, v242, v243
	v_add_u32_e32 v101, v173, v4
	ds_write_b64 v101, v[2:3] offset:768
	global_load_dwordx4 v[78:81], v168, s[38:39]
	global_load_dwordx4 v[66:69], v168, s[38:39] offset:2048
	global_load_dwordx4 v[82:85], v168, s[40:41]
	global_load_dwordx4 v[58:61], v168, s[40:41] offset:2048
	s_waitcnt lgkmcnt(0)
	s_barrier
	v_add_u32_e32 v2, 0x2000, v172
	v_xor_b32_e32 v103, 64, v2
	v_mov_b32_e32 v2, 0
	v_xor_b32_e32 v104, 32, v171
	v_xor_b32_e32 v105, 64, v171
	v_xor_b32_e32 v106, 0x60, v171
	v_xor_b32_e32 v107, 0x80, v171
	v_xor_b32_e32 v108, 0xa0, v171
	v_xor_b32_e32 v109, 0xc0, v171
	s_add_i32 s72, s67, 0x2400
	v_xor_b32_e32 v110, 0xe0, v171
	s_add_i32 s73, s67, 0x2800
	s_add_i32 s74, s67, 0x2c00
	s_mov_b32 s52, 0
	s_mov_b64 s[48:49], 0
	v_mov_b32_e32 v3, v2
	v_mov_b32_e32 v4, v2
	v_mov_b32_e32 v5, v2
	v_mov_b32_e32 v10, v2
	v_mov_b32_e32 v11, v2
	v_mov_b32_e32 v12, v2
	v_mov_b32_e32 v13, v2
	v_mov_b32_e32 v14, v2
	v_mov_b32_e32 v15, v2
	v_mov_b32_e32 v16, v2
	v_mov_b32_e32 v17, v2
	v_mov_b32_e32 v30, v2
	v_mov_b32_e32 v31, v2
	v_mov_b32_e32 v32, v2
	v_mov_b32_e32 v33, v2
	v_mov_b32_e32 v34, v2
	v_mov_b32_e32 v35, v2
	v_mov_b32_e32 v36, v2
	v_mov_b32_e32 v37, v2
	v_mov_b32_e32 v62, v2
	v_mov_b32_e32 v63, v2
	v_mov_b32_e32 v64, v2
	v_mov_b32_e32 v65, v2
	v_mov_b32_e32 v54, v2
	v_mov_b32_e32 v55, v2
	v_mov_b32_e32 v56, v2
	v_mov_b32_e32 v57, v2
	v_mov_b32_e32 v86, v2
	v_mov_b32_e32 v87, v2
	v_mov_b32_e32 v88, v2
	v_mov_b32_e32 v89, v2
	v_mov_b32_e32 v6, v2
	v_mov_b32_e32 v7, v2
	v_mov_b32_e32 v8, v2
	v_mov_b32_e32 v9, v2
	v_mov_b32_e32 v42, v2
	v_mov_b32_e32 v43, v2
	v_mov_b32_e32 v44, v2
	v_mov_b32_e32 v45, v2
	v_mov_b32_e32 v18, v2
	v_mov_b32_e32 v19, v2
	v_mov_b32_e32 v20, v2
	v_mov_b32_e32 v21, v2
	v_mov_b32_e32 v70, v2
	v_mov_b32_e32 v71, v2
	v_mov_b32_e32 v72, v2
	v_mov_b32_e32 v73, v2
	v_mov_b32_e32 v46, v2
	v_mov_b32_e32 v47, v2
	v_mov_b32_e32 v48, v2
	v_mov_b32_e32 v49, v2
	v_mov_b32_e32 v90, v2
	v_mov_b32_e32 v91, v2
	v_mov_b32_e32 v92, v2
	v_mov_b32_e32 v93, v2
	v_mov_b32_e32 v74, v2
	v_mov_b32_e32 v75, v2
	v_mov_b32_e32 v76, v2
	v_mov_b32_e32 v77, v2
	v_mov_b32_e32 v94, v2
	v_mov_b32_e32 v95, v2
	v_mov_b32_e32 v96, v2
	v_mov_b32_e32 v97, v2
	s_add_u32 s50, s18, 0x80
	s_addc_u32 s51, s19, 0
	s_mov_b32 s76, m0
	s_mov_b32 m0, s71
	s_nop 0
	global_load_lds_dwordx4 v169, s[50:51]
	s_mov_b32 m0, s76
	s_mov_b32 s76, m0
	s_mov_b32 m0, s72
	s_nop 0
	global_load_lds_dwordx4 v170, s[50:51]
	s_mov_b32 m0, s76
	s_mov_b32 s76, m0
	s_mov_b32 m0, s73
	s_nop 0
	global_load_lds_dwordx4 v174, s[50:51]
	s_mov_b32 m0, s76
	s_mov_b32 s76, m0
	s_mov_b32 m0, s74
	s_nop 0
	global_load_lds_dwordx4 v175, s[50:51]
	s_mov_b32 m0, s76
.LBB0_272:
	s_waitcnt vmcnt(8)
	s_min_u32 s6, s52, 12
	ds_read_b128 v[112:115], v172
	ds_read_b128 v[116:119], v172 offset:2048
	s_cmp_lt_u32 s52, 13
	ds_read_b64_tr_b16 v[120:121], v171
	ds_read_b64_tr_b16 v[122:123], v171 offset:1024
	s_cselect_b64 vcc, -1, 0
	s_lshl_b32 s6, s6, 17
	s_add_u32 s53, s22, s6
	s_addc_u32 s75, s23, 0
	s_add_u32 s6, s53, 0x60000
	ds_read_b64_tr_b16 v[124:125], v104
	ds_read_b64_tr_b16 v[126:127], v104 offset:1024
	s_addc_u32 s7, s75, 0
	s_waitcnt lgkmcnt(2)
	v_mfma_f32_16x16x32_bf16 v[94:97], v[120:123], v[112:115], v[94:97]
	s_add_u32 s50, s48, 0x100
	s_min_u32 s50, s50, 0x780
	s_add_u32 s50, s18, s50
	v_mfma_f32_16x16x32_bf16 v[74:77], v[120:123], v[116:119], v[74:77]
	v_cvt_pk_bf16_f32 v38, v38, v39
	v_cvt_pk_bf16_f32 v39, v40, v41
	v_cndmask_b32_e32 v111, 0, v168, vcc
	s_addc_u32 s51, s19, 0
	ds_write_b64 v98, v[38:39] offset:16384
	ds_read_b64_tr_b16 v[38:39], v105
	ds_read_b64_tr_b16 v[40:41], v105 offset:1024
	v_cvt_pk_bf16_f32 v26, v26, v27
	v_cvt_pk_bf16_f32 v27, v28, v29
	s_waitcnt lgkmcnt(3)
	v_mfma_f32_16x16x32_bf16 v[90:93], v[124:127], v[112:115], v[90:93]
	ds_write_b64 v99, v[26:27] offset:16640
	v_mfma_f32_16x16x32_bf16 v[26:29], v[124:127], v[116:119], v[46:49]
	s_nop 2
	ds_read_b64_tr_b16 v[46:47], v106
	ds_read_b64_tr_b16 v[48:49], v106 offset:1024
	s_waitcnt lgkmcnt(3)
	v_mfma_f32_16x16x32_bf16 v[70:73], v[38:41], v[112:115], v[70:73]
	v_cvt_pk_bf16_f32 v50, v50, v51
	v_cvt_pk_bf16_f32 v51, v52, v53
	ds_write_b64 v100, v[50:51] offset:16896
	v_mfma_f32_16x16x32_bf16 v[18:21], v[38:41], v[116:119], v[18:21]
	ds_read_b64_tr_b16 v[38:39], v107
	ds_read_b64_tr_b16 v[40:41], v107 offset:1024
	s_waitcnt lgkmcnt(3)
	v_mfma_f32_16x16x32_bf16 v[42:45], v[46:49], v[112:115], v[42:45]
	v_cvt_pk_bf16_f32 v22, v22, v23
	v_cvt_pk_bf16_f32 v23, v24, v25
	ds_write_b64 v101, v[22:23] offset:17152
	v_mfma_f32_16x16x32_bf16 v[6:9], v[46:49], v[116:119], v[6:9]
	ds_read_b64_tr_b16 v[46:47], v108
	ds_read_b64_tr_b16 v[48:49], v108 offset:1024
	s_waitcnt lgkmcnt(3)
	v_mfma_f32_16x16x32_bf16 v[22:25], v[38:41], v[112:115], v[86:89]
	v_mfma_f32_16x16x32_bf16 v[50:53], v[38:41], v[116:119], v[54:57]
	ds_read_b64_tr_b16 v[38:39], v109
	ds_read_b64_tr_b16 v[40:41], v109 offset:1024
	s_waitcnt lgkmcnt(2)
	v_mfma_f32_16x16x32_bf16 v[54:57], v[46:49], v[112:115], v[62:65]
	v_mfma_f32_16x16x32_bf16 v[34:37], v[46:49], v[116:119], v[34:37]
	ds_read_b64_tr_b16 v[46:47], v110
	ds_read_b64_tr_b16 v[48:49], v110 offset:1024
	s_waitcnt lgkmcnt(2)
	v_mfma_f32_16x16x32_bf16 v[30:33], v[38:41], v[112:115], v[30:33]
	v_mfma_f32_16x16x32_bf16 v[14:17], v[38:41], v[116:119], v[14:17]
	ds_read_b64_tr_b16 v[38:39], v171 offset:8192
	ds_read_b64_tr_b16 v[40:41], v171 offset:9216
	ds_read_b128 v[62:65], v102
	ds_read_b128 v[86:89], v102 offset:2048
	s_waitcnt lgkmcnt(4)
	v_mfma_f32_16x16x32_bf16 v[10:13], v[46:49], v[112:115], v[10:13]
	v_mfma_f32_16x16x32_bf16 v[2:5], v[46:49], v[116:119], v[2:5]
	s_waitcnt lgkmcnt(1)
	v_mfma_f32_16x16x32_bf16 v[46:49], v[38:41], v[62:65], v[94:97]
	s_nop 2
	ds_read_b64_tr_b16 v[94:95], v104 offset:8192
	ds_read_b64_tr_b16 v[96:97], v104 offset:9216
	s_waitcnt lgkmcnt(2)
	v_mfma_f32_16x16x32_bf16 v[74:77], v[38:41], v[86:89], v[74:77]
	s_mov_b32 s76, m0
	s_mov_b32 m0, s67
	s_nop 0
	global_load_lds_dwordx4 v169, s[50:51]
	s_mov_b32 m0, s76
	ds_read_b64_tr_b16 v[38:39], v105 offset:8192
	ds_read_b64_tr_b16 v[40:41], v105 offset:9216
	s_waitcnt lgkmcnt(2)
	v_mfma_f32_16x16x32_bf16 v[90:93], v[94:97], v[62:65], v[90:93]
	s_mov_b32 s76, m0
	s_mov_b32 m0, s68
	s_nop 0
	global_load_lds_dwordx4 v170, s[50:51]
	s_mov_b32 m0, s76
	v_mfma_f32_16x16x32_bf16 v[94:97], v[94:97], v[86:89], v[26:29]
	s_nop 2
	ds_read_b64_tr_b16 v[26:27], v106 offset:8192
	ds_read_b64_tr_b16 v[28:29], v106 offset:9216
	s_waitcnt lgkmcnt(2)
	v_mfma_f32_16x16x32_bf16 v[70:73], v[38:41], v[62:65], v[70:73]
	s_mov_b32 s76, m0
	s_mov_b32 m0, s69
	s_nop 0
	global_load_lds_dwordx4 v174, s[50:51]
	s_mov_b32 m0, s76
	v_mfma_f32_16x16x32_bf16 v[18:21], v[38:41], v[86:89], v[18:21]
	ds_read_b64_tr_b16 v[112:113], v107 offset:8192
	ds_read_b64_tr_b16 v[114:115], v107 offset:9216
	s_waitcnt lgkmcnt(2)
	v_mfma_f32_16x16x32_bf16 v[42:45], v[26:29], v[62:65], v[42:45]
	s_mov_b32 s76, m0
	s_mov_b32 m0, s70
	s_nop 0
	global_load_lds_dwordx4 v175, s[50:51]
	s_mov_b32 m0, s76
	v_mfma_f32_16x16x32_bf16 v[6:9], v[26:29], v[86:89], v[6:9]
	s_waitcnt lgkmcnt(0)
	v_mfma_f32_16x16x32_bf16 v[116:119], v[112:115], v[62:65], v[22:25]
	s_nop 2
	ds_read_b64_tr_b16 v[22:23], v108 offset:8192
	ds_read_b64_tr_b16 v[24:25], v108 offset:9216
	global_load_dwordx4 v[38:41], v111, s[6:7]
	v_mfma_f32_16x16x32_bf16 v[112:115], v[112:115], v[86:89], v[50:53]
	ds_read_b64_tr_b16 v[120:121], v109 offset:8192
	ds_read_b64_tr_b16 v[122:123], v109 offset:9216
	s_waitcnt lgkmcnt(2)
	v_mfma_f32_16x16x32_bf16 v[54:57], v[22:25], v[62:65], v[54:57]
	global_load_dwordx4 v[26:29], v111, s[6:7] offset:2048
	v_mfma_f32_16x16x32_bf16 v[34:37], v[22:25], v[86:89], v[34:37]
	ds_read_b64_tr_b16 v[124:125], v110 offset:8192
	ds_read_b64_tr_b16 v[126:127], v110 offset:9216
	s_waitcnt lgkmcnt(2)
	v_mfma_f32_16x16x32_bf16 v[30:33], v[120:123], v[62:65], v[30:33]
	s_add_u32 s6, s53, 0x61000
	s_addc_u32 s7, s75, 0
	global_load_dwordx4 v[50:53], v111, s[6:7]
	v_mfma_f32_16x16x32_bf16 v[14:17], v[120:123], v[86:89], v[14:17]
	s_waitcnt lgkmcnt(0)
	v_mfma_f32_16x16x32_bf16 v[10:13], v[124:127], v[62:65], v[10:13]
	global_load_dwordx4 v[22:25], v111, s[6:7] offset:2048
	v_mfma_f32_16x16x32_bf16 v[2:5], v[124:127], v[86:89], v[2:5]
	s_min_u32 s6, s52, 11
	s_add_i32 s75, s52, 2
	s_cmp_lt_u32 s52, 12
	s_cselect_b64 vcc, -1, 0
	s_lshl_b32 s6, s6, 17
	s_waitcnt lgkmcnt(0)
	s_barrier
	s_add_u32 s76, s22, s6
	s_waitcnt vmcnt(8)
	s_addc_u32 s77, s23, 0
	s_add_u32 s50, s76, 0x80000
	ds_read_b64_tr_b16 v[62:63], v171 offset:16384
	ds_read_b64_tr_b16 v[64:65], v171 offset:17408
	ds_read_b128 v[86:89], v172 offset:8192
	ds_read_b128 v[120:123], v172 offset:10240
	s_addc_u32 s51, s77, 0
	s_add_u32 s48, s48, 0x100
	s_addc_u32 s49, s49, 0
	s_cmp_lt_u32 s52, 14
	ds_read_b64_tr_b16 v[124:125], v104 offset:16384
	ds_read_b64_tr_b16 v[126:127], v104 offset:17408
	s_cselect_b64 s[6:7], -1, 0
	s_waitcnt lgkmcnt(3)
	v_mfma_f32_16x16x32_bf16 v[46:49], v[62:65], v[86:89], v[46:49]
	v_cndmask_b32_e32 v111, 0, v168, vcc
	s_and_b64 vcc, s[6:7], exec
	s_add_i32 s52, s48, 0x80
	s_min_u32 s52, s52, 0x780
	s_waitcnt lgkmcnt(2)
	v_mfma_f32_16x16x32_bf16 v[62:65], v[62:65], v[120:123], v[74:77]
	s_add_u32 s52, s18, s52
	s_addc_u32 s53, s19, 0
	s_nop 0
	v_cvt_pk_bf16_f32 v74, v78, v79
	v_cvt_pk_bf16_f32 v75, v80, v81
	ds_write_b64 v98, v[74:75]
	ds_read_b64_tr_b16 v[74:75], v105 offset:16384
	ds_read_b64_tr_b16 v[76:77], v105 offset:17408
	v_cvt_pk_bf16_f32 v66, v66, v67
	v_cvt_pk_bf16_f32 v67, v68, v69
	s_waitcnt lgkmcnt(3)
	v_mfma_f32_16x16x32_bf16 v[78:81], v[124:127], v[86:89], v[90:93]
	ds_write_b64 v99, v[66:67] offset:256
	v_mfma_f32_16x16x32_bf16 v[66:69], v[124:127], v[120:123], v[94:97]
	s_nop 0
	ds_read_b64_tr_b16 v[90:91], v106 offset:16384
	ds_read_b64_tr_b16 v[92:93], v106 offset:17408
	s_waitcnt lgkmcnt(3)
	v_mfma_f32_16x16x32_bf16 v[70:73], v[74:77], v[86:89], v[70:73]
	v_cvt_pk_bf16_f32 v82, v82, v83
	v_cvt_pk_bf16_f32 v83, v84, v85
	ds_write_b64 v100, v[82:83] offset:512
	v_mfma_f32_16x16x32_bf16 v[18:21], v[74:77], v[120:123], v[18:21]
	ds_read_b64_tr_b16 v[74:75], v107 offset:16384
	ds_read_b64_tr_b16 v[76:77], v107 offset:17408
	s_waitcnt lgkmcnt(3)
	v_mfma_f32_16x16x32_bf16 v[42:45], v[90:93], v[86:89], v[42:45]
	v_cvt_pk_bf16_f32 v58, v58, v59
	v_cvt_pk_bf16_f32 v59, v60, v61
	ds_write_b64 v101, v[58:59] offset:768
	v_mfma_f32_16x16x32_bf16 v[6:9], v[90:93], v[120:123], v[6:9]
	ds_read_b64_tr_b16 v[82:83], v108 offset:16384
	ds_read_b64_tr_b16 v[84:85], v108 offset:17408
	s_waitcnt lgkmcnt(3)
	v_mfma_f32_16x16x32_bf16 v[58:61], v[74:77], v[86:89], v[116:119]
	v_mfma_f32_16x16x32_bf16 v[112:115], v[74:77], v[120:123], v[112:115]
	s_waitcnt lgkmcnt(0)
	v_mfma_f32_16x16x32_bf16 v[116:119], v[82:85], v[86:89], v[54:57]
	s_nop 2
	ds_read_b64_tr_b16 v[54:55], v109 offset:16384
	ds_read_b64_tr_b16 v[56:57], v109 offset:17408
	v_mfma_f32_16x16x32_bf16 v[34:37], v[82:85], v[120:123], v[34:37]
	ds_read_b64_tr_b16 v[74:75], v110 offset:16384
	ds_read_b64_tr_b16 v[76:77], v110 offset:17408
	s_waitcnt lgkmcnt(2)
	v_mfma_f32_16x16x32_bf16 v[30:33], v[54:57], v[86:89], v[30:33]
	v_mfma_f32_16x16x32_bf16 v[14:17], v[54:57], v[120:123], v[14:17]
	ds_read_b64_tr_b16 v[54:55], v171 offset:24576
	ds_read_b64_tr_b16 v[56:57], v171 offset:25600
	ds_read_b128 v[124:127], v103
	ds_read_b128 v[136:139], v103 offset:2048
	s_waitcnt lgkmcnt(4)
	v_mfma_f32_16x16x32_bf16 v[10:13], v[74:77], v[86:89], v[10:13]
	v_mfma_f32_16x16x32_bf16 v[2:5], v[74:77], v[120:123], v[2:5]
	s_waitcnt lgkmcnt(1)
	v_mfma_f32_16x16x32_bf16 v[94:97], v[54:57], v[124:127], v[46:49]
	s_nop 2
	ds_read_b64_tr_b16 v[46:47], v104 offset:24576
	ds_read_b64_tr_b16 v[48:49], v104 offset:25600
	s_waitcnt lgkmcnt(2)
	v_mfma_f32_16x16x32_bf16 v[74:77], v[54:57], v[136:139], v[62:65]
	s_mov_b32 s78, m0
	s_mov_b32 m0, s71
	s_nop 0
	global_load_lds_dwordx4 v169, s[52:53]
	s_mov_b32 m0, s78
	ds_read_b64_tr_b16 v[54:55], v105 offset:24576
	ds_read_b64_tr_b16 v[56:57], v105 offset:25600
	s_waitcnt lgkmcnt(2)
	v_mfma_f32_16x16x32_bf16 v[90:93], v[46:49], v[124:127], v[78:81]
	s_mov_b32 s78, m0
	s_mov_b32 m0, s72
	s_nop 0
	global_load_lds_dwordx4 v170, s[52:53]
	s_mov_b32 m0, s78
	v_mfma_f32_16x16x32_bf16 v[46:49], v[46:49], v[136:139], v[66:69]
	ds_read_b64_tr_b16 v[62:63], v106 offset:24576
	ds_read_b64_tr_b16 v[64:65], v106 offset:25600
	s_waitcnt lgkmcnt(2)
	v_mfma_f32_16x16x32_bf16 v[70:73], v[54:57], v[124:127], v[70:73]
	s_mov_b32 s78, m0
	s_mov_b32 m0, s73
	s_nop 0
	global_load_lds_dwordx4 v174, s[52:53]
	s_mov_b32 m0, s78
	v_mfma_f32_16x16x32_bf16 v[18:21], v[54:57], v[136:139], v[18:21]
	ds_read_b64_tr_b16 v[54:55], v107 offset:24576
	ds_read_b64_tr_b16 v[56:57], v107 offset:25600
	s_waitcnt lgkmcnt(2)
	v_mfma_f32_16x16x32_bf16 v[42:45], v[62:65], v[124:127], v[42:45]
	s_mov_b32 s78, m0
	s_mov_b32 m0, s74
	s_nop 0
	global_load_lds_dwordx4 v175, s[52:53]
	s_mov_b32 m0, s78
	v_mfma_f32_16x16x32_bf16 v[6:9], v[62:65], v[136:139], v[6:9]
	s_waitcnt lgkmcnt(0)
	v_mfma_f32_16x16x32_bf16 v[86:89], v[54:57], v[124:127], v[58:61]
	s_nop 2
	ds_read_b64_tr_b16 v[58:59], v108 offset:24576
	ds_read_b64_tr_b16 v[60:61], v108 offset:25600
	s_cbranch_vccz .Lmy_tl_272_0
	global_load_dwordx4 v[78:81], v111, s[50:51]

.LBB0_277:
	v_mov_b32_e32 v125, 0
	v_lshlrev_b32_e32 v98, 5, v134
	v_add_u32_e32 v99, 0x2000, v172
	s_andn2_b64 vcc, exec, s[10:11]
	v_xor_b32_e32 v178, 64, v172
	v_xor_b32_e32 v179, 32, v171
	v_xor_b32_e32 v180, 64, v171
	v_xor_b32_e32 v181, 0x60, v171
	v_xor_b32_e32 v182, 0x80, v171
	v_xor_b32_e32 v183, 0xa0, v171
	v_xor_b32_e32 v184, 0xc0, v171
	v_xor_b32_e32 v185, 0xe0, v171
	v_add_u32_e32 v186, v173, v98
	v_xor_b32_e32 v190, 32, v98
	v_xor_b32_e32 v189, 64, v98
	v_xor_b32_e32 v188, 0x60, v98
	v_xor_b32_e32 v187, 64, v99
	v_mov_b32_e32 v124, v125
	v_mov_b32_e32 v123, v125
	v_mov_b32_e32 v122, v125
	v_mov_b32_e32 v117, v125
	v_mov_b32_e32 v116, v125
	v_mov_b32_e32 v115, v125
	v_mov_b32_e32 v114, v125
	v_mov_b32_e32 v109, v125
	v_mov_b32_e32 v108, v125
	v_mov_b32_e32 v107, v125
	v_mov_b32_e32 v106, v125
	v_mov_b32_e32 v105, v125
	v_mov_b32_e32 v104, v125
	v_mov_b32_e32 v103, v125
	v_mov_b32_e32 v102, v125
	v_mov_b32_e32 v129, v125
	v_mov_b32_e32 v128, v125
	v_mov_b32_e32 v127, v125
	v_mov_b32_e32 v126, v125
	v_mov_b32_e32 v121, v125
	v_mov_b32_e32 v120, v125
	v_mov_b32_e32 v119, v125
	v_mov_b32_e32 v118, v125
	v_mov_b32_e32 v113, v125
	v_mov_b32_e32 v112, v125
	v_mov_b32_e32 v111, v125
	v_mov_b32_e32 v110, v125
	v_mov_b32_e32 v101, v125
	v_mov_b32_e32 v100, v125
	v_mov_b32_e32 v99, v125
	v_mov_b32_e32 v98, v125
	s_cbranch_vccnz .LBB0_281
	s_waitcnt vmcnt(9)
	v_lshlrev_b32_e32 v2, 8, v131
	v_and_or_b32 v191, v2, s60, v133
	s_waitcnt vmcnt(8)
	v_lshlrev_b32_e32 v2, 8, v130
	v_and_or_b32 v192, v2, s60, v132
	s_mov_b32 s6, m0
	s_mov_b32 m0, s67
	s_nop 0
	global_load_lds_dwordx4 v169, s[18:19]
	s_mov_b32 m0, s6
	s_add_i32 s50, s67, 0x800
	s_mov_b32 s6, m0
	s_mov_b32 m0, s68
	s_nop 0
	global_load_lds_dwordx4 v170, s[18:19]
	s_mov_b32 m0, s6
	s_add_i32 s51, s67, 0xc00
	s_mov_b32 s6, m0
	s_mov_b32 m0, s50
	s_nop 0
	global_load_lds_dwordx4 v174, s[18:19]
	s_mov_b32 m0, s6
	s_add_i32 s52, s67, 0x1000
	s_mov_b32 s6, m0
	s_mov_b32 m0, s51
	s_nop 0
	global_load_lds_dwordx4 v175, s[18:19]
	s_mov_b32 m0, s6
	s_add_i32 s53, s67, 0x1400
	s_mov_b32 s6, m0
	s_mov_b32 m0, s52
	s_nop 0
	global_load_lds_dwordx4 v176, s[18:19]
	s_mov_b32 m0, s6
	s_add_i32 s69, s67, 0x1800
	s_mov_b32 s6, m0
	s_mov_b32 m0, s53
	s_nop 0
	global_load_lds_dwordx4 v177, s[18:19]
	s_mov_b32 m0, s6
	s_add_i32 s70, s67, 0x1c00
	s_mov_b32 s6, m0
	s_mov_b32 m0, s69
	s_nop 0
	global_load_lds_dwordx4 v191, s[18:19]
	s_mov_b32 m0, s6
	v_add_u32_e32 v193, v173, v190
	s_mov_b32 s6, m0
	s_mov_b32 m0, s70
	s_nop 0
	global_load_lds_dwordx4 v192, s[18:19]
	s_mov_b32 m0, s6
	s_waitcnt vmcnt(8)
	v_mov_b32_e32 v138, v60
	v_mov_b32_e32 v139, v61
	v_mov_b32_e32 v140, v62
	v_mov_b32_e32 v141, v63
	v_mov_b32_e32 v134, v64
	v_mov_b32_e32 v135, v65
	v_mov_b32_e32 v136, v66
	v_mov_b32_e32 v137, v67
	v_mov_b32_e32 v142, v68
	v_mov_b32_e32 v143, v69
	v_mov_b32_e32 v144, v70
	v_mov_b32_e32 v145, v71
	v_mov_b32_e32 v130, v72
	v_mov_b32_e32 v131, v73
	v_mov_b32_e32 v132, v74
	v_mov_b32_e32 v133, v75
	v_add_u32_e32 v194, v173, v189
	v_cvt_pk_bf16_f32 v2, v228, v229
	v_cvt_pk_bf16_f32 v3, v230, v231
	ds_write_b64 v186, v[2:3]
	v_cvt_pk_bf16_f32 v2, v232, v233
	v_cvt_pk_bf16_f32 v3, v234, v235
	ds_write_b64 v193, v[2:3] offset:256
	v_cvt_pk_bf16_f32 v2, v236, v237
	v_cvt_pk_bf16_f32 v3, v238, v239
	ds_write_b64 v194, v[2:3] offset:512
	v_cvt_pk_bf16_f32 v2, v240, v241
	v_cvt_pk_bf16_f32 v3, v242, v243
	v_add_u32_e32 v195, v173, v188
	ds_write_b64 v195, v[2:3] offset:768
	global_load_dwordx4 v[154:157], v168, s[38:39]
	global_load_dwordx4 v[150:153], v168, s[38:39] offset:2048
	global_load_dwordx4 v[158:161], v168, s[40:41]
	global_load_dwordx4 v[146:149], v168, s[40:41] offset:2048
	s_waitcnt lgkmcnt(0)
	s_barrier
	v_mov_b32_e32 v98, 0
	s_add_i32 s71, s67, 0x2000
	s_add_i32 s72, s67, 0x2400
	s_add_i32 s73, s67, 0x2800
	s_add_i32 s74, s67, 0x2c00
	s_add_i32 s75, s67, 0x3000
	s_add_i32 s76, s67, 0x3400
	s_add_i32 s77, s67, 0x3800
	s_add_i32 s78, s67, 0x3c00
	s_mov_b32 s48, 0
	s_mov_b64 s[8:9], 0
	v_mov_b32_e32 v99, v98
	v_mov_b32_e32 v100, v98
	v_mov_b32_e32 v101, v98
	v_mov_b32_e32 v26, v98
	v_mov_b32_e32 v27, v98
	v_mov_b32_e32 v28, v98
	v_mov_b32_e32 v29, v98
	v_mov_b32_e32 v2, v98
	v_mov_b32_e32 v3, v98
	v_mov_b32_e32 v4, v98
	v_mov_b32_e32 v5, v98
	v_mov_b32_e32 v10, v98
	v_mov_b32_e32 v11, v98
	v_mov_b32_e32 v12, v98
	v_mov_b32_e32 v13, v98
	v_mov_b32_e32 v110, v98
	v_mov_b32_e32 v111, v98
	v_mov_b32_e32 v112, v98
	v_mov_b32_e32 v113, v98
	v_mov_b32_e32 v50, v98
	v_mov_b32_e32 v51, v98
	v_mov_b32_e32 v52, v98
	v_mov_b32_e32 v53, v98
	v_mov_b32_e32 v14, v98
	v_mov_b32_e32 v15, v98
	v_mov_b32_e32 v16, v98
	v_mov_b32_e32 v17, v98
	v_mov_b32_e32 v30, v98
	v_mov_b32_e32 v31, v98
	v_mov_b32_e32 v32, v98
	v_mov_b32_e32 v33, v98
	v_mov_b32_e32 v118, v98
	v_mov_b32_e32 v119, v98
	v_mov_b32_e32 v120, v98
	v_mov_b32_e32 v121, v98
	v_mov_b32_e32 v66, v98
	v_mov_b32_e32 v67, v98
	v_mov_b32_e32 v68, v98
	v_mov_b32_e32 v69, v98
	v_mov_b32_e32 v34, v98
	v_mov_b32_e32 v35, v98
	v_mov_b32_e32 v36, v98
	v_mov_b32_e32 v37, v98
	v_mov_b32_e32 v62, v98
	v_mov_b32_e32 v63, v98
	v_mov_b32_e32 v64, v98
	v_mov_b32_e32 v65, v98
	v_mov_b32_e32 v126, v98
	v_mov_b32_e32 v127, v98
	v_mov_b32_e32 v128, v98
	v_mov_b32_e32 v129, v98
	v_mov_b32_e32 v82, v98
	v_mov_b32_e32 v83, v98
	v_mov_b32_e32 v84, v98
	v_mov_b32_e32 v85, v98
	v_mov_b32_e32 v54, v98
	v_mov_b32_e32 v55, v98
	v_mov_b32_e32 v56, v98
	v_mov_b32_e32 v57, v98
	v_mov_b32_e32 v86, v98
	v_mov_b32_e32 v87, v98
	v_mov_b32_e32 v88, v98
	v_mov_b32_e32 v89, v98
	v_mov_b32_e32 v102, v98
	v_mov_b32_e32 v103, v98
	v_mov_b32_e32 v104, v98
	v_mov_b32_e32 v105, v98
	v_mov_b32_e32 v22, v98
	v_mov_b32_e32 v23, v98
	v_mov_b32_e32 v24, v98
	v_mov_b32_e32 v25, v98
	v_mov_b32_e32 v6, v98
	v_mov_b32_e32 v7, v98
	v_mov_b32_e32 v8, v98
	v_mov_b32_e32 v9, v98
	v_mov_b32_e32 v42, v98
	v_mov_b32_e32 v43, v98
	v_mov_b32_e32 v44, v98
	v_mov_b32_e32 v45, v98
	v_mov_b32_e32 v106, v98
	v_mov_b32_e32 v107, v98
	v_mov_b32_e32 v108, v98
	v_mov_b32_e32 v109, v98
	v_mov_b32_e32 v38, v98
	v_mov_b32_e32 v39, v98
	v_mov_b32_e32 v40, v98
	v_mov_b32_e32 v41, v98
	v_mov_b32_e32 v18, v98
	v_mov_b32_e32 v19, v98
	v_mov_b32_e32 v20, v98
	v_mov_b32_e32 v21, v98
	v_mov_b32_e32 v70, v98
	v_mov_b32_e32 v71, v98
	v_mov_b32_e32 v72, v98
	v_mov_b32_e32 v73, v98
	v_mov_b32_e32 v114, v98
	v_mov_b32_e32 v115, v98
	v_mov_b32_e32 v116, v98
	v_mov_b32_e32 v117, v98
	v_mov_b32_e32 v58, v98
	v_mov_b32_e32 v59, v98
	v_mov_b32_e32 v60, v98
	v_mov_b32_e32 v61, v98
	v_mov_b32_e32 v46, v98
	v_mov_b32_e32 v47, v98
	v_mov_b32_e32 v48, v98
	v_mov_b32_e32 v49, v98
	v_mov_b32_e32 v90, v98
	v_mov_b32_e32 v91, v98
	v_mov_b32_e32 v92, v98
	v_mov_b32_e32 v93, v98
	v_mov_b32_e32 v122, v98
	v_mov_b32_e32 v123, v98
	v_mov_b32_e32 v124, v98
	v_mov_b32_e32 v125, v98
	v_mov_b32_e32 v78, v98
	v_mov_b32_e32 v79, v98
	v_mov_b32_e32 v80, v98
	v_mov_b32_e32 v81, v98
	v_mov_b32_e32 v74, v98
	v_mov_b32_e32 v75, v98
	v_mov_b32_e32 v76, v98
	v_mov_b32_e32 v77, v98
	v_mov_b32_e32 v94, v98
	v_mov_b32_e32 v95, v98
	v_mov_b32_e32 v96, v98
	v_mov_b32_e32 v97, v98
	s_add_u32 s10, s18, 0x80
	s_addc_u32 s11, s19, 0
	s_mov_b32 s80, m0
	s_mov_b32 m0, s71
	s_nop 0
	global_load_lds_dwordx4 v169, s[10:11]
	s_mov_b32 m0, s80
	s_mov_b32 s80, m0
	s_mov_b32 m0, s72
	s_nop 0
	global_load_lds_dwordx4 v170, s[10:11]
	s_mov_b32 m0, s80
	s_mov_b32 s80, m0
	s_mov_b32 m0, s73
	s_nop 0
	global_load_lds_dwordx4 v174, s[10:11]
	s_mov_b32 m0, s80
	s_mov_b32 s80, m0
	s_mov_b32 m0, s74
	s_nop 0
	global_load_lds_dwordx4 v175, s[10:11]
	s_mov_b32 m0, s80
	s_mov_b32 s80, m0
	s_mov_b32 m0, s75
	s_nop 0
	global_load_lds_dwordx4 v176, s[10:11]
	s_mov_b32 m0, s80
	s_mov_b32 s80, m0
	s_mov_b32 m0, s76
	s_nop 0
	global_load_lds_dwordx4 v177, s[10:11]
	s_mov_b32 m0, s80
	s_mov_b32 s80, m0
	s_mov_b32 m0, s77
	s_nop 0
	global_load_lds_dwordx4 v191, s[10:11]
	s_mov_b32 m0, s80
	s_mov_b32 s80, m0
	s_mov_b32 m0, s78
	s_nop 0
	global_load_lds_dwordx4 v192, s[10:11]
	s_mov_b32 m0, s80
.LBB0_279:
	s_waitcnt vmcnt(12)
	s_min_u32 s6, s48, 12
	ds_read_b64_tr_b16 v[196:197], v171
	ds_read_b64_tr_b16 v[198:199], v171 offset:1024
	ds_read_b128 v[200:203], v172
	ds_read_b128 v[204:207], v172 offset:2048
	ds_read_b128 v[208:211], v172 offset:4096
	ds_read_b128 v[214:217], v172 offset:6144
	s_cmp_lt_u32 s48, 13
	s_cselect_b64 vcc, -1, 0
	s_lshl_b32 s6, s6, 17
	s_add_u32 s49, s22, s6
	s_addc_u32 s79, s23, 0
	s_add_u32 s6, s49, 0x60000
	ds_read_b64_tr_b16 v[224:225], v179
	ds_read_b64_tr_b16 v[226:227], v179 offset:1024
	s_waitcnt lgkmcnt(5)
	v_mfma_f32_16x16x32_bf16 v[94:97], v[196:199], v[200:203], v[94:97]
	s_addc_u32 s7, s79, 0
	s_add_u32 s10, s8, 0x100
	s_min_u32 s10, s10, 0x780
	s_waitcnt lgkmcnt(4)
	v_mfma_f32_16x16x32_bf16 v[74:77], v[196:199], v[204:207], v[74:77]
	s_add_u32 s10, s18, s10
	v_cvt_pk_bf16_f32 v138, v138, v139
	v_cvt_pk_bf16_f32 v139, v140, v141
	s_waitcnt lgkmcnt(3)
	v_mfma_f32_16x16x32_bf16 v[78:81], v[196:199], v[208:211], v[78:81]
	v_cndmask_b32_e32 v212, 0, v168, vcc
	s_addc_u32 s11, s19, 0
	ds_write_b64 v186, v[138:139] offset:16384
	s_waitcnt lgkmcnt(3)
	v_mfma_f32_16x16x32_bf16 v[122:125], v[196:199], v[214:217], v[122:125]
	ds_read_b64_tr_b16 v[138:139], v180
	ds_read_b64_tr_b16 v[140:141], v180 offset:1024
	s_waitcnt lgkmcnt(3)
	v_mfma_f32_16x16x32_bf16 v[90:93], v[224:227], v[200:203], v[90:93]
	v_cvt_pk_bf16_f32 v134, v134, v135
	v_cvt_pk_bf16_f32 v135, v136, v137
	ds_write_b64 v193, v[134:135] offset:16640
	v_mfma_f32_16x16x32_bf16 v[46:49], v[224:227], v[204:207], v[46:49]
	v_mfma_f32_16x16x32_bf16 v[58:61], v[224:227], v[208:211], v[58:61]
	v_mfma_f32_16x16x32_bf16 v[114:117], v[224:227], v[214:217], v[114:117]
	ds_read_b64_tr_b16 v[134:135], v181
	ds_read_b64_tr_b16 v[136:137], v181 offset:1024
	s_waitcnt lgkmcnt(3)
	v_mfma_f32_16x16x32_bf16 v[70:73], v[138:141], v[200:203], v[70:73]
	v_cvt_pk_bf16_f32 v142, v142, v143
	v_cvt_pk_bf16_f32 v143, v144, v145
	ds_write_b64 v194, v[142:143] offset:16896
	v_mfma_f32_16x16x32_bf16 v[18:21], v[138:141], v[204:207], v[18:21]
	v_mfma_f32_16x16x32_bf16 v[38:41], v[138:141], v[208:211], v[38:41]
	v_mfma_f32_16x16x32_bf16 v[106:109], v[138:141], v[214:217], v[106:109]
	ds_read_b64_tr_b16 v[138:139], v182
	ds_read_b64_tr_b16 v[140:141], v182 offset:1024
	s_waitcnt lgkmcnt(3)
	v_mfma_f32_16x16x32_bf16 v[42:45], v[134:137], v[200:203], v[42:45]
	v_cvt_pk_bf16_f32 v130, v130, v131
	v_cvt_pk_bf16_f32 v131, v132, v133
	ds_write_b64 v195, v[130:131] offset:17152
	v_mfma_f32_16x16x32_bf16 v[6:9], v[134:137], v[204:207], v[6:9]
	v_mfma_f32_16x16x32_bf16 v[22:25], v[134:137], v[208:211], v[22:25]
	v_mfma_f32_16x16x32_bf16 v[102:105], v[134:137], v[214:217], v[102:105]
	ds_read_b64_tr_b16 v[130:131], v183
	ds_read_b64_tr_b16 v[132:133], v183 offset:1024
	s_waitcnt lgkmcnt(3)
	v_mfma_f32_16x16x32_bf16 v[86:89], v[138:141], v[200:203], v[86:89]
	v_mfma_f32_16x16x32_bf16 v[54:57], v[138:141], v[204:207], v[54:57]
	v_mfma_f32_16x16x32_bf16 v[82:85], v[138:141], v[208:211], v[82:85]
	v_mfma_f32_16x16x32_bf16 v[126:129], v[138:141], v[214:217], v[126:129]
	ds_read_b64_tr_b16 v[134:135], v184
	ds_read_b64_tr_b16 v[136:137], v184 offset:1024
	s_waitcnt lgkmcnt(2)
	v_mfma_f32_16x16x32_bf16 v[62:65], v[130:133], v[200:203], v[62:65]
	v_mfma_f32_16x16x32_bf16 v[34:37], v[130:133], v[204:207], v[34:37]
	v_mfma_f32_16x16x32_bf16 v[66:69], v[130:133], v[208:211], v[66:69]
	v_mfma_f32_16x16x32_bf16 v[118:121], v[130:133], v[214:217], v[118:121]
	ds_read_b64_tr_b16 v[130:131], v185
	ds_read_b64_tr_b16 v[132:133], v185 offset:1024
	s_waitcnt lgkmcnt(2)
	v_mfma_f32_16x16x32_bf16 v[30:33], v[134:137], v[200:203], v[30:33]
	v_mfma_f32_16x16x32_bf16 v[14:17], v[134:137], v[204:207], v[14:17]
	v_mfma_f32_16x16x32_bf16 v[50:53], v[134:137], v[208:211], v[50:53]
	v_mfma_f32_16x16x32_bf16 v[110:113], v[134:137], v[214:217], v[110:113]
	s_waitcnt lgkmcnt(0)
	v_mfma_f32_16x16x32_bf16 v[10:13], v[130:133], v[200:203], v[10:13]
	ds_read_b64_tr_b16 v[134:135], v171 offset:8192
	ds_read_b64_tr_b16 v[136:137], v171 offset:9216
	v_mfma_f32_16x16x32_bf16 v[2:5], v[130:133], v[204:207], v[2:5]
	v_mfma_f32_16x16x32_bf16 v[26:29], v[130:133], v[208:211], v[26:29]
	ds_read_b128 v[196:199], v178
	ds_read_b128 v[200:203], v178 offset:2048
	ds_read_b128 v[204:207], v178 offset:4096
	ds_read_b128 v[208:211], v178 offset:6144
	v_mfma_f32_16x16x32_bf16 v[98:101], v[130:133], v[214:217], v[98:101]
	ds_read_b64_tr_b16 v[130:131], v179 offset:8192
	ds_read_b64_tr_b16 v[132:133], v179 offset:9216
	s_waitcnt lgkmcnt(5)
	v_mfma_f32_16x16x32_bf16 v[94:97], v[134:137], v[196:199], v[94:97]
	s_waitcnt lgkmcnt(4)
	v_mfma_f32_16x16x32_bf16 v[74:77], v[134:137], v[200:203], v[74:77]
	s_waitcnt lgkmcnt(3)
	v_mfma_f32_16x16x32_bf16 v[78:81], v[134:137], v[204:207], v[78:81]
	s_waitcnt lgkmcnt(2)
	v_mfma_f32_16x16x32_bf16 v[122:125], v[134:137], v[208:211], v[122:125]
	s_mov_b32 s80, m0
	s_mov_b32 m0, s67
	s_nop 0
	global_load_lds_dwordx4 v169, s[10:11]
	s_mov_b32 m0, s80
	ds_read_b64_tr_b16 v[134:135], v180 offset:8192
	ds_read_b64_tr_b16 v[136:137], v180 offset:9216
	s_waitcnt lgkmcnt(2)
	v_mfma_f32_16x16x32_bf16 v[90:93], v[130:133], v[196:199], v[90:93]
	s_mov_b32 s80, m0
	s_mov_b32 m0, s68
	s_nop 0
	global_load_lds_dwordx4 v170, s[10:11]
	s_mov_b32 m0, s80
	v_mfma_f32_16x16x32_bf16 v[46:49], v[130:133], v[200:203], v[46:49]
	v_mfma_f32_16x16x32_bf16 v[58:61], v[130:133], v[204:207], v[58:61]
	v_mfma_f32_16x16x32_bf16 v[114:117], v[130:133], v[208:211], v[114:117]
	ds_read_b64_tr_b16 v[130:131], v181 offset:8192
	ds_read_b64_tr_b16 v[132:133], v181 offset:9216
	s_waitcnt lgkmcnt(2)
	v_mfma_f32_16x16x32_bf16 v[70:73], v[134:137], v[196:199], v[70:73]
	s_mov_b32 s80, m0
	s_mov_b32 m0, s50
	s_nop 0
	global_load_lds_dwordx4 v174, s[10:11]
	s_mov_b32 m0, s80
	v_mfma_f32_16x16x32_bf16 v[18:21], v[134:137], v[200:203], v[18:21]
	v_mfma_f32_16x16x32_bf16 v[38:41], v[134:137], v[204:207], v[38:41]
	v_mfma_f32_16x16x32_bf16 v[106:109], v[134:137], v[208:211], v[106:109]
	ds_read_b64_tr_b16 v[134:135], v182 offset:8192
	ds_read_b64_tr_b16 v[136:137], v182 offset:9216
	s_waitcnt lgkmcnt(2)
	v_mfma_f32_16x16x32_bf16 v[42:45], v[130:133], v[196:199], v[42:45]
	s_mov_b32 s80, m0
	s_mov_b32 m0, s51
	s_nop 0
	global_load_lds_dwordx4 v175, s[10:11]
	s_mov_b32 m0, s80
	v_mfma_f32_16x16x32_bf16 v[6:9], v[130:133], v[200:203], v[6:9]
	v_mfma_f32_16x16x32_bf16 v[22:25], v[130:133], v[204:207], v[22:25]
	v_mfma_f32_16x16x32_bf16 v[102:105], v[130:133], v[208:211], v[102:105]
	ds_read_b64_tr_b16 v[130:131], v183 offset:8192
	ds_read_b64_tr_b16 v[132:133], v183 offset:9216
	s_waitcnt lgkmcnt(2)
	v_mfma_f32_16x16x32_bf16 v[86:89], v[134:137], v[196:199], v[86:89]
	s_mov_b32 s80, m0
	s_mov_b32 m0, s52
	s_nop 0
	global_load_lds_dwordx4 v176, s[10:11]
	s_mov_b32 m0, s80
	global_load_dwordx4 v[138:141], v212, s[6:7]
	v_mfma_f32_16x16x32_bf16 v[54:57], v[134:137], v[200:203], v[54:57]
	v_mfma_f32_16x16x32_bf16 v[82:85], v[134:137], v[204:207], v[82:85]
	v_mfma_f32_16x16x32_bf16 v[126:129], v[134:137], v[208:211], v[126:129]
	ds_read_b64_tr_b16 v[214:215], v184 offset:8192
	ds_read_b64_tr_b16 v[216:217], v184 offset:9216
	s_waitcnt lgkmcnt(2)
	v_mfma_f32_16x16x32_bf16 v[62:65], v[130:133], v[196:199], v[62:65]
	s_mov_b32 s80, m0
	s_mov_b32 m0, s53
	s_nop 0
	global_load_lds_dwordx4 v177, s[10:11]
	s_mov_b32 m0, s80
	global_load_dwordx4 v[134:137], v212, s[6:7] offset:2048
	v_mfma_f32_16x16x32_bf16 v[34:37], v[130:133], v[200:203], v[34:37]
	v_mfma_f32_16x16x32_bf16 v[66:69], v[130:133], v[204:207], v[66:69]
	v_mfma_f32_16x16x32_bf16 v[118:121], v[130:133], v[208:211], v[118:121]
	ds_read_b64_tr_b16 v[224:225], v185 offset:8192
	ds_read_b64_tr_b16 v[226:227], v185 offset:9216
	s_waitcnt lgkmcnt(2)
	v_mfma_f32_16x16x32_bf16 v[30:33], v[214:217], v[196:199], v[30:33]
	s_mov_b32 s80, m0
	s_mov_b32 m0, s69
	s_nop 0
	global_load_lds_dwordx4 v191, s[10:11]
	s_mov_b32 m0, s80
	s_add_u32 s6, s49, 0x61000
	s_addc_u32 s7, s79, 0
	global_load_dwordx4 v[142:145], v212, s[6:7]
	v_mfma_f32_16x16x32_bf16 v[14:17], v[214:217], v[200:203], v[14:17]
	v_mfma_f32_16x16x32_bf16 v[50:53], v[214:217], v[204:207], v[50:53]
	v_mfma_f32_16x16x32_bf16 v[110:113], v[214:217], v[208:211], v[110:113]
	s_waitcnt lgkmcnt(0)
	v_mfma_f32_16x16x32_bf16 v[10:13], v[224:227], v[196:199], v[10:13]
	s_mov_b32 s80, m0
	s_mov_b32 m0, s70
	s_nop 0
	global_load_lds_dwordx4 v192, s[10:11]
	s_mov_b32 m0, s80
	global_load_dwordx4 v[130:133], v212, s[6:7] offset:2048
	v_mfma_f32_16x16x32_bf16 v[2:5], v[224:227], v[200:203], v[2:5]
	v_mfma_f32_16x16x32_bf16 v[26:29], v[224:227], v[204:207], v[26:29]
	v_mfma_f32_16x16x32_bf16 v[98:101], v[224:227], v[208:211], v[98:101]
	s_min_u32 s6, s48, 11
	s_add_i32 s79, s48, 2
	s_cmp_lt_u32 s48, 12
	s_cselect_b64 vcc, -1, 0
	s_lshl_b32 s6, s6, 17
	s_waitcnt lgkmcnt(0)
	s_barrier
	s_add_u32 s80, s22, s6
	s_waitcnt vmcnt(12)
	s_addc_u32 s81, s23, 0
	ds_read_b64_tr_b16 v[196:197], v171 offset:16384
	ds_read_b64_tr_b16 v[198:199], v171 offset:17408
	s_add_u32 s10, s80, 0x80000
	ds_read_b128 v[200:203], v172 offset:8192
	ds_read_b128 v[204:207], v172 offset:10240
	ds_read_b128 v[208:211], v172 offset:12288
	ds_read_b128 v[214:217], v172 offset:14336
	s_addc_u32 s11, s81, 0
	s_add_u32 s8, s8, 0x100
	s_addc_u32 s9, s9, 0
	s_cmp_lt_u32 s48, 14
	ds_read_b64_tr_b16 v[224:225], v179 offset:16384
	ds_read_b64_tr_b16 v[226:227], v179 offset:17408
	s_cselect_b64 s[6:7], -1, 0
	s_waitcnt lgkmcnt(5)
	v_mfma_f32_16x16x32_bf16 v[94:97], v[196:199], v[200:203], v[94:97]
	v_cndmask_b32_e32 v212, 0, v168, vcc
	s_and_b64 vcc, s[6:7], exec
	s_add_i32 s48, s8, 0x80
	s_min_u32 s48, s48, 0x780
	s_waitcnt lgkmcnt(4)
	v_mfma_f32_16x16x32_bf16 v[74:77], v[196:199], v[204:207], v[74:77]
	s_add_u32 s48, s18, s48
	v_cvt_pk_bf16_f32 v154, v154, v155
	v_cvt_pk_bf16_f32 v155, v156, v157
	s_waitcnt lgkmcnt(3)
	v_mfma_f32_16x16x32_bf16 v[78:81], v[196:199], v[208:211], v[78:81]
	s_addc_u32 s49, s19, 0
	ds_write_b64 v186, v[154:155]
	s_waitcnt lgkmcnt(3)
	v_mfma_f32_16x16x32_bf16 v[122:125], v[196:199], v[214:217], v[122:125]
	ds_read_b64_tr_b16 v[154:155], v180 offset:16384
	ds_read_b64_tr_b16 v[156:157], v180 offset:17408
	s_waitcnt lgkmcnt(3)
	v_mfma_f32_16x16x32_bf16 v[90:93], v[224:227], v[200:203], v[90:93]
	v_cvt_pk_bf16_f32 v150, v150, v151
	v_cvt_pk_bf16_f32 v151, v152, v153
	ds_write_b64 v193, v[150:151] offset:256
	v_mfma_f32_16x16x32_bf16 v[46:49], v[224:227], v[204:207], v[46:49]
	v_mfma_f32_16x16x32_bf16 v[58:61], v[224:227], v[208:211], v[58:61]
	v_mfma_f32_16x16x32_bf16 v[114:117], v[224:227], v[214:217], v[114:117]
	ds_read_b64_tr_b16 v[150:151], v181 offset:16384
	ds_read_b64_tr_b16 v[152:153], v181 offset:17408
	s_waitcnt lgkmcnt(3)
	v_mfma_f32_16x16x32_bf16 v[70:73], v[154:157], v[200:203], v[70:73]
	v_cvt_pk_bf16_f32 v158, v158, v159
	v_cvt_pk_bf16_f32 v159, v160, v161
	ds_write_b64 v194, v[158:159] offset:512
	v_mfma_f32_16x16x32_bf16 v[18:21], v[154:157], v[204:207], v[18:21]
	v_mfma_f32_16x16x32_bf16 v[38:41], v[154:157], v[208:211], v[38:41]
	v_mfma_f32_16x16x32_bf16 v[106:109], v[154:157], v[214:217], v[106:109]
	ds_read_b64_tr_b16 v[154:155], v182 offset:16384
	ds_read_b64_tr_b16 v[156:157], v182 offset:17408
	s_waitcnt lgkmcnt(3)
	v_mfma_f32_16x16x32_bf16 v[42:45], v[150:153], v[200:203], v[42:45]
	v_cvt_pk_bf16_f32 v146, v146, v147
	v_cvt_pk_bf16_f32 v147, v148, v149
	ds_write_b64 v195, v[146:147] offset:768
	v_mfma_f32_16x16x32_bf16 v[6:9], v[150:153], v[204:207], v[6:9]
	v_mfma_f32_16x16x32_bf16 v[22:25], v[150:153], v[208:211], v[22:25]
	v_mfma_f32_16x16x32_bf16 v[102:105], v[150:153], v[214:217], v[102:105]
	ds_read_b64_tr_b16 v[146:147], v183 offset:16384
	ds_read_b64_tr_b16 v[148:149], v183 offset:17408
	s_waitcnt lgkmcnt(3)
	v_mfma_f32_16x16x32_bf16 v[86:89], v[154:157], v[200:203], v[86:89]
	v_mfma_f32_16x16x32_bf16 v[54:57], v[154:157], v[204:207], v[54:57]
	v_mfma_f32_16x16x32_bf16 v[82:85], v[154:157], v[208:211], v[82:85]
	v_mfma_f32_16x16x32_bf16 v[126:129], v[154:157], v[214:217], v[126:129]
	ds_read_b64_tr_b16 v[150:151], v184 offset:16384
	ds_read_b64_tr_b16 v[152:153], v184 offset:17408
	s_waitcnt lgkmcnt(2)
	v_mfma_f32_16x16x32_bf16 v[62:65], v[146:149], v[200:203], v[62:65]
	v_mfma_f32_16x16x32_bf16 v[34:37], v[146:149], v[204:207], v[34:37]
	v_mfma_f32_16x16x32_bf16 v[66:69], v[146:149], v[208:211], v[66:69]
	v_mfma_f32_16x16x32_bf16 v[118:121], v[146:149], v[214:217], v[118:121]
	ds_read_b64_tr_b16 v[146:147], v185 offset:16384
	ds_read_b64_tr_b16 v[148:149], v185 offset:17408
	s_waitcnt lgkmcnt(2)
	v_mfma_f32_16x16x32_bf16 v[30:33], v[150:153], v[200:203], v[30:33]
	v_mfma_f32_16x16x32_bf16 v[14:17], v[150:153], v[204:207], v[14:17]
	v_mfma_f32_16x16x32_bf16 v[50:53], v[150:153], v[208:211], v[50:53]
	v_mfma_f32_16x16x32_bf16 v[110:113], v[150:153], v[214:217], v[110:113]
	s_waitcnt lgkmcnt(0)
	v_mfma_f32_16x16x32_bf16 v[10:13], v[146:149], v[200:203], v[10:13]
	ds_read_b64_tr_b16 v[150:151], v171 offset:24576
	ds_read_b64_tr_b16 v[152:153], v171 offset:25600
	ds_read_b128 v[196:199], v187
	ds_read_b128 v[200:203], v187 offset:2048
	v_mfma_f32_16x16x32_bf16 v[2:5], v[146:149], v[204:207], v[2:5]
	v_mfma_f32_16x16x32_bf16 v[26:29], v[146:149], v[208:211], v[26:29]
	ds_read_b128 v[204:207], v187 offset:4096
	ds_read_b128 v[208:211], v187 offset:6144
	v_mfma_f32_16x16x32_bf16 v[98:101], v[146:149], v[214:217], v[98:101]
	ds_read_b64_tr_b16 v[146:147], v179 offset:24576
	ds_read_b64_tr_b16 v[148:149], v179 offset:25600
	s_waitcnt lgkmcnt(5)
	v_mfma_f32_16x16x32_bf16 v[94:97], v[150:153], v[196:199], v[94:97]
	s_waitcnt lgkmcnt(4)
	v_mfma_f32_16x16x32_bf16 v[74:77], v[150:153], v[200:203], v[74:77]
	s_waitcnt lgkmcnt(3)
	v_mfma_f32_16x16x32_bf16 v[78:81], v[150:153], v[204:207], v[78:81]
	s_waitcnt lgkmcnt(2)
	v_mfma_f32_16x16x32_bf16 v[122:125], v[150:153], v[208:211], v[122:125]
	s_mov_b32 s82, m0
	s_mov_b32 m0, s71
	s_nop 0
	global_load_lds_dwordx4 v169, s[48:49]
	s_mov_b32 m0, s82
	ds_read_b64_tr_b16 v[150:151], v180 offset:24576
	ds_read_b64_tr_b16 v[152:153], v180 offset:25600
	s_waitcnt lgkmcnt(2)
	v_mfma_f32_16x16x32_bf16 v[90:93], v[146:149], v[196:199], v[90:93]
	s_mov_b32 s82, m0
	s_mov_b32 m0, s72
	s_nop 0
	global_load_lds_dwordx4 v170, s[48:49]
	s_mov_b32 m0, s82
	v_mfma_f32_16x16x32_bf16 v[46:49], v[146:149], v[200:203], v[46:49]
	v_mfma_f32_16x16x32_bf16 v[58:61], v[146:149], v[204:207], v[58:61]
	v_mfma_f32_16x16x32_bf16 v[114:117], v[146:149], v[208:211], v[114:117]
	ds_read_b64_tr_b16 v[146:147], v181 offset:24576
	ds_read_b64_tr_b16 v[148:149], v181 offset:25600
	s_waitcnt lgkmcnt(2)
	v_mfma_f32_16x16x32_bf16 v[70:73], v[150:153], v[196:199], v[70:73]
	s_mov_b32 s82, m0
	s_mov_b32 m0, s73
	s_nop 0
	global_load_lds_dwordx4 v174, s[48:49]
	s_mov_b32 m0, s82
	v_mfma_f32_16x16x32_bf16 v[18:21], v[150:153], v[200:203], v[18:21]
	v_mfma_f32_16x16x32_bf16 v[38:41], v[150:153], v[204:207], v[38:41]
	v_mfma_f32_16x16x32_bf16 v[106:109], v[150:153], v[208:211], v[106:109]
	ds_read_b64_tr_b16 v[150:151], v182 offset:24576
	ds_read_b64_tr_b16 v[152:153], v182 offset:25600
	s_waitcnt lgkmcnt(2)
	v_mfma_f32_16x16x32_bf16 v[42:45], v[146:149], v[196:199], v[42:45]
	s_mov_b32 s82, m0
	s_mov_b32 m0, s74
	s_nop 0
	global_load_lds_dwordx4 v175, s[48:49]
	s_mov_b32 m0, s82
	v_mfma_f32_16x16x32_bf16 v[6:9], v[146:149], v[200:203], v[6:9]
	v_mfma_f32_16x16x32_bf16 v[22:25], v[146:149], v[204:207], v[22:25]
	v_mfma_f32_16x16x32_bf16 v[102:105], v[146:149], v[208:211], v[102:105]
	ds_read_b64_tr_b16 v[146:147], v183 offset:24576
	ds_read_b64_tr_b16 v[148:149], v183 offset:25600
	s_waitcnt lgkmcnt(2)
	v_mfma_f32_16x16x32_bf16 v[86:89], v[150:153], v[196:199], v[86:89]
	s_mov_b32 s82, m0
	s_mov_b32 m0, s75
	s_nop 0
	global_load_lds_dwordx4 v176, s[48:49]
	s_mov_b32 m0, s82
	s_cbranch_vccz .Lmy_tl_279_0
	global_load_dwordx4 v[154:157], v212, s[10:11]
.Lmy_tl_279_0:
	v_mfma_f32_16x16x32_bf16 v[54:57], v[150:153], v[200:203], v[54:57]
	v_mfma_f32_16x16x32_bf16 v[82:85], v[150:153], v[204:207], v[82:85]
	v_mfma_f32_16x16x32_bf16 v[126:129], v[150:153], v[208:211], v[126:129]
	ds_read_b64_tr_b16 v[214:215], v184 offset:24576
	ds_read_b64_tr_b16 v[216:217], v184 offset:25600
	s_waitcnt lgkmcnt(2)
	v_mfma_f32_16x16x32_bf16 v[62:65], v[146:149], v[196:199], v[62:65]
	s_mov_b32 s82, m0
	s_mov_b32 m0, s76
	s_nop 0
	global_load_lds_dwordx4 v177, s[48:49]
	s_mov_b32 m0, s82
	s_cbranch_vccz .Lmy_tl_279_1
	global_load_dwordx4 v[150:153], v212, s[10:11] offset:2048
.Lmy_tl_279_1:
	v_mfma_f32_16x16x32_bf16 v[34:37], v[146:149], v[200:203], v[34:37]
	v_mfma_f32_16x16x32_bf16 v[66:69], v[146:149], v[204:207], v[66:69]
	v_mfma_f32_16x16x32_bf16 v[118:121], v[146:149], v[208:211], v[118:121]
	ds_read_b64_tr_b16 v[224:225], v185 offset:24576
	ds_read_b64_tr_b16 v[226:227], v185 offset:25600
	s_waitcnt lgkmcnt(2)
	v_mfma_f32_16x16x32_bf16 v[30:33], v[214:217], v[196:199], v[30:33]
	s_mov_b32 s82, m0
	s_mov_b32 m0, s77
	s_nop 0
	global_load_lds_dwordx4 v191, s[48:49]
	s_mov_b32 m0, s82
	s_add_u32 s6, s80, 0x81000
	s_addc_u32 s7, s81, 0
	s_cbranch_vccz .Lmy_tl_279_2
	global_load_dwordx4 v[158:161], v212, s[6:7]
.Lmy_tl_279_2:
	v_mfma_f32_16x16x32_bf16 v[14:17], v[214:217], v[200:203], v[14:17]
	v_mfma_f32_16x16x32_bf16 v[50:53], v[214:217], v[204:207], v[50:53]
	v_mfma_f32_16x16x32_bf16 v[110:113], v[214:217], v[208:211], v[110:113]
	s_waitcnt lgkmcnt(0)
	v_mfma_f32_16x16x32_bf16 v[10:13], v[224:227], v[196:199], v[10:13]
	s_mov_b32 s82, m0
	s_mov_b32 m0, s78
	s_nop 0
	global_load_lds_dwordx4 v192, s[48:49]
	s_mov_b32 m0, s82
	s_cbranch_vccz .Lmy_tl_279_3
	global_load_dwordx4 v[146:149], v212, s[6:7] offset:2048

.LBB0_281:
	s_and_b64 vcc, exec, s[8:9]
	s_cbranch_vccz .LBB0_285
	s_mov_b32 s6, m0
	s_mov_b32 m0, s67
	s_nop 0
	global_load_lds_dwordx4 v169, s[18:19]
	s_mov_b32 m0, s6
	v_add_u32_e32 v47, v173, v189
	s_mov_b32 s6, m0
	s_mov_b32 m0, s68
	s_nop 0
	global_load_lds_dwordx4 v170, s[18:19]
	s_mov_b32 m0, s6
	s_waitcnt vmcnt(2)
	v_mov_b32_e32 v18, v60
	v_mov_b32_e32 v19, v61
	v_mov_b32_e32 v20, v62
	v_mov_b32_e32 v21, v63
	v_mov_b32_e32 v6, v64
	v_mov_b32_e32 v7, v65
	v_mov_b32_e32 v8, v66
	v_mov_b32_e32 v9, v67
	v_mov_b32_e32 v14, v68
	v_mov_b32_e32 v15, v69
	v_mov_b32_e32 v16, v70
	v_mov_b32_e32 v17, v71
	v_mov_b32_e32 v2, v72
	v_mov_b32_e32 v3, v73
	v_mov_b32_e32 v4, v74
	v_mov_b32_e32 v5, v75
	v_add_u32_e32 v46, v173, v190
	v_cvt_pk_bf16_f32 v10, v228, v229
	v_cvt_pk_bf16_f32 v11, v230, v231
	ds_write_b64 v186, v[10:11]
	v_cvt_pk_bf16_f32 v10, v236, v237
	v_cvt_pk_bf16_f32 v11, v238, v239
	v_cvt_pk_bf16_f32 v12, v232, v233
	v_cvt_pk_bf16_f32 v13, v234, v235
	ds_write_b64 v47, v[10:11] offset:512
	v_cvt_pk_bf16_f32 v10, v240, v241
	v_cvt_pk_bf16_f32 v11, v242, v243
	v_add_u32_e32 v48, v173, v188
	ds_write_b64 v46, v[12:13] offset:256
	ds_write_b64 v48, v[10:11] offset:768
	global_load_dwordx4 v[38:41], v168, s[38:39]
	global_load_dwordx4 v[26:29], v168, s[38:39] offset:2048
	global_load_dwordx4 v[34:37], v168, s[40:41]
	global_load_dwordx4 v[22:25], v168, s[40:41] offset:2048
	s_waitcnt lgkmcnt(0)
	s_barrier
	v_mov_b32_e32 v10, 0
	s_add_i32 s48, s67, 0x2000
	s_add_i32 s49, s67, 0x2400
	s_mov_b32 s50, 0
	s_mov_b64 s[8:9], 0
	v_mov_b32_e32 v11, v10
	v_mov_b32_e32 v12, v10
	v_mov_b32_e32 v13, v10
	v_mov_b32_e32 v30, v10
	v_mov_b32_e32 v31, v10
	v_mov_b32_e32 v32, v10
	v_mov_b32_e32 v33, v10
	v_mov_b32_e32 v62, v10
	v_mov_b32_e32 v63, v10
	v_mov_b32_e32 v64, v10
	v_mov_b32_e32 v65, v10
	v_mov_b32_e32 v86, v10
	v_mov_b32_e32 v87, v10
	v_mov_b32_e32 v88, v10
	v_mov_b32_e32 v89, v10
	v_mov_b32_e32 v42, v10
	v_mov_b32_e32 v43, v10
	v_mov_b32_e32 v44, v10
	v_mov_b32_e32 v45, v10
	v_mov_b32_e32 v70, v10
	v_mov_b32_e32 v71, v10
	v_mov_b32_e32 v72, v10
	v_mov_b32_e32 v73, v10
	v_mov_b32_e32 v90, v10
	v_mov_b32_e32 v91, v10
	v_mov_b32_e32 v92, v10
	v_mov_b32_e32 v93, v10
	v_mov_b32_e32 v94, v10
	v_mov_b32_e32 v95, v10
	v_mov_b32_e32 v96, v10
	v_mov_b32_e32 v97, v10
	s_add_u32 s10, s18, 0x80
	s_addc_u32 s11, s19, 0
	s_mov_b32 s53, m0
	s_mov_b32 m0, s48
	s_nop 0
	global_load_lds_dwordx4 v169, s[10:11]
	s_mov_b32 m0, s53
	s_mov_b32 s53, m0
	s_mov_b32 m0, s49
	s_nop 0
	global_load_lds_dwordx4 v170, s[10:11]
	s_mov_b32 m0, s53
.LBB0_283:
	s_cmp_lt_u32 s50, 13
	s_cselect_b64 vcc, -1, 0
	s_min_u32 s6, s50, 12
	s_lshl_b32 s6, s6, 17
	s_add_u32 s51, s22, s6
	s_waitcnt vmcnt(6)
	s_addc_u32 s52, s23, 0
	ds_read_b128 v[50:53], v172
	ds_read_b64_tr_b16 v[54:55], v171
	ds_read_b64_tr_b16 v[56:57], v171 offset:1024
	s_add_u32 s6, s51, 0x60000
	ds_read_b64_tr_b16 v[58:59], v179
	ds_read_b64_tr_b16 v[60:61], v179 offset:1024
	s_addc_u32 s7, s52, 0
	s_add_u32 s10, s8, 0x100
	s_min_u32 s10, s10, 0x780
	s_add_u32 s10, s18, s10
	v_cvt_pk_bf16_f32 v18, v18, v19
	v_cvt_pk_bf16_f32 v19, v20, v21
	v_cndmask_b32_e32 v49, 0, v168, vcc
	s_addc_u32 s11, s19, 0
	s_waitcnt lgkmcnt(2)
	v_mfma_f32_16x16x32_bf16 v[54:57], v[54:57], v[50:53], v[94:97]
	ds_write_b64 v186, v[18:19] offset:16384
	ds_read_b64_tr_b16 v[18:19], v180
	ds_read_b64_tr_b16 v[20:21], v180 offset:1024
	v_cvt_pk_bf16_f32 v6, v6, v7
	v_cvt_pk_bf16_f32 v7, v8, v9
	s_waitcnt lgkmcnt(3)
	v_mfma_f32_16x16x32_bf16 v[58:61], v[58:61], v[50:53], v[90:93]
	ds_write_b64 v46, v[6:7] offset:16640
	ds_read_b64_tr_b16 v[6:7], v181
	ds_read_b64_tr_b16 v[8:9], v181 offset:1024
	s_waitcnt lgkmcnt(3)
	v_mfma_f32_16x16x32_bf16 v[18:21], v[18:21], v[50:53], v[70:73]
	v_cvt_pk_bf16_f32 v14, v14, v15
	v_cvt_pk_bf16_f32 v15, v16, v17
	ds_write_b64 v47, v[14:15] offset:16896
	ds_read_b64_tr_b16 v[14:15], v182
	ds_read_b64_tr_b16 v[16:17], v182 offset:1024
	s_waitcnt lgkmcnt(3)
	v_mfma_f32_16x16x32_bf16 v[6:9], v[6:9], v[50:53], v[42:45]
	v_cvt_pk_bf16_f32 v2, v2, v3
	v_cvt_pk_bf16_f32 v3, v4, v5
	ds_write_b64 v48, v[2:3] offset:17152
	ds_read_b64_tr_b16 v[2:3], v183
	ds_read_b64_tr_b16 v[4:5], v183 offset:1024
	s_waitcnt lgkmcnt(3)
	v_mfma_f32_16x16x32_bf16 v[14:17], v[14:17], v[50:53], v[86:89]
	ds_read_b64_tr_b16 v[42:43], v184
	ds_read_b64_tr_b16 v[44:45], v184 offset:1024
	s_waitcnt lgkmcnt(2)
	v_mfma_f32_16x16x32_bf16 v[2:5], v[2:5], v[50:53], v[62:65]
	s_nop 2
	ds_read_b64_tr_b16 v[62:63], v185
	ds_read_b64_tr_b16 v[64:65], v185 offset:1024
	s_waitcnt lgkmcnt(2)
	v_mfma_f32_16x16x32_bf16 v[30:33], v[42:45], v[50:53], v[30:33]
	ds_read_b64_tr_b16 v[42:43], v171 offset:8192
	ds_read_b64_tr_b16 v[44:45], v171 offset:9216
	ds_read_b128 v[66:69], v178
	s_waitcnt lgkmcnt(3)
	v_mfma_f32_16x16x32_bf16 v[10:13], v[62:65], v[50:53], v[10:13]
	ds_read_b64_tr_b16 v[50:51], v179 offset:8192
	ds_read_b64_tr_b16 v[52:53], v179 offset:9216
	s_waitcnt lgkmcnt(2)
	v_mfma_f32_16x16x32_bf16 v[42:45], v[42:45], v[66:69], v[54:57]
	s_mov_b32 s53, m0
	s_mov_b32 m0, s67
	s_nop 0
	global_load_lds_dwordx4 v169, s[10:11]
	s_mov_b32 m0, s53
	s_nop 2
	ds_read_b64_tr_b16 v[54:55], v180 offset:8192
	ds_read_b64_tr_b16 v[56:57], v180 offset:9216
	s_waitcnt lgkmcnt(2)
	v_mfma_f32_16x16x32_bf16 v[50:53], v[50:53], v[66:69], v[58:61]
	s_mov_b32 s53, m0
	s_mov_b32 m0, s68
	s_nop 0
	global_load_lds_dwordx4 v170, s[10:11]
	s_mov_b32 m0, s53
	s_nop 2
	ds_read_b64_tr_b16 v[58:59], v181 offset:8192
	ds_read_b64_tr_b16 v[60:61], v181 offset:9216
	s_waitcnt lgkmcnt(2)
	v_mfma_f32_16x16x32_bf16 v[54:57], v[54:57], v[66:69], v[18:21]
	s_nop 2
	ds_read_b64_tr_b16 v[18:19], v182 offset:8192
	ds_read_b64_tr_b16 v[20:21], v182 offset:9216
	s_waitcnt lgkmcnt(2)
	v_mfma_f32_16x16x32_bf16 v[58:61], v[58:61], v[66:69], v[6:9]
	s_nop 2
	ds_read_b64_tr_b16 v[6:7], v183 offset:8192
	ds_read_b64_tr_b16 v[8:9], v183 offset:9216
	s_waitcnt lgkmcnt(2)
	v_mfma_f32_16x16x32_bf16 v[62:65], v[18:21], v[66:69], v[14:17]
	global_load_dwordx4 v[18:21], v49, s[6:7]
	s_nop 2
	ds_read_b64_tr_b16 v[14:15], v184 offset:8192
	ds_read_b64_tr_b16 v[16:17], v184 offset:9216
	s_waitcnt lgkmcnt(2)
	v_mfma_f32_16x16x32_bf16 v[70:73], v[6:9], v[66:69], v[2:5]
	global_load_dwordx4 v[6:9], v49, s[6:7] offset:2048
	ds_read_b64_tr_b16 v[74:75], v185 offset:8192
	ds_read_b64_tr_b16 v[76:77], v185 offset:9216
	s_waitcnt lgkmcnt(2)
	v_mfma_f32_16x16x32_bf16 v[30:33], v[14:17], v[66:69], v[30:33]
	s_add_u32 s6, s51, 0x61000
	s_addc_u32 s7, s52, 0
	global_load_dwordx4 v[14:17], v49, s[6:7]
	s_waitcnt lgkmcnt(0)
	v_mfma_f32_16x16x32_bf16 v[10:13], v[74:77], v[66:69], v[10:13]
	global_load_dwordx4 v[2:5], v49, s[6:7] offset:2048
	s_add_i32 s51, s50, 2
	s_cmp_lt_u32 s50, 12
	s_cselect_b64 vcc, -1, 0
	s_min_u32 s6, s50, 11
	s_lshl_b32 s6, s6, 17
	s_waitcnt lgkmcnt(0)
	s_barrier
	s_add_u32 s69, s22, s6
	s_waitcnt vmcnt(6)
	s_addc_u32 s70, s23, 0
	s_add_u32 s10, s69, 0x80000
	ds_read_b64_tr_b16 v[66:67], v171 offset:16384
	ds_read_b64_tr_b16 v[68:69], v171 offset:17408
	ds_read_b128 v[74:77], v172 offset:8192
	s_addc_u32 s11, s70, 0
	s_add_u32 s8, s8, 0x100
	s_addc_u32 s9, s9, 0
	s_cmp_lt_u32 s50, 14
	ds_read_b64_tr_b16 v[78:79], v179 offset:16384
	ds_read_b64_tr_b16 v[80:81], v179 offset:17408
	s_cselect_b64 s[6:7], -1, 0
	s_waitcnt lgkmcnt(2)
	v_mfma_f32_16x16x32_bf16 v[42:45], v[66:69], v[74:77], v[42:45]
	v_cndmask_b32_e32 v49, 0, v168, vcc
	s_and_b64 vcc, s[6:7], exec
	s_add_i32 s50, s8, 0x80
	s_min_u32 s50, s50, 0x780
	s_add_u32 s52, s18, s50
	v_cvt_pk_bf16_f32 v38, v38, v39
	v_cvt_pk_bf16_f32 v39, v40, v41
	s_addc_u32 s53, s19, 0
	ds_write_b64 v186, v[38:39]
	ds_read_b64_tr_b16 v[38:39], v180 offset:16384
	ds_read_b64_tr_b16 v[40:41], v180 offset:17408
	v_cvt_pk_bf16_f32 v26, v26, v27
	v_cvt_pk_bf16_f32 v27, v28, v29
	s_waitcnt lgkmcnt(3)
	v_mfma_f32_16x16x32_bf16 v[50:53], v[78:81], v[74:77], v[50:53]
	ds_write_b64 v46, v[26:27] offset:256
	ds_read_b64_tr_b16 v[26:27], v181 offset:16384
	ds_read_b64_tr_b16 v[28:29], v181 offset:17408
	s_waitcnt lgkmcnt(3)
	v_mfma_f32_16x16x32_bf16 v[38:41], v[38:41], v[74:77], v[54:57]
	v_cvt_pk_bf16_f32 v34, v34, v35
	v_cvt_pk_bf16_f32 v35, v36, v37
	ds_write_b64 v47, v[34:35] offset:512
	ds_read_b64_tr_b16 v[34:35], v182 offset:16384
	ds_read_b64_tr_b16 v[36:37], v182 offset:17408
	s_waitcnt lgkmcnt(3)
	v_mfma_f32_16x16x32_bf16 v[26:29], v[26:29], v[74:77], v[58:61]
	v_cvt_pk_bf16_f32 v22, v22, v23
	v_cvt_pk_bf16_f32 v23, v24, v25
	ds_write_b64 v48, v[22:23] offset:768
	ds_read_b64_tr_b16 v[22:23], v183 offset:16384
	ds_read_b64_tr_b16 v[24:25], v183 offset:17408
	s_waitcnt lgkmcnt(3)
	v_mfma_f32_16x16x32_bf16 v[34:37], v[34:37], v[74:77], v[62:65]
	ds_read_b64_tr_b16 v[54:55], v184 offset:16384
	ds_read_b64_tr_b16 v[56:57], v184 offset:17408
	s_waitcnt lgkmcnt(2)
	v_mfma_f32_16x16x32_bf16 v[22:25], v[22:25], v[74:77], v[70:73]
	ds_read_b64_tr_b16 v[58:59], v185 offset:16384
	ds_read_b64_tr_b16 v[60:61], v185 offset:17408
	s_waitcnt lgkmcnt(2)
	v_mfma_f32_16x16x32_bf16 v[30:33], v[54:57], v[74:77], v[30:33]
	ds_read_b64_tr_b16 v[54:55], v171 offset:24576
	ds_read_b64_tr_b16 v[56:57], v171 offset:25600
	ds_read_b128 v[66:69], v187
	s_waitcnt lgkmcnt(3)
	v_mfma_f32_16x16x32_bf16 v[10:13], v[58:61], v[74:77], v[10:13]
	ds_read_b64_tr_b16 v[58:59], v179 offset:24576
	ds_read_b64_tr_b16 v[60:61], v179 offset:25600
	s_waitcnt lgkmcnt(2)
	v_mfma_f32_16x16x32_bf16 v[94:97], v[54:57], v[66:69], v[42:45]
	s_mov_b32 s50, m0
	s_mov_b32 m0, s48
	s_nop 0
	global_load_lds_dwordx4 v169, s[52:53]
	s_mov_b32 m0, s50
	s_nop 2
	ds_read_b64_tr_b16 v[42:43], v180 offset:24576
	ds_read_b64_tr_b16 v[44:45], v180 offset:25600
	s_waitcnt lgkmcnt(2)
	v_mfma_f32_16x16x32_bf16 v[90:93], v[58:61], v[66:69], v[50:53]
	s_mov_b32 s50, m0
	s_mov_b32 m0, s49
	s_nop 0
	global_load_lds_dwordx4 v170, s[52:53]
	s_mov_b32 m0, s50
	s_nop 2
	ds_read_b64_tr_b16 v[50:51], v181 offset:24576
	ds_read_b64_tr_b16 v[52:53], v181 offset:25600
	s_waitcnt lgkmcnt(2)
	v_mfma_f32_16x16x32_bf16 v[70:73], v[42:45], v[66:69], v[38:41]
	s_nop 2
	ds_read_b64_tr_b16 v[38:39], v182 offset:24576
	ds_read_b64_tr_b16 v[40:41], v182 offset:25600
	s_waitcnt lgkmcnt(2)
	v_mfma_f32_16x16x32_bf16 v[42:45], v[50:53], v[66:69], v[26:29]
	s_nop 2
	ds_read_b64_tr_b16 v[26:27], v183 offset:24576
	ds_read_b64_tr_b16 v[28:29], v183 offset:25600
	s_waitcnt lgkmcnt(2)
	v_mfma_f32_16x16x32_bf16 v[86:89], v[38:41], v[66:69], v[34:37]
	s_cbranch_vccz .Lmy_tl_283_0
	global_load_dwordx4 v[38:41], v49, s[10:11]

.LBB0_869:
	s_sub_i32 s11, s62, s64
	v_mov_b32_e32 v162, v0
	s_min_i32 s11, s11, 0x200
	s_add_i32 s12, s11, 0x7f
	v_readfirstlane_b32 s10, v162
	s_lshr_b32 s66, s12, 7
	s_ashr_i32 s12, s10, 2
	s_and_b32 s12, s12, -16
	s_mul_i32 s12, s12, s66
	s_add_i32 s12, s12, s64
	v_bfe_u32 v2, v162, 3, 3
	v_or_b32_e32 v10, s12, v2
	s_add_i32 s65, s11, s64
	v_mov_b32_e32 v11, s64
	v_cmp_gt_i32_e32 vcc, s65, v10
	v_or_b32_e32 v4, 8, v10
	v_add_u32_e32 v6, 16, v10
	v_cndmask_b32_e32 v2, v11, v10, vcc
	v_cmp_gt_i32_e32 vcc, s65, v4
	s_cmpk_gt_u32 s11, 0x80
	s_cselect_b64 s[44:45], -1, 0
	v_cndmask_b32_e32 v4, v11, v4, vcc
	v_cmp_gt_i32_e32 vcc, s65, v6
	s_and_b64 vcc, s[44:45], vcc
	v_add_u32_e32 v8, 24, v10
	v_cndmask_b32_e32 v6, v11, v6, vcc
	v_cmp_gt_i32_e32 vcc, s65, v8
	s_and_b64 vcc, s[44:45], vcc
	v_ashrrev_i32_e32 v3, 31, v2
	v_ashrrev_i32_e32 v7, 31, v6
	v_cndmask_b32_e32 v8, v11, v8, vcc
	v_lshl_add_u64 v[2:3], v[2:3], 2, s[24:25]
	v_ashrrev_i32_e32 v5, 31, v4
	v_lshl_add_u64 v[6:7], v[6:7], 2, s[24:25]
	v_ashrrev_i32_e32 v9, 31, v8
	v_lshl_add_u64 v[4:5], v[4:5], 2, s[24:25]
	v_lshl_add_u64 v[8:9], v[8:9], 2, s[24:25]
	global_load_dword v12, v[2:3], off
	global_load_dword v13, v[4:5], off
	s_nop 0
	global_load_dword v6, v[6:7], off
	s_nop 0
	global_load_dword v7, v[8:9], off
	v_add_u32_e32 v2, 32, v10
	s_cmpk_gt_u32 s11, 0x100
	s_cselect_b64 s[42:43], -1, 0
	v_cmp_gt_i32_e32 vcc, s65, v2
	s_and_b64 vcc, s[42:43], vcc
	v_add_u32_e32 v4, 40, v10
	v_cndmask_b32_e32 v2, v11, v2, vcc
	v_cmp_gt_i32_e32 vcc, s65, v4
	s_and_b64 vcc, s[42:43], vcc
	v_ashrrev_i32_e32 v3, 31, v2
	v_cndmask_b32_e32 v4, v11, v4, vcc
	v_lshl_add_u64 v[2:3], v[2:3], 2, s[24:25]
	v_ashrrev_i32_e32 v5, 31, v4
	v_lshl_add_u64 v[4:5], v[4:5], 2, s[24:25]
	global_load_dword v8, v[2:3], off
	global_load_dword v9, v[4:5], off
	v_add_u32_e32 v2, 48, v10
	s_cmpk_gt_u32 s11, 0x180
	s_cselect_b64 s[40:41], -1, 0
	v_cmp_gt_i32_e32 vcc, s65, v2
	s_and_b64 vcc, s[40:41], vcc
	v_add_u32_e32 v4, 56, v10
	v_cndmask_b32_e32 v2, v11, v2, vcc
	v_cmp_gt_i32_e32 vcc, s65, v4
	s_and_b64 vcc, s[40:41], vcc
	v_ashrrev_i32_e32 v3, 31, v2
	v_cndmask_b32_e32 v4, v11, v4, vcc
	v_lshl_add_u64 v[2:3], v[2:3], 2, s[24:25]
	v_ashrrev_i32_e32 v5, 31, v4
	v_lshl_add_u64 v[4:5], v[4:5], 2, s[24:25]
	global_load_dword v131, v[2:3], off
	global_load_dword v130, v[4:5], off
	v_and_b32_e32 v10, 31, v162
	v_and_b32_e32 v2, 7, v162
	v_bfe_u32 v3, v162, 4, 2
	v_cmp_gt_u32_e32 vcc, 16, v10
	v_bitop3_b32 v2, v3, v2, 4 bitop3:0x36
	v_ashrrev_i32_e32 v11, 5, v162
	v_cndmask_b32_e32 v15, v166, v167, vcc
	v_bitop3_b32 v14, v3, v162, 7 bitop3:0x78
	v_lshlrev_b32_e32 v132, 4, v2
	v_lshl_add_u32 v2, v10, 4, v15
	v_lshlrev_b32_e32 v133, 4, v14
	v_lshl_or_b32 v168, v11, 13, v2
	global_load_dwordx4 v[228:231], v168, s[22:23]
	global_load_dwordx4 v[232:235], v168, s[22:23] offset:2048
	global_load_dwordx4 v[236:239], v168, s[28:29]
	global_load_dwordx4 v[240:243], v168, s[28:29] offset:2048
	global_load_dwordx4 v[60:63], v168, s[30:31]
	global_load_dwordx4 v[64:67], v168, s[30:31] offset:2048
	global_load_dwordx4 v[68:71], v168, s[34:35]
	global_load_dwordx4 v[72:75], v168, s[34:35] offset:2048
	v_lshrrev_b32_e32 v5, 4, v162
	v_lshlrev_b32_e32 v3, 11, v3
	s_lshl_b32 s10, s10, 8
	s_and_b32 s10, s10, 0xffffc000
	v_and_b32_e32 v4, 15, v162
	s_add_i32 s67, s10, 0
	s_add_i32 s68, s67, 0x400
	s_mov_b64 s[10:11], -1
	s_mov_b64 s[12:13], 0
	s_cmp_lt_i32 s66, 2
	s_mov_b64 s[14:15], 0
	s_waitcnt vmcnt(15)
	v_lshlrev_b32_e32 v2, 8, v12
	v_and_or_b32 v169, v2, s60, v133
	s_waitcnt vmcnt(14)
	v_lshlrev_b32_e32 v2, 8, v13
	v_and_or_b32 v170, v2, s60, v132
	s_waitcnt vmcnt(13)
	v_lshlrev_b32_e32 v2, 8, v6
	s_waitcnt vmcnt(12)
	v_lshlrev_b32_e32 v6, 8, v7
	v_and_or_b32 v175, v6, s60, v132
	v_and_or_b32 v174, v2, s60, v133
	s_waitcnt vmcnt(11)
	v_lshlrev_b32_e32 v2, 8, v8
	s_waitcnt vmcnt(10)
	v_lshlrev_b32_e32 v6, 8, v9
	v_and_or_b32 v177, v6, s60, v132
	v_lshlrev_b32_e32 v6, 3, v162
	v_and_or_b32 v176, v2, s60, v133
	v_lshlrev_b32_e32 v2, 10, v11
	v_and_b32_e32 v6, 24, v6
	v_add3_u32 v173, s61, v2, v6
	v_bfe_u32 v2, v162, 2, 3
	v_bitop3_b32 v134, v2, v5, 4 bitop3:0x78
	v_bfe_u32 v2, v162, 2, 2
	v_lshlrev_b32_e32 v7, 8, v2
	v_add3_u32 v3, s61, v3, v7
	v_lshrrev_b32_e32 v7, 2, v162
	v_and_or_b32 v2, v7, 4, v2
	v_lshlrev_b32_e32 v2, 5, v2
	v_add3_u32 v171, v3, v6, v2
	v_bfe_u32 v3, v162, 1, 3
	v_bitop3_b32 v3, v5, v3, 3 bitop3:0x6c
	v_lshlrev_b32_e32 v2, 7, v4
	v_lshlrev_b32_e32 v3, 4, v3
	v_add3_u32 v172, s67, v2, v3
	s_cbranch_scc1 .LBB0_881
	s_cmp_gt_i32 s66, 2
	s_cbranch_scc0 .LBB0_875
	s_cmp_eq_u32 s66, 3
	s_mov_b64 s[14:15], -1
	s_cbranch_scc0 .LBB0_876
	s_mov_b32 s10, m0
	s_mov_b32 m0, s67
	s_nop 0
	global_load_lds_dwordx4 v169, s[8:9]
	s_mov_b32 m0, s10
	s_add_i32 s50, s67, 0x800
	s_mov_b32 s10, m0
	s_mov_b32 m0, s68
	s_nop 0
	global_load_lds_dwordx4 v170, s[8:9]
	s_mov_b32 m0, s10
	s_add_i32 s51, s67, 0xc00
	s_mov_b32 s10, m0
	s_mov_b32 m0, s50
	s_nop 0
	global_load_lds_dwordx4 v174, s[8:9]
	s_mov_b32 m0, s10
	s_add_i32 s69, s67, 0x1000
	s_mov_b32 s10, m0
	s_mov_b32 m0, s51
	s_nop 0
	global_load_lds_dwordx4 v175, s[8:9]
	s_mov_b32 m0, s10
	s_add_i32 s70, s67, 0x1400
	s_mov_b32 s10, m0
	s_mov_b32 m0, s69
	s_nop 0
	global_load_lds_dwordx4 v176, s[8:9]
	s_mov_b32 m0, s10
	v_mov_b32_e32 v26, 0
	s_mov_b32 s10, m0
	s_mov_b32 m0, s70
	s_nop 0
	global_load_lds_dwordx4 v177, s[8:9]
	s_mov_b32 m0, s10
	s_waitcnt vmcnt(6)
	v_mov_b32_e32 v106, v60
	v_mov_b32_e32 v107, v61
	v_mov_b32_e32 v108, v62
	v_mov_b32_e32 v109, v63
	v_mov_b32_e32 v102, v64
	v_mov_b32_e32 v103, v65
	v_mov_b32_e32 v104, v66
	v_mov_b32_e32 v105, v67
	v_mov_b32_e32 v110, v68
	v_mov_b32_e32 v111, v69
	v_mov_b32_e32 v112, v70
	v_mov_b32_e32 v113, v71
	v_mov_b32_e32 v98, v72
	v_mov_b32_e32 v99, v73
	v_mov_b32_e32 v100, v74
	v_mov_b32_e32 v101, v75
	v_xor_b32_e32 v139, 64, v172
	v_cvt_pk_bf16_f32 v2, v228, v229
	v_cvt_pk_bf16_f32 v3, v230, v231
	v_lshlrev_b32_e32 v4, 5, v134
	v_add_u32_e32 v135, v173, v4
	v_xor_b32_e32 v5, 32, v4
	ds_write_b64 v135, v[2:3]
	v_cvt_pk_bf16_f32 v2, v232, v233
	v_cvt_pk_bf16_f32 v3, v234, v235
	v_add_u32_e32 v136, v173, v5
	v_xor_b32_e32 v5, 64, v4
	ds_write_b64 v136, v[2:3] offset:256
	v_cvt_pk_bf16_f32 v2, v236, v237
	v_cvt_pk_bf16_f32 v3, v238, v239
	v_add_u32_e32 v137, v173, v5
	v_xor_b32_e32 v4, 0x60, v4
	ds_write_b64 v137, v[2:3] offset:512
	v_cvt_pk_bf16_f32 v2, v240, v241
	v_cvt_pk_bf16_f32 v3, v242, v243
	v_add_u32_e32 v138, v173, v4
	ds_write_b64 v138, v[2:3] offset:768
	global_load_dwordx4 v[122:125], v168, s[36:37]
	global_load_dwordx4 v[118:121], v168, s[36:37] offset:2048
	global_load_dwordx4 v[126:129], v168, s[38:39]
	global_load_dwordx4 v[114:117], v168, s[38:39] offset:2048
	s_waitcnt lgkmcnt(0)
	s_barrier
	v_add_u32_e32 v2, 0x2000, v172
	s_add_i32 s71, s67, 0x2000
	v_xor_b32_e32 v140, 64, v2
	v_xor_b32_e32 v141, 32, v171
	v_xor_b32_e32 v142, 64, v171
	v_xor_b32_e32 v143, 0x60, v171
	v_xor_b32_e32 v144, 0x80, v171
	v_xor_b32_e32 v145, 0xa0, v171
	v_xor_b32_e32 v146, 0xc0, v171
	s_add_i32 s72, s67, 0x2400
	v_xor_b32_e32 v147, 0xe0, v171
	s_add_i32 s73, s67, 0x2800
	s_add_i32 s74, s67, 0x2c00
	s_add_i32 s75, s67, 0x3000
	s_add_i32 s76, s67, 0x3400
	s_mov_b32 s48, 0
	s_mov_b64 s[14:15], 0
	v_mov_b32_e32 v27, v26
	v_mov_b32_e32 v28, v26
	v_mov_b32_e32 v29, v26
	v_mov_b32_e32 v2, v26
	v_mov_b32_e32 v3, v26
	v_mov_b32_e32 v4, v26
	v_mov_b32_e32 v5, v26
	v_mov_b32_e32 v10, v26
	v_mov_b32_e32 v11, v26
	v_mov_b32_e32 v12, v26
	v_mov_b32_e32 v13, v26
	v_mov_b32_e32 v50, v26
	v_mov_b32_e32 v51, v26
	v_mov_b32_e32 v52, v26
	v_mov_b32_e32 v53, v26
	v_mov_b32_e32 v14, v26
	v_mov_b32_e32 v15, v26
	v_mov_b32_e32 v16, v26
	v_mov_b32_e32 v17, v26
	v_mov_b32_e32 v30, v26
	v_mov_b32_e32 v31, v26
	v_mov_b32_e32 v32, v26
	v_mov_b32_e32 v33, v26
	v_mov_b32_e32 v66, v26
	v_mov_b32_e32 v67, v26
	v_mov_b32_e32 v68, v26
	v_mov_b32_e32 v69, v26
	v_mov_b32_e32 v34, v26
	v_mov_b32_e32 v35, v26
	v_mov_b32_e32 v36, v26
	v_mov_b32_e32 v37, v26
	v_mov_b32_e32 v62, v26
	v_mov_b32_e32 v63, v26
	v_mov_b32_e32 v64, v26
	v_mov_b32_e32 v65, v26
	v_mov_b32_e32 v82, v26
	v_mov_b32_e32 v83, v26
	v_mov_b32_e32 v84, v26
	v_mov_b32_e32 v85, v26
	v_mov_b32_e32 v54, v26
	v_mov_b32_e32 v55, v26
	v_mov_b32_e32 v56, v26
	v_mov_b32_e32 v57, v26
	v_mov_b32_e32 v86, v26
	v_mov_b32_e32 v87, v26
	v_mov_b32_e32 v88, v26
	v_mov_b32_e32 v89, v26
	v_mov_b32_e32 v22, v26
	v_mov_b32_e32 v23, v26
	v_mov_b32_e32 v24, v26
	v_mov_b32_e32 v25, v26
	v_mov_b32_e32 v6, v26
	v_mov_b32_e32 v7, v26
	v_mov_b32_e32 v8, v26
	v_mov_b32_e32 v9, v26
	v_mov_b32_e32 v42, v26
	v_mov_b32_e32 v43, v26
	v_mov_b32_e32 v44, v26
	v_mov_b32_e32 v45, v26
	v_mov_b32_e32 v38, v26
	v_mov_b32_e32 v39, v26
	v_mov_b32_e32 v40, v26
	v_mov_b32_e32 v41, v26
	v_mov_b32_e32 v18, v26
	v_mov_b32_e32 v19, v26
	v_mov_b32_e32 v20, v26
	v_mov_b32_e32 v21, v26
	v_mov_b32_e32 v70, v26
	v_mov_b32_e32 v71, v26
	v_mov_b32_e32 v72, v26
	v_mov_b32_e32 v73, v26
	v_mov_b32_e32 v58, v26
	v_mov_b32_e32 v59, v26
	v_mov_b32_e32 v60, v26
	v_mov_b32_e32 v61, v26
	v_mov_b32_e32 v46, v26
	v_mov_b32_e32 v47, v26
	v_mov_b32_e32 v48, v26
	v_mov_b32_e32 v49, v26
	v_mov_b32_e32 v90, v26
	v_mov_b32_e32 v91, v26
	v_mov_b32_e32 v92, v26
	v_mov_b32_e32 v93, v26
	v_mov_b32_e32 v78, v26
	v_mov_b32_e32 v79, v26
	v_mov_b32_e32 v80, v26
	v_mov_b32_e32 v81, v26
	v_mov_b32_e32 v74, v26
	v_mov_b32_e32 v75, v26
	v_mov_b32_e32 v76, v26
	v_mov_b32_e32 v77, v26
	v_mov_b32_e32 v94, v26
	v_mov_b32_e32 v95, v26
	v_mov_b32_e32 v96, v26
	v_mov_b32_e32 v97, v26
	s_add_u32 s46, s8, 0x80
	s_addc_u32 s47, s9, 0
	s_mov_b32 s78, m0
	s_mov_b32 m0, s71
	s_nop 0
	global_load_lds_dwordx4 v169, s[46:47]
	s_mov_b32 m0, s78
	s_mov_b32 s78, m0
	s_mov_b32 m0, s72
	s_nop 0
	global_load_lds_dwordx4 v170, s[46:47]
	s_mov_b32 m0, s78
	s_mov_b32 s78, m0
	s_mov_b32 m0, s73
	s_nop 0
	global_load_lds_dwordx4 v174, s[46:47]
	s_mov_b32 m0, s78
	s_mov_b32 s78, m0
	s_mov_b32 m0, s74
	s_nop 0
	global_load_lds_dwordx4 v175, s[46:47]
	s_mov_b32 m0, s78
	s_mov_b32 s78, m0
	s_mov_b32 m0, s75
	s_nop 0
	global_load_lds_dwordx4 v176, s[46:47]
	s_mov_b32 m0, s78
	s_mov_b32 s78, m0
	s_mov_b32 m0, s76
	s_nop 0
	global_load_lds_dwordx4 v177, s[46:47]
	s_mov_b32 m0, s78
.LBB0_873:
	s_waitcnt vmcnt(10)
	s_min_u32 s10, s48, 12
	ds_read_b128 v[148:151], v172
	ds_read_b128 v[152:155], v172 offset:2048
	ds_read_b128 v[156:159], v172 offset:4096
	ds_read_b64_tr_b16 v[178:179], v171
	ds_read_b64_tr_b16 v[180:181], v171 offset:1024
	s_cmp_lt_u32 s48, 13
	s_cselect_b64 vcc, -1, 0
	s_lshl_b32 s10, s10, 17
	s_add_u32 s49, s22, s10
	s_addc_u32 s77, s23, 0
	s_add_u32 s10, s49, 0x60000
	ds_read_b64_tr_b16 v[182:183], v141
	ds_read_b64_tr_b16 v[184:185], v141 offset:1024
	s_addc_u32 s11, s77, 0
	s_waitcnt lgkmcnt(2)
	v_mfma_f32_16x16x32_bf16 v[94:97], v[178:181], v[148:151], v[94:97]
	s_add_u32 s46, s14, 0x100
	s_min_u32 s46, s46, 0x780
	s_add_u32 s46, s8, s46
	v_mfma_f32_16x16x32_bf16 v[74:77], v[178:181], v[152:155], v[74:77]
	v_cvt_pk_bf16_f32 v106, v106, v107
	v_cvt_pk_bf16_f32 v107, v108, v109
	v_cndmask_b32_e32 v160, 0, v168, vcc
	v_mfma_f32_16x16x32_bf16 v[78:81], v[178:181], v[156:159], v[78:81]
	s_addc_u32 s47, s9, 0
	ds_write_b64 v135, v[106:107] offset:16384
	ds_read_b64_tr_b16 v[106:107], v142
	ds_read_b64_tr_b16 v[108:109], v142 offset:1024
	s_waitcnt lgkmcnt(3)
	v_mfma_f32_16x16x32_bf16 v[90:93], v[182:185], v[148:151], v[90:93]
	v_cvt_pk_bf16_f32 v102, v102, v103
	v_cvt_pk_bf16_f32 v103, v104, v105
	ds_write_b64 v136, v[102:103] offset:16640
	v_mfma_f32_16x16x32_bf16 v[46:49], v[182:185], v[152:155], v[46:49]
	v_mfma_f32_16x16x32_bf16 v[58:61], v[182:185], v[156:159], v[58:61]
	ds_read_b64_tr_b16 v[102:103], v143
	ds_read_b64_tr_b16 v[104:105], v143 offset:1024
	s_waitcnt lgkmcnt(3)
	v_mfma_f32_16x16x32_bf16 v[70:73], v[106:109], v[148:151], v[70:73]
	v_cvt_pk_bf16_f32 v110, v110, v111
	v_cvt_pk_bf16_f32 v111, v112, v113
	ds_write_b64 v137, v[110:111] offset:16896
	v_mfma_f32_16x16x32_bf16 v[18:21], v[106:109], v[152:155], v[18:21]
	v_mfma_f32_16x16x32_bf16 v[38:41], v[106:109], v[156:159], v[38:41]
	ds_read_b64_tr_b16 v[106:107], v144
	ds_read_b64_tr_b16 v[108:109], v144 offset:1024
	s_waitcnt lgkmcnt(3)
	v_mfma_f32_16x16x32_bf16 v[42:45], v[102:105], v[148:151], v[42:45]
	v_cvt_pk_bf16_f32 v98, v98, v99
	v_cvt_pk_bf16_f32 v99, v100, v101
	ds_write_b64 v138, v[98:99] offset:17152
	v_mfma_f32_16x16x32_bf16 v[6:9], v[102:105], v[152:155], v[6:9]
	v_mfma_f32_16x16x32_bf16 v[22:25], v[102:105], v[156:159], v[22:25]
	ds_read_b64_tr_b16 v[98:99], v145
	ds_read_b64_tr_b16 v[100:101], v145 offset:1024
	s_waitcnt lgkmcnt(3)
	v_mfma_f32_16x16x32_bf16 v[86:89], v[106:109], v[148:151], v[86:89]
	v_mfma_f32_16x16x32_bf16 v[54:57], v[106:109], v[152:155], v[54:57]
	v_mfma_f32_16x16x32_bf16 v[82:85], v[106:109], v[156:159], v[82:85]
	ds_read_b64_tr_b16 v[102:103], v146
	ds_read_b64_tr_b16 v[104:105], v146 offset:1024
	s_waitcnt lgkmcnt(2)
	v_mfma_f32_16x16x32_bf16 v[62:65], v[98:101], v[148:151], v[62:65]
	v_mfma_f32_16x16x32_bf16 v[34:37], v[98:101], v[152:155], v[34:37]
	v_mfma_f32_16x16x32_bf16 v[66:69], v[98:101], v[156:159], v[66:69]
	ds_read_b64_tr_b16 v[98:99], v147
	ds_read_b64_tr_b16 v[100:101], v147 offset:1024
	s_waitcnt lgkmcnt(2)
	v_mfma_f32_16x16x32_bf16 v[30:33], v[102:105], v[148:151], v[30:33]
	v_mfma_f32_16x16x32_bf16 v[14:17], v[102:105], v[152:155], v[14:17]
	v_mfma_f32_16x16x32_bf16 v[50:53], v[102:105], v[156:159], v[50:53]
	s_waitcnt lgkmcnt(0)
	v_mfma_f32_16x16x32_bf16 v[10:13], v[98:101], v[148:151], v[10:13]
	ds_read_b64_tr_b16 v[102:103], v171 offset:8192
	ds_read_b64_tr_b16 v[104:105], v171 offset:9216
	v_mfma_f32_16x16x32_bf16 v[2:5], v[98:101], v[152:155], v[2:5]
	ds_read_b128 v[148:151], v139
	ds_read_b128 v[152:155], v139 offset:2048
	ds_read_b128 v[178:181], v139 offset:4096
	v_mfma_f32_16x16x32_bf16 v[26:29], v[98:101], v[156:159], v[26:29]
	ds_read_b64_tr_b16 v[98:99], v141 offset:8192
	ds_read_b64_tr_b16 v[100:101], v141 offset:9216
	s_waitcnt lgkmcnt(4)
	v_mfma_f32_16x16x32_bf16 v[94:97], v[102:105], v[148:151], v[94:97]
	s_waitcnt lgkmcnt(3)
	v_mfma_f32_16x16x32_bf16 v[74:77], v[102:105], v[152:155], v[74:77]
	s_waitcnt lgkmcnt(2)
	v_mfma_f32_16x16x32_bf16 v[78:81], v[102:105], v[178:181], v[78:81]
	s_mov_b32 s78, m0
	s_mov_b32 m0, s67
	s_nop 0
	global_load_lds_dwordx4 v169, s[46:47]
	s_mov_b32 m0, s78
	ds_read_b64_tr_b16 v[102:103], v142 offset:8192
	ds_read_b64_tr_b16 v[104:105], v142 offset:9216
	s_waitcnt lgkmcnt(2)
	v_mfma_f32_16x16x32_bf16 v[90:93], v[98:101], v[148:151], v[90:93]
	s_mov_b32 s78, m0
	s_mov_b32 m0, s68
	s_nop 0
	global_load_lds_dwordx4 v170, s[46:47]
	s_mov_b32 m0, s78
	v_mfma_f32_16x16x32_bf16 v[46:49], v[98:101], v[152:155], v[46:49]
	v_mfma_f32_16x16x32_bf16 v[58:61], v[98:101], v[178:181], v[58:61]
	ds_read_b64_tr_b16 v[98:99], v143 offset:8192
	ds_read_b64_tr_b16 v[100:101], v143 offset:9216
	s_waitcnt lgkmcnt(2)
	v_mfma_f32_16x16x32_bf16 v[70:73], v[102:105], v[148:151], v[70:73]
	s_mov_b32 s78, m0
	s_mov_b32 m0, s50
	s_nop 0
	global_load_lds_dwordx4 v174, s[46:47]
	s_mov_b32 m0, s78
	v_mfma_f32_16x16x32_bf16 v[18:21], v[102:105], v[152:155], v[18:21]
	v_mfma_f32_16x16x32_bf16 v[38:41], v[102:105], v[178:181], v[38:41]
	ds_read_b64_tr_b16 v[102:103], v144 offset:8192
	ds_read_b64_tr_b16 v[104:105], v144 offset:9216
	s_waitcnt lgkmcnt(2)
	v_mfma_f32_16x16x32_bf16 v[42:45], v[98:101], v[148:151], v[42:45]
	s_mov_b32 s78, m0
	s_mov_b32 m0, s51
	s_nop 0
	global_load_lds_dwordx4 v175, s[46:47]
	s_mov_b32 m0, s78
	v_mfma_f32_16x16x32_bf16 v[6:9], v[98:101], v[152:155], v[6:9]
	v_mfma_f32_16x16x32_bf16 v[22:25], v[98:101], v[178:181], v[22:25]
	ds_read_b64_tr_b16 v[98:99], v145 offset:8192
	ds_read_b64_tr_b16 v[100:101], v145 offset:9216
	s_waitcnt lgkmcnt(2)
	v_mfma_f32_16x16x32_bf16 v[86:89], v[102:105], v[148:151], v[86:89]
	s_mov_b32 s78, m0
	s_mov_b32 m0, s69
	s_nop 0
	global_load_lds_dwordx4 v176, s[46:47]
	s_mov_b32 m0, s78
	global_load_dwordx4 v[106:109], v160, s[10:11]
	v_mfma_f32_16x16x32_bf16 v[54:57], v[102:105], v[152:155], v[54:57]
	v_mfma_f32_16x16x32_bf16 v[82:85], v[102:105], v[178:181], v[82:85]
	ds_read_b64_tr_b16 v[156:157], v146 offset:8192
	ds_read_b64_tr_b16 v[158:159], v146 offset:9216
	s_waitcnt lgkmcnt(2)
	v_mfma_f32_16x16x32_bf16 v[62:65], v[98:101], v[148:151], v[62:65]
	s_mov_b32 s78, m0
	s_mov_b32 m0, s70
	s_nop 0
	global_load_lds_dwordx4 v177, s[46:47]
	s_mov_b32 m0, s78
	global_load_dwordx4 v[102:105], v160, s[10:11] offset:2048
	v_mfma_f32_16x16x32_bf16 v[34:37], v[98:101], v[152:155], v[34:37]
	v_mfma_f32_16x16x32_bf16 v[66:69], v[98:101], v[178:181], v[66:69]
	ds_read_b64_tr_b16 v[182:183], v147 offset:8192
	ds_read_b64_tr_b16 v[184:185], v147 offset:9216
	s_waitcnt lgkmcnt(2)
	v_mfma_f32_16x16x32_bf16 v[30:33], v[156:159], v[148:151], v[30:33]
	s_add_u32 s10, s49, 0x61000
	s_addc_u32 s11, s77, 0
	global_load_dwordx4 v[110:113], v160, s[10:11]
	v_mfma_f32_16x16x32_bf16 v[14:17], v[156:159], v[152:155], v[14:17]
	v_mfma_f32_16x16x32_bf16 v[50:53], v[156:159], v[178:181], v[50:53]
	s_waitcnt lgkmcnt(0)
	v_mfma_f32_16x16x32_bf16 v[10:13], v[182:185], v[148:151], v[10:13]
	global_load_dwordx4 v[98:101], v160, s[10:11] offset:2048
	v_mfma_f32_16x16x32_bf16 v[2:5], v[182:185], v[152:155], v[2:5]
	v_mfma_f32_16x16x32_bf16 v[26:29], v[182:185], v[178:181], v[26:29]
	s_min_u32 s10, s48, 11
	s_add_i32 s77, s48, 2
	s_cmp_lt_u32 s48, 12
	s_cselect_b64 vcc, -1, 0
	s_lshl_b32 s10, s10, 17
	s_waitcnt lgkmcnt(0)
	s_barrier
	s_add_u32 s78, s22, s10
	s_waitcnt vmcnt(10)
	s_addc_u32 s80, s23, 0
	s_add_u32 s46, s78, 0x80000
	ds_read_b64_tr_b16 v[148:149], v171 offset:16384
	ds_read_b64_tr_b16 v[150:151], v171 offset:17408
	ds_read_b128 v[152:155], v172 offset:8192
	ds_read_b128 v[156:159], v172 offset:10240
	ds_read_b128 v[178:181], v172 offset:12288
	s_addc_u32 s47, s80, 0
	s_add_u32 s14, s14, 0x100
	s_addc_u32 s15, s15, 0
	s_cmp_lt_u32 s48, 14
	ds_read_b64_tr_b16 v[182:183], v141 offset:16384
	ds_read_b64_tr_b16 v[184:185], v141 offset:17408
	s_cselect_b64 s[10:11], -1, 0
	s_waitcnt lgkmcnt(4)
	v_mfma_f32_16x16x32_bf16 v[94:97], v[148:151], v[152:155], v[94:97]
	v_cndmask_b32_e32 v160, 0, v168, vcc
	s_and_b64 vcc, s[10:11], exec
	s_add_i32 s48, s14, 0x80
	s_min_u32 s48, s48, 0x780
	s_waitcnt lgkmcnt(3)
	v_mfma_f32_16x16x32_bf16 v[74:77], v[148:151], v[156:159], v[74:77]
	s_add_u32 s48, s8, s48
	v_cvt_pk_bf16_f32 v122, v122, v123
	v_cvt_pk_bf16_f32 v123, v124, v125
	s_waitcnt lgkmcnt(2)
	v_mfma_f32_16x16x32_bf16 v[78:81], v[148:151], v[178:181], v[78:81]
	s_addc_u32 s49, s9, 0
	ds_write_b64 v135, v[122:123]
	ds_read_b64_tr_b16 v[122:123], v142 offset:16384
	ds_read_b64_tr_b16 v[124:125], v142 offset:17408
	s_waitcnt lgkmcnt(3)
	v_mfma_f32_16x16x32_bf16 v[90:93], v[182:185], v[152:155], v[90:93]
	v_cvt_pk_bf16_f32 v118, v118, v119
	v_cvt_pk_bf16_f32 v119, v120, v121
	ds_write_b64 v136, v[118:119] offset:256
	v_mfma_f32_16x16x32_bf16 v[46:49], v[182:185], v[156:159], v[46:49]
	v_mfma_f32_16x16x32_bf16 v[58:61], v[182:185], v[178:181], v[58:61]
	ds_read_b64_tr_b16 v[118:119], v143 offset:16384
	ds_read_b64_tr_b16 v[120:121], v143 offset:17408
	s_waitcnt lgkmcnt(3)
	v_mfma_f32_16x16x32_bf16 v[70:73], v[122:125], v[152:155], v[70:73]
	v_cvt_pk_bf16_f32 v126, v126, v127
	v_cvt_pk_bf16_f32 v127, v128, v129
	ds_write_b64 v137, v[126:127] offset:512
	v_mfma_f32_16x16x32_bf16 v[18:21], v[122:125], v[156:159], v[18:21]
	v_mfma_f32_16x16x32_bf16 v[38:41], v[122:125], v[178:181], v[38:41]
	ds_read_b64_tr_b16 v[122:123], v144 offset:16384
	ds_read_b64_tr_b16 v[124:125], v144 offset:17408
	s_waitcnt lgkmcnt(3)
	v_mfma_f32_16x16x32_bf16 v[42:45], v[118:121], v[152:155], v[42:45]
	v_cvt_pk_bf16_f32 v114, v114, v115
	v_cvt_pk_bf16_f32 v115, v116, v117
	ds_write_b64 v138, v[114:115] offset:768
	v_mfma_f32_16x16x32_bf16 v[6:9], v[118:121], v[156:159], v[6:9]
	v_mfma_f32_16x16x32_bf16 v[22:25], v[118:121], v[178:181], v[22:25]
	ds_read_b64_tr_b16 v[114:115], v145 offset:16384
	ds_read_b64_tr_b16 v[116:117], v145 offset:17408
	s_waitcnt lgkmcnt(3)
	v_mfma_f32_16x16x32_bf16 v[86:89], v[122:125], v[152:155], v[86:89]
	v_mfma_f32_16x16x32_bf16 v[54:57], v[122:125], v[156:159], v[54:57]
	v_mfma_f32_16x16x32_bf16 v[82:85], v[122:125], v[178:181], v[82:85]
	ds_read_b64_tr_b16 v[118:119], v146 offset:16384
	ds_read_b64_tr_b16 v[120:121], v146 offset:17408
	s_waitcnt lgkmcnt(2)
	v_mfma_f32_16x16x32_bf16 v[62:65], v[114:117], v[152:155], v[62:65]
	v_mfma_f32_16x16x32_bf16 v[34:37], v[114:117], v[156:159], v[34:37]
	v_mfma_f32_16x16x32_bf16 v[66:69], v[114:117], v[178:181], v[66:69]
	ds_read_b64_tr_b16 v[114:115], v147 offset:16384
	ds_read_b64_tr_b16 v[116:117], v147 offset:17408
	s_waitcnt lgkmcnt(2)
	v_mfma_f32_16x16x32_bf16 v[30:33], v[118:121], v[152:155], v[30:33]
	v_mfma_f32_16x16x32_bf16 v[14:17], v[118:121], v[156:159], v[14:17]
	v_mfma_f32_16x16x32_bf16 v[50:53], v[118:121], v[178:181], v[50:53]
	s_waitcnt lgkmcnt(0)
	v_mfma_f32_16x16x32_bf16 v[10:13], v[114:117], v[152:155], v[10:13]
	ds_read_b64_tr_b16 v[118:119], v171 offset:24576
	ds_read_b64_tr_b16 v[120:121], v171 offset:25600
	v_mfma_f32_16x16x32_bf16 v[2:5], v[114:117], v[156:159], v[2:5]
	ds_read_b128 v[148:151], v140
	ds_read_b128 v[152:155], v140 offset:2048
	ds_read_b128 v[156:159], v140 offset:4096
	v_mfma_f32_16x16x32_bf16 v[26:29], v[114:117], v[178:181], v[26:29]
	ds_read_b64_tr_b16 v[114:115], v141 offset:24576
	ds_read_b64_tr_b16 v[116:117], v141 offset:25600
	s_waitcnt lgkmcnt(4)
	v_mfma_f32_16x16x32_bf16 v[94:97], v[118:121], v[148:151], v[94:97]
	s_waitcnt lgkmcnt(3)
	v_mfma_f32_16x16x32_bf16 v[74:77], v[118:121], v[152:155], v[74:77]
	s_waitcnt lgkmcnt(2)
	v_mfma_f32_16x16x32_bf16 v[78:81], v[118:121], v[156:159], v[78:81]
	s_mov_b32 s81, m0
	s_mov_b32 m0, s71
	s_nop 0
	global_load_lds_dwordx4 v169, s[48:49]
	s_mov_b32 m0, s81
	ds_read_b64_tr_b16 v[118:119], v142 offset:24576
	ds_read_b64_tr_b16 v[120:121], v142 offset:25600
	s_waitcnt lgkmcnt(2)
	v_mfma_f32_16x16x32_bf16 v[90:93], v[114:117], v[148:151], v[90:93]
	s_mov_b32 s81, m0
	s_mov_b32 m0, s72
	s_nop 0
	global_load_lds_dwordx4 v170, s[48:49]
	s_mov_b32 m0, s81
	v_mfma_f32_16x16x32_bf16 v[46:49], v[114:117], v[152:155], v[46:49]
	v_mfma_f32_16x16x32_bf16 v[58:61], v[114:117], v[156:159], v[58:61]
	ds_read_b64_tr_b16 v[114:115], v143 offset:24576
	ds_read_b64_tr_b16 v[116:117], v143 offset:25600
	s_waitcnt lgkmcnt(2)
	v_mfma_f32_16x16x32_bf16 v[70:73], v[118:121], v[148:151], v[70:73]
	s_mov_b32 s81, m0
	s_mov_b32 m0, s73
	s_nop 0
	global_load_lds_dwordx4 v174, s[48:49]
	s_mov_b32 m0, s81
	v_mfma_f32_16x16x32_bf16 v[18:21], v[118:121], v[152:155], v[18:21]
	v_mfma_f32_16x16x32_bf16 v[38:41], v[118:121], v[156:159], v[38:41]
	ds_read_b64_tr_b16 v[118:119], v144 offset:24576
	ds_read_b64_tr_b16 v[120:121], v144 offset:25600
	s_waitcnt lgkmcnt(2)
	v_mfma_f32_16x16x32_bf16 v[42:45], v[114:117], v[148:151], v[42:45]
	s_mov_b32 s81, m0
	s_mov_b32 m0, s74
	s_nop 0
	global_load_lds_dwordx4 v175, s[48:49]
	s_mov_b32 m0, s81
	v_mfma_f32_16x16x32_bf16 v[6:9], v[114:117], v[152:155], v[6:9]
	v_mfma_f32_16x16x32_bf16 v[22:25], v[114:117], v[156:159], v[22:25]
	ds_read_b64_tr_b16 v[114:115], v145 offset:24576
	ds_read_b64_tr_b16 v[116:117], v145 offset:25600
	s_waitcnt lgkmcnt(2)
	v_mfma_f32_16x16x32_bf16 v[86:89], v[118:121], v[148:151], v[86:89]
	s_mov_b32 s81, m0
	s_mov_b32 m0, s75
	s_nop 0
	global_load_lds_dwordx4 v176, s[48:49]
	s_mov_b32 m0, s81
	s_cbranch_vccz .Lmy_tl_873_0
	global_load_dwordx4 v[122:125], v160, s[46:47]
.Lmy_tl_873_0:
	v_mfma_f32_16x16x32_bf16 v[54:57], v[118:121], v[152:155], v[54:57]
	v_mfma_f32_16x16x32_bf16 v[82:85], v[118:121], v[156:159], v[82:85]
	ds_read_b64_tr_b16 v[178:179], v146 offset:24576
	ds_read_b64_tr_b16 v[180:181], v146 offset:25600
	s_waitcnt lgkmcnt(2)
	v_mfma_f32_16x16x32_bf16 v[62:65], v[114:117], v[148:151], v[62:65]
	s_mov_b32 s81, m0
	s_mov_b32 m0, s76
	s_nop 0
	global_load_lds_dwordx4 v177, s[48:49]
	s_mov_b32 m0, s81
	s_cbranch_vccz .Lmy_tl_873_1
	global_load_dwordx4 v[118:121], v160, s[46:47] offset:2048

.LBB0_877:
	s_mov_b32 s10, m0
	s_mov_b32 m0, s67
	s_nop 0
	global_load_lds_dwordx4 v169, s[8:9]
	s_mov_b32 m0, s10
	s_add_i32 s69, s67, 0x800
	s_mov_b32 s10, m0
	s_mov_b32 m0, s68
	s_nop 0
	global_load_lds_dwordx4 v170, s[8:9]
	s_mov_b32 m0, s10
	s_add_i32 s70, s67, 0xc00
	s_mov_b32 s10, m0
	s_mov_b32 m0, s69
	s_nop 0
	global_load_lds_dwordx4 v174, s[8:9]
	s_mov_b32 m0, s10
	v_xor_b32_e32 v102, 64, v172
	s_mov_b32 s10, m0
	s_mov_b32 m0, s70
	s_nop 0
	global_load_lds_dwordx4 v175, s[8:9]
	s_mov_b32 m0, s10
	s_waitcnt vmcnt(4)
	v_mov_b32_e32 v38, v60
	v_mov_b32_e32 v39, v61
	v_mov_b32_e32 v40, v62
	v_mov_b32_e32 v41, v63
	v_mov_b32_e32 v26, v64
	v_mov_b32_e32 v27, v65
	v_mov_b32_e32 v28, v66
	v_mov_b32_e32 v29, v67
	v_mov_b32_e32 v50, v68
	v_mov_b32_e32 v51, v69
	v_mov_b32_e32 v52, v70
	v_mov_b32_e32 v53, v71
	v_mov_b32_e32 v22, v72
	v_mov_b32_e32 v23, v73
	v_mov_b32_e32 v24, v74
	v_mov_b32_e32 v25, v75
	s_add_i32 s71, s67, 0x2000
	v_cvt_pk_bf16_f32 v2, v228, v229
	v_cvt_pk_bf16_f32 v3, v230, v231
	v_lshlrev_b32_e32 v4, 5, v134
	v_add_u32_e32 v98, v173, v4
	v_xor_b32_e32 v5, 32, v4
	ds_write_b64 v98, v[2:3]
	v_cvt_pk_bf16_f32 v2, v232, v233
	v_cvt_pk_bf16_f32 v3, v234, v235
	v_add_u32_e32 v99, v173, v5
	v_xor_b32_e32 v5, 64, v4
	ds_write_b64 v99, v[2:3] offset:256
	v_cvt_pk_bf16_f32 v2, v236, v237
	v_cvt_pk_bf16_f32 v3, v238, v239
	v_add_u32_e32 v100, v173, v5
	v_xor_b32_e32 v4, 0x60, v4
	ds_write_b64 v100, v[2:3] offset:512
	v_cvt_pk_bf16_f32 v2, v240, v241
	v_cvt_pk_bf16_f32 v3, v242, v243
	v_add_u32_e32 v101, v173, v4
	ds_write_b64 v101, v[2:3] offset:768
	global_load_dwordx4 v[78:81], v168, s[36:37]
	global_load_dwordx4 v[66:69], v168, s[36:37] offset:2048
	global_load_dwordx4 v[82:85], v168, s[38:39]
	global_load_dwordx4 v[58:61], v168, s[38:39] offset:2048
	s_waitcnt lgkmcnt(0)
	s_barrier
	v_add_u32_e32 v2, 0x2000, v172
	v_xor_b32_e32 v103, 64, v2
	v_mov_b32_e32 v2, 0
	v_xor_b32_e32 v104, 32, v171
	v_xor_b32_e32 v105, 64, v171
	v_xor_b32_e32 v106, 0x60, v171
	v_xor_b32_e32 v107, 0x80, v171
	v_xor_b32_e32 v108, 0xa0, v171
	v_xor_b32_e32 v109, 0xc0, v171
	s_add_i32 s72, s67, 0x2400
	v_xor_b32_e32 v110, 0xe0, v171
	s_add_i32 s73, s67, 0x2800
	s_add_i32 s74, s67, 0x2c00
	s_mov_b32 s50, 0
	s_mov_b64 s[46:47], 0
	v_mov_b32_e32 v3, v2
	v_mov_b32_e32 v4, v2
	v_mov_b32_e32 v5, v2
	v_mov_b32_e32 v10, v2
	v_mov_b32_e32 v11, v2
	v_mov_b32_e32 v12, v2
	v_mov_b32_e32 v13, v2
	v_mov_b32_e32 v14, v2
	v_mov_b32_e32 v15, v2
	v_mov_b32_e32 v16, v2
	v_mov_b32_e32 v17, v2
	v_mov_b32_e32 v30, v2
	v_mov_b32_e32 v31, v2
	v_mov_b32_e32 v32, v2
	v_mov_b32_e32 v33, v2
	v_mov_b32_e32 v34, v2
	v_mov_b32_e32 v35, v2
	v_mov_b32_e32 v36, v2
	v_mov_b32_e32 v37, v2
	v_mov_b32_e32 v62, v2
	v_mov_b32_e32 v63, v2
	v_mov_b32_e32 v64, v2
	v_mov_b32_e32 v65, v2
	v_mov_b32_e32 v54, v2
	v_mov_b32_e32 v55, v2
	v_mov_b32_e32 v56, v2
	v_mov_b32_e32 v57, v2
	v_mov_b32_e32 v86, v2
	v_mov_b32_e32 v87, v2
	v_mov_b32_e32 v88, v2
	v_mov_b32_e32 v89, v2
	v_mov_b32_e32 v6, v2
	v_mov_b32_e32 v7, v2
	v_mov_b32_e32 v8, v2
	v_mov_b32_e32 v9, v2
	v_mov_b32_e32 v42, v2
	v_mov_b32_e32 v43, v2
	v_mov_b32_e32 v44, v2
	v_mov_b32_e32 v45, v2
	v_mov_b32_e32 v18, v2
	v_mov_b32_e32 v19, v2
	v_mov_b32_e32 v20, v2
	v_mov_b32_e32 v21, v2
	v_mov_b32_e32 v70, v2
	v_mov_b32_e32 v71, v2
	v_mov_b32_e32 v72, v2
	v_mov_b32_e32 v73, v2
	v_mov_b32_e32 v46, v2
	v_mov_b32_e32 v47, v2
	v_mov_b32_e32 v48, v2
	v_mov_b32_e32 v49, v2
	v_mov_b32_e32 v90, v2
	v_mov_b32_e32 v91, v2
	v_mov_b32_e32 v92, v2
	v_mov_b32_e32 v93, v2
	v_mov_b32_e32 v74, v2
	v_mov_b32_e32 v75, v2
	v_mov_b32_e32 v76, v2
	v_mov_b32_e32 v77, v2
	v_mov_b32_e32 v94, v2
	v_mov_b32_e32 v95, v2
	v_mov_b32_e32 v96, v2
	v_mov_b32_e32 v97, v2
	s_add_u32 s48, s8, 0x80
	s_addc_u32 s49, s9, 0
	s_mov_b32 s76, m0
	s_mov_b32 m0, s71
	s_nop 0
	global_load_lds_dwordx4 v169, s[48:49]
	s_mov_b32 m0, s76
	s_mov_b32 s76, m0
	s_mov_b32 m0, s72
	s_nop 0
	global_load_lds_dwordx4 v170, s[48:49]
	s_mov_b32 m0, s76
	s_mov_b32 s76, m0
	s_mov_b32 m0, s73
	s_nop 0
	global_load_lds_dwordx4 v174, s[48:49]
	s_mov_b32 m0, s76
	s_mov_b32 s76, m0
	s_mov_b32 m0, s74
	s_nop 0
	global_load_lds_dwordx4 v175, s[48:49]
	s_mov_b32 m0, s76
.LBB0_878:
	s_waitcnt vmcnt(8)
	s_min_u32 s10, s50, 12
	ds_read_b128 v[112:115], v172
	ds_read_b128 v[116:119], v172 offset:2048
	s_cmp_lt_u32 s50, 13
	ds_read_b64_tr_b16 v[120:121], v171
	ds_read_b64_tr_b16 v[122:123], v171 offset:1024
	s_cselect_b64 vcc, -1, 0
	s_lshl_b32 s10, s10, 17
	s_add_u32 s51, s22, s10
	s_addc_u32 s75, s23, 0
	s_add_u32 s10, s51, 0x60000
	ds_read_b64_tr_b16 v[124:125], v104
	ds_read_b64_tr_b16 v[126:127], v104 offset:1024
	s_addc_u32 s11, s75, 0
	s_waitcnt lgkmcnt(2)
	v_mfma_f32_16x16x32_bf16 v[94:97], v[120:123], v[112:115], v[94:97]
	s_add_u32 s48, s46, 0x100
	s_min_u32 s48, s48, 0x780
	s_add_u32 s48, s8, s48
	v_mfma_f32_16x16x32_bf16 v[74:77], v[120:123], v[116:119], v[74:77]
	v_cvt_pk_bf16_f32 v38, v38, v39
	v_cvt_pk_bf16_f32 v39, v40, v41
	v_cndmask_b32_e32 v111, 0, v168, vcc
	s_addc_u32 s49, s9, 0
	ds_write_b64 v98, v[38:39] offset:16384
	ds_read_b64_tr_b16 v[38:39], v105
	ds_read_b64_tr_b16 v[40:41], v105 offset:1024
	v_cvt_pk_bf16_f32 v26, v26, v27
	v_cvt_pk_bf16_f32 v27, v28, v29
	s_waitcnt lgkmcnt(3)
	v_mfma_f32_16x16x32_bf16 v[90:93], v[124:127], v[112:115], v[90:93]
	ds_write_b64 v99, v[26:27] offset:16640
	v_mfma_f32_16x16x32_bf16 v[26:29], v[124:127], v[116:119], v[46:49]
	s_nop 2
	ds_read_b64_tr_b16 v[46:47], v106
	ds_read_b64_tr_b16 v[48:49], v106 offset:1024
	s_waitcnt lgkmcnt(3)
	v_mfma_f32_16x16x32_bf16 v[70:73], v[38:41], v[112:115], v[70:73]
	v_cvt_pk_bf16_f32 v50, v50, v51
	v_cvt_pk_bf16_f32 v51, v52, v53
	ds_write_b64 v100, v[50:51] offset:16896
	v_mfma_f32_16x16x32_bf16 v[18:21], v[38:41], v[116:119], v[18:21]
	ds_read_b64_tr_b16 v[38:39], v107
	ds_read_b64_tr_b16 v[40:41], v107 offset:1024
	s_waitcnt lgkmcnt(3)
	v_mfma_f32_16x16x32_bf16 v[42:45], v[46:49], v[112:115], v[42:45]
	v_cvt_pk_bf16_f32 v22, v22, v23
	v_cvt_pk_bf16_f32 v23, v24, v25
	ds_write_b64 v101, v[22:23] offset:17152
	v_mfma_f32_16x16x32_bf16 v[6:9], v[46:49], v[116:119], v[6:9]
	ds_read_b64_tr_b16 v[46:47], v108
	ds_read_b64_tr_b16 v[48:49], v108 offset:1024
	s_waitcnt lgkmcnt(3)
	v_mfma_f32_16x16x32_bf16 v[22:25], v[38:41], v[112:115], v[86:89]
	v_mfma_f32_16x16x32_bf16 v[50:53], v[38:41], v[116:119], v[54:57]
	ds_read_b64_tr_b16 v[38:39], v109
	ds_read_b64_tr_b16 v[40:41], v109 offset:1024
	s_waitcnt lgkmcnt(2)
	v_mfma_f32_16x16x32_bf16 v[54:57], v[46:49], v[112:115], v[62:65]
	v_mfma_f32_16x16x32_bf16 v[34:37], v[46:49], v[116:119], v[34:37]
	ds_read_b64_tr_b16 v[46:47], v110
	ds_read_b64_tr_b16 v[48:49], v110 offset:1024
	s_waitcnt lgkmcnt(2)
	v_mfma_f32_16x16x32_bf16 v[30:33], v[38:41], v[112:115], v[30:33]
	v_mfma_f32_16x16x32_bf16 v[14:17], v[38:41], v[116:119], v[14:17]
	ds_read_b64_tr_b16 v[38:39], v171 offset:8192
	ds_read_b64_tr_b16 v[40:41], v171 offset:9216
	ds_read_b128 v[62:65], v102
	ds_read_b128 v[86:89], v102 offset:2048
	s_waitcnt lgkmcnt(4)
	v_mfma_f32_16x16x32_bf16 v[10:13], v[46:49], v[112:115], v[10:13]
	v_mfma_f32_16x16x32_bf16 v[2:5], v[46:49], v[116:119], v[2:5]
	s_waitcnt lgkmcnt(1)
	v_mfma_f32_16x16x32_bf16 v[46:49], v[38:41], v[62:65], v[94:97]
	s_nop 2
	ds_read_b64_tr_b16 v[94:95], v104 offset:8192
	ds_read_b64_tr_b16 v[96:97], v104 offset:9216
	s_waitcnt lgkmcnt(2)
	v_mfma_f32_16x16x32_bf16 v[74:77], v[38:41], v[86:89], v[74:77]
	s_mov_b32 s76, m0
	s_mov_b32 m0, s67
	s_nop 0
	global_load_lds_dwordx4 v169, s[48:49]
	s_mov_b32 m0, s76
	ds_read_b64_tr_b16 v[38:39], v105 offset:8192
	ds_read_b64_tr_b16 v[40:41], v105 offset:9216
	s_waitcnt lgkmcnt(2)
	v_mfma_f32_16x16x32_bf16 v[90:93], v[94:97], v[62:65], v[90:93]
	s_mov_b32 s76, m0
	s_mov_b32 m0, s68
	s_nop 0
	global_load_lds_dwordx4 v170, s[48:49]
	s_mov_b32 m0, s76
	v_mfma_f32_16x16x32_bf16 v[94:97], v[94:97], v[86:89], v[26:29]
	s_nop 2
	ds_read_b64_tr_b16 v[26:27], v106 offset:8192
	ds_read_b64_tr_b16 v[28:29], v106 offset:9216
	s_waitcnt lgkmcnt(2)
	v_mfma_f32_16x16x32_bf16 v[70:73], v[38:41], v[62:65], v[70:73]
	s_mov_b32 s76, m0
	s_mov_b32 m0, s69
	s_nop 0
	global_load_lds_dwordx4 v174, s[48:49]
	s_mov_b32 m0, s76
	v_mfma_f32_16x16x32_bf16 v[18:21], v[38:41], v[86:89], v[18:21]
	ds_read_b64_tr_b16 v[112:113], v107 offset:8192
	ds_read_b64_tr_b16 v[114:115], v107 offset:9216
	s_waitcnt lgkmcnt(2)
	v_mfma_f32_16x16x32_bf16 v[42:45], v[26:29], v[62:65], v[42:45]
	s_mov_b32 s76, m0
	s_mov_b32 m0, s70
	s_nop 0
	global_load_lds_dwordx4 v175, s[48:49]
	s_mov_b32 m0, s76
	v_mfma_f32_16x16x32_bf16 v[6:9], v[26:29], v[86:89], v[6:9]
	s_waitcnt lgkmcnt(0)
	v_mfma_f32_16x16x32_bf16 v[116:119], v[112:115], v[62:65], v[22:25]
	s_nop 2
	ds_read_b64_tr_b16 v[22:23], v108 offset:8192
	ds_read_b64_tr_b16 v[24:25], v108 offset:9216
	global_load_dwordx4 v[38:41], v111, s[10:11]
	v_mfma_f32_16x16x32_bf16 v[112:115], v[112:115], v[86:89], v[50:53]
	ds_read_b64_tr_b16 v[120:121], v109 offset:8192
	ds_read_b64_tr_b16 v[122:123], v109 offset:9216
	s_waitcnt lgkmcnt(2)
	v_mfma_f32_16x16x32_bf16 v[54:57], v[22:25], v[62:65], v[54:57]
	global_load_dwordx4 v[26:29], v111, s[10:11] offset:2048
	v_mfma_f32_16x16x32_bf16 v[34:37], v[22:25], v[86:89], v[34:37]
	ds_read_b64_tr_b16 v[124:125], v110 offset:8192
	ds_read_b64_tr_b16 v[126:127], v110 offset:9216
	s_waitcnt lgkmcnt(2)
	v_mfma_f32_16x16x32_bf16 v[30:33], v[120:123], v[62:65], v[30:33]
	s_add_u32 s10, s51, 0x61000
	s_addc_u32 s11, s75, 0
	global_load_dwordx4 v[50:53], v111, s[10:11]
	v_mfma_f32_16x16x32_bf16 v[14:17], v[120:123], v[86:89], v[14:17]
	s_waitcnt lgkmcnt(0)
	v_mfma_f32_16x16x32_bf16 v[10:13], v[124:127], v[62:65], v[10:13]
	global_load_dwordx4 v[22:25], v111, s[10:11] offset:2048
	v_mfma_f32_16x16x32_bf16 v[2:5], v[124:127], v[86:89], v[2:5]
	s_min_u32 s10, s50, 11
	s_add_i32 s75, s50, 2
	s_cmp_lt_u32 s50, 12
	s_cselect_b64 vcc, -1, 0
	s_lshl_b32 s10, s10, 17
	s_waitcnt lgkmcnt(0)
	s_barrier
	s_add_u32 s76, s22, s10
	s_waitcnt vmcnt(8)
	s_addc_u32 s77, s23, 0
	s_add_u32 s48, s76, 0x80000
	ds_read_b64_tr_b16 v[62:63], v171 offset:16384
	ds_read_b64_tr_b16 v[64:65], v171 offset:17408
	ds_read_b128 v[86:89], v172 offset:8192
	ds_read_b128 v[120:123], v172 offset:10240
	s_addc_u32 s49, s77, 0
	s_add_u32 s46, s46, 0x100
	s_addc_u32 s47, s47, 0
	s_cmp_lt_u32 s50, 14
	ds_read_b64_tr_b16 v[124:125], v104 offset:16384
	ds_read_b64_tr_b16 v[126:127], v104 offset:17408
	s_cselect_b64 s[10:11], -1, 0
	s_waitcnt lgkmcnt(3)
	v_mfma_f32_16x16x32_bf16 v[46:49], v[62:65], v[86:89], v[46:49]
	v_cndmask_b32_e32 v111, 0, v168, vcc
	s_and_b64 vcc, s[10:11], exec
	s_add_i32 s50, s46, 0x80
	s_min_u32 s50, s50, 0x780
	s_waitcnt lgkmcnt(2)
	v_mfma_f32_16x16x32_bf16 v[62:65], v[62:65], v[120:123], v[74:77]
	s_add_u32 s50, s8, s50
	s_addc_u32 s51, s9, 0
	s_nop 0
	v_cvt_pk_bf16_f32 v74, v78, v79
	v_cvt_pk_bf16_f32 v75, v80, v81
	ds_write_b64 v98, v[74:75]
	ds_read_b64_tr_b16 v[74:75], v105 offset:16384
	ds_read_b64_tr_b16 v[76:77], v105 offset:17408
	v_cvt_pk_bf16_f32 v66, v66, v67
	v_cvt_pk_bf16_f32 v67, v68, v69
	s_waitcnt lgkmcnt(3)
	v_mfma_f32_16x16x32_bf16 v[78:81], v[124:127], v[86:89], v[90:93]
	ds_write_b64 v99, v[66:67] offset:256
	v_mfma_f32_16x16x32_bf16 v[66:69], v[124:127], v[120:123], v[94:97]
	s_nop 0
	ds_read_b64_tr_b16 v[90:91], v106 offset:16384
	ds_read_b64_tr_b16 v[92:93], v106 offset:17408
	s_waitcnt lgkmcnt(3)
	v_mfma_f32_16x16x32_bf16 v[70:73], v[74:77], v[86:89], v[70:73]
	v_cvt_pk_bf16_f32 v82, v82, v83
	v_cvt_pk_bf16_f32 v83, v84, v85
	ds_write_b64 v100, v[82:83] offset:512
	v_mfma_f32_16x16x32_bf16 v[18:21], v[74:77], v[120:123], v[18:21]
	ds_read_b64_tr_b16 v[74:75], v107 offset:16384
	ds_read_b64_tr_b16 v[76:77], v107 offset:17408
	s_waitcnt lgkmcnt(3)
	v_mfma_f32_16x16x32_bf16 v[42:45], v[90:93], v[86:89], v[42:45]
	v_cvt_pk_bf16_f32 v58, v58, v59
	v_cvt_pk_bf16_f32 v59, v60, v61
	ds_write_b64 v101, v[58:59] offset:768
	v_mfma_f32_16x16x32_bf16 v[6:9], v[90:93], v[120:123], v[6:9]
	ds_read_b64_tr_b16 v[82:83], v108 offset:16384
	ds_read_b64_tr_b16 v[84:85], v108 offset:17408
	s_waitcnt lgkmcnt(3)
	v_mfma_f32_16x16x32_bf16 v[58:61], v[74:77], v[86:89], v[116:119]
	v_mfma_f32_16x16x32_bf16 v[112:115], v[74:77], v[120:123], v[112:115]
	s_waitcnt lgkmcnt(0)
	v_mfma_f32_16x16x32_bf16 v[116:119], v[82:85], v[86:89], v[54:57]
	s_nop 2
	ds_read_b64_tr_b16 v[54:55], v109 offset:16384
	ds_read_b64_tr_b16 v[56:57], v109 offset:17408
	v_mfma_f32_16x16x32_bf16 v[34:37], v[82:85], v[120:123], v[34:37]
	ds_read_b64_tr_b16 v[74:75], v110 offset:16384
	ds_read_b64_tr_b16 v[76:77], v110 offset:17408
	s_waitcnt lgkmcnt(2)
	v_mfma_f32_16x16x32_bf16 v[30:33], v[54:57], v[86:89], v[30:33]
	v_mfma_f32_16x16x32_bf16 v[14:17], v[54:57], v[120:123], v[14:17]
	ds_read_b64_tr_b16 v[54:55], v171 offset:24576
	ds_read_b64_tr_b16 v[56:57], v171 offset:25600
	ds_read_b128 v[124:127], v103
	ds_read_b128 v[136:139], v103 offset:2048
	s_waitcnt lgkmcnt(4)
	v_mfma_f32_16x16x32_bf16 v[10:13], v[74:77], v[86:89], v[10:13]
	v_mfma_f32_16x16x32_bf16 v[2:5], v[74:77], v[120:123], v[2:5]
	s_waitcnt lgkmcnt(1)
	v_mfma_f32_16x16x32_bf16 v[94:97], v[54:57], v[124:127], v[46:49]
	s_nop 2
	ds_read_b64_tr_b16 v[46:47], v104 offset:24576
	ds_read_b64_tr_b16 v[48:49], v104 offset:25600
	s_waitcnt lgkmcnt(2)
	v_mfma_f32_16x16x32_bf16 v[74:77], v[54:57], v[136:139], v[62:65]
	s_mov_b32 s78, m0
	s_mov_b32 m0, s71
	s_nop 0
	global_load_lds_dwordx4 v169, s[50:51]
	s_mov_b32 m0, s78
	ds_read_b64_tr_b16 v[54:55], v105 offset:24576
	ds_read_b64_tr_b16 v[56:57], v105 offset:25600
	s_waitcnt lgkmcnt(2)
	v_mfma_f32_16x16x32_bf16 v[90:93], v[46:49], v[124:127], v[78:81]
	s_mov_b32 s78, m0
	s_mov_b32 m0, s72
	s_nop 0
	global_load_lds_dwordx4 v170, s[50:51]
	s_mov_b32 m0, s78
	v_mfma_f32_16x16x32_bf16 v[46:49], v[46:49], v[136:139], v[66:69]
	ds_read_b64_tr_b16 v[62:63], v106 offset:24576
	ds_read_b64_tr_b16 v[64:65], v106 offset:25600
	s_waitcnt lgkmcnt(2)
	v_mfma_f32_16x16x32_bf16 v[70:73], v[54:57], v[124:127], v[70:73]
	s_mov_b32 s78, m0
	s_mov_b32 m0, s73
	s_nop 0
	global_load_lds_dwordx4 v174, s[50:51]
	s_mov_b32 m0, s78
	v_mfma_f32_16x16x32_bf16 v[18:21], v[54:57], v[136:139], v[18:21]
	ds_read_b64_tr_b16 v[54:55], v107 offset:24576
	ds_read_b64_tr_b16 v[56:57], v107 offset:25600
	s_waitcnt lgkmcnt(2)
	v_mfma_f32_16x16x32_bf16 v[42:45], v[62:65], v[124:127], v[42:45]
	s_mov_b32 s78, m0
	s_mov_b32 m0, s74
	s_nop 0
	global_load_lds_dwordx4 v175, s[50:51]
	s_mov_b32 m0, s78
	v_mfma_f32_16x16x32_bf16 v[6:9], v[62:65], v[136:139], v[6:9]
	s_waitcnt lgkmcnt(0)
	v_mfma_f32_16x16x32_bf16 v[86:89], v[54:57], v[124:127], v[58:61]
	s_nop 2
	ds_read_b64_tr_b16 v[58:59], v108 offset:24576
	ds_read_b64_tr_b16 v[60:61], v108 offset:25600
	s_cbranch_vccz .Lmy_tl_878_0
	global_load_dwordx4 v[78:81], v111, s[48:49]

.LBB0_883:
	v_mov_b32_e32 v125, 0
	v_lshlrev_b32_e32 v98, 5, v134
	v_add_u32_e32 v99, 0x2000, v172
	s_andn2_b64 vcc, exec, s[14:15]
	v_xor_b32_e32 v178, 64, v172
	v_xor_b32_e32 v179, 32, v171
	v_xor_b32_e32 v180, 64, v171
	v_xor_b32_e32 v181, 0x60, v171
	v_xor_b32_e32 v182, 0x80, v171
	v_xor_b32_e32 v183, 0xa0, v171
	v_xor_b32_e32 v184, 0xc0, v171
	v_xor_b32_e32 v185, 0xe0, v171
	v_add_u32_e32 v186, v173, v98
	v_xor_b32_e32 v190, 32, v98
	v_xor_b32_e32 v189, 64, v98
	v_xor_b32_e32 v188, 0x60, v98
	v_xor_b32_e32 v187, 64, v99
	v_mov_b32_e32 v124, v125
	v_mov_b32_e32 v123, v125
	v_mov_b32_e32 v122, v125
	v_mov_b32_e32 v117, v125
	v_mov_b32_e32 v116, v125
	v_mov_b32_e32 v115, v125
	v_mov_b32_e32 v114, v125
	v_mov_b32_e32 v109, v125
	v_mov_b32_e32 v108, v125
	v_mov_b32_e32 v107, v125
	v_mov_b32_e32 v106, v125
	v_mov_b32_e32 v105, v125
	v_mov_b32_e32 v104, v125
	v_mov_b32_e32 v103, v125
	v_mov_b32_e32 v102, v125
	v_mov_b32_e32 v129, v125
	v_mov_b32_e32 v128, v125
	v_mov_b32_e32 v127, v125
	v_mov_b32_e32 v126, v125
	v_mov_b32_e32 v121, v125
	v_mov_b32_e32 v120, v125
	v_mov_b32_e32 v119, v125
	v_mov_b32_e32 v118, v125
	v_mov_b32_e32 v113, v125
	v_mov_b32_e32 v112, v125
	v_mov_b32_e32 v111, v125
	v_mov_b32_e32 v110, v125
	v_mov_b32_e32 v101, v125
	v_mov_b32_e32 v100, v125
	v_mov_b32_e32 v99, v125
	v_mov_b32_e32 v98, v125
	s_cbranch_vccnz .LBB0_887
	s_waitcnt vmcnt(9)
	v_lshlrev_b32_e32 v2, 8, v131
	v_and_or_b32 v191, v2, s60, v133
	s_waitcnt vmcnt(8)
	v_lshlrev_b32_e32 v2, 8, v130
	v_and_or_b32 v192, v2, s60, v132
	s_mov_b32 s10, m0
	s_mov_b32 m0, s67
	s_nop 0
	global_load_lds_dwordx4 v169, s[8:9]
	s_mov_b32 m0, s10
	s_add_i32 s48, s67, 0x800
	s_mov_b32 s10, m0
	s_mov_b32 m0, s68
	s_nop 0
	global_load_lds_dwordx4 v170, s[8:9]
	s_mov_b32 m0, s10
	s_add_i32 s49, s67, 0xc00
	s_mov_b32 s10, m0
	s_mov_b32 m0, s48
	s_nop 0
	global_load_lds_dwordx4 v174, s[8:9]
	s_mov_b32 m0, s10
	s_add_i32 s50, s67, 0x1000
	s_mov_b32 s10, m0
	s_mov_b32 m0, s49
	s_nop 0
	global_load_lds_dwordx4 v175, s[8:9]
	s_mov_b32 m0, s10
	s_add_i32 s51, s67, 0x1400
	s_mov_b32 s10, m0
	s_mov_b32 m0, s50
	s_nop 0
	global_load_lds_dwordx4 v176, s[8:9]
	s_mov_b32 m0, s10
	s_add_i32 s69, s67, 0x1800
	s_mov_b32 s10, m0
	s_mov_b32 m0, s51
	s_nop 0
	global_load_lds_dwordx4 v177, s[8:9]
	s_mov_b32 m0, s10
	s_add_i32 s70, s67, 0x1c00
	s_mov_b32 s10, m0
	s_mov_b32 m0, s69
	s_nop 0
	global_load_lds_dwordx4 v191, s[8:9]
	s_mov_b32 m0, s10
	v_add_u32_e32 v193, v173, v190
	s_mov_b32 s10, m0
	s_mov_b32 m0, s70
	s_nop 0
	global_load_lds_dwordx4 v192, s[8:9]
	s_mov_b32 m0, s10
	s_waitcnt vmcnt(8)
	v_mov_b32_e32 v138, v60
	v_mov_b32_e32 v139, v61
	v_mov_b32_e32 v140, v62
	v_mov_b32_e32 v141, v63
	v_mov_b32_e32 v134, v64
	v_mov_b32_e32 v135, v65
	v_mov_b32_e32 v136, v66
	v_mov_b32_e32 v137, v67
	v_mov_b32_e32 v142, v68
	v_mov_b32_e32 v143, v69
	v_mov_b32_e32 v144, v70
	v_mov_b32_e32 v145, v71
	v_mov_b32_e32 v130, v72
	v_mov_b32_e32 v131, v73
	v_mov_b32_e32 v132, v74
	v_mov_b32_e32 v133, v75
	v_add_u32_e32 v194, v173, v189
	v_cvt_pk_bf16_f32 v2, v228, v229
	v_cvt_pk_bf16_f32 v3, v230, v231
	ds_write_b64 v186, v[2:3]
	v_cvt_pk_bf16_f32 v2, v232, v233
	v_cvt_pk_bf16_f32 v3, v234, v235
	ds_write_b64 v193, v[2:3] offset:256
	v_cvt_pk_bf16_f32 v2, v236, v237
	v_cvt_pk_bf16_f32 v3, v238, v239
	ds_write_b64 v194, v[2:3] offset:512
	v_cvt_pk_bf16_f32 v2, v240, v241
	v_cvt_pk_bf16_f32 v3, v242, v243
	v_add_u32_e32 v195, v173, v188
	ds_write_b64 v195, v[2:3] offset:768
	global_load_dwordx4 v[154:157], v168, s[36:37]
	global_load_dwordx4 v[150:153], v168, s[36:37] offset:2048
	global_load_dwordx4 v[158:161], v168, s[38:39]
	global_load_dwordx4 v[146:149], v168, s[38:39] offset:2048
	s_waitcnt lgkmcnt(0)
	s_barrier
	v_mov_b32_e32 v98, 0
	s_add_i32 s71, s67, 0x2000
	s_add_i32 s72, s67, 0x2400
	s_add_i32 s73, s67, 0x2800
	s_add_i32 s74, s67, 0x2c00
	s_add_i32 s75, s67, 0x3000
	s_add_i32 s76, s67, 0x3400
	s_add_i32 s77, s67, 0x3800
	s_add_i32 s78, s67, 0x3c00
	s_mov_b32 s46, 0
	s_mov_b64 s[12:13], 0
	v_mov_b32_e32 v99, v98
	v_mov_b32_e32 v100, v98
	v_mov_b32_e32 v101, v98
	v_mov_b32_e32 v26, v98
	v_mov_b32_e32 v27, v98
	v_mov_b32_e32 v28, v98
	v_mov_b32_e32 v29, v98
	v_mov_b32_e32 v2, v98
	v_mov_b32_e32 v3, v98
	v_mov_b32_e32 v4, v98
	v_mov_b32_e32 v5, v98
	v_mov_b32_e32 v10, v98
	v_mov_b32_e32 v11, v98
	v_mov_b32_e32 v12, v98
	v_mov_b32_e32 v13, v98
	v_mov_b32_e32 v110, v98
	v_mov_b32_e32 v111, v98
	v_mov_b32_e32 v112, v98
	v_mov_b32_e32 v113, v98
	v_mov_b32_e32 v50, v98
	v_mov_b32_e32 v51, v98
	v_mov_b32_e32 v52, v98
	v_mov_b32_e32 v53, v98
	v_mov_b32_e32 v14, v98
	v_mov_b32_e32 v15, v98
	v_mov_b32_e32 v16, v98
	v_mov_b32_e32 v17, v98
	v_mov_b32_e32 v30, v98
	v_mov_b32_e32 v31, v98
	v_mov_b32_e32 v32, v98
	v_mov_b32_e32 v33, v98
	v_mov_b32_e32 v118, v98
	v_mov_b32_e32 v119, v98
	v_mov_b32_e32 v120, v98
	v_mov_b32_e32 v121, v98
	v_mov_b32_e32 v66, v98
	v_mov_b32_e32 v67, v98
	v_mov_b32_e32 v68, v98
	v_mov_b32_e32 v69, v98
	v_mov_b32_e32 v34, v98
	v_mov_b32_e32 v35, v98
	v_mov_b32_e32 v36, v98
	v_mov_b32_e32 v37, v98
	v_mov_b32_e32 v62, v98
	v_mov_b32_e32 v63, v98
	v_mov_b32_e32 v64, v98
	v_mov_b32_e32 v65, v98
	v_mov_b32_e32 v126, v98
	v_mov_b32_e32 v127, v98
	v_mov_b32_e32 v128, v98
	v_mov_b32_e32 v129, v98
	v_mov_b32_e32 v82, v98
	v_mov_b32_e32 v83, v98
	v_mov_b32_e32 v84, v98
	v_mov_b32_e32 v85, v98
	v_mov_b32_e32 v54, v98
	v_mov_b32_e32 v55, v98
	v_mov_b32_e32 v56, v98
	v_mov_b32_e32 v57, v98
	v_mov_b32_e32 v86, v98
	v_mov_b32_e32 v87, v98
	v_mov_b32_e32 v88, v98
	v_mov_b32_e32 v89, v98
	v_mov_b32_e32 v102, v98
	v_mov_b32_e32 v103, v98
	v_mov_b32_e32 v104, v98
	v_mov_b32_e32 v105, v98
	v_mov_b32_e32 v22, v98
	v_mov_b32_e32 v23, v98
	v_mov_b32_e32 v24, v98
	v_mov_b32_e32 v25, v98
	v_mov_b32_e32 v6, v98
	v_mov_b32_e32 v7, v98
	v_mov_b32_e32 v8, v98
	v_mov_b32_e32 v9, v98
	v_mov_b32_e32 v42, v98
	v_mov_b32_e32 v43, v98
	v_mov_b32_e32 v44, v98
	v_mov_b32_e32 v45, v98
	v_mov_b32_e32 v106, v98
	v_mov_b32_e32 v107, v98
	v_mov_b32_e32 v108, v98
	v_mov_b32_e32 v109, v98
	v_mov_b32_e32 v38, v98
	v_mov_b32_e32 v39, v98
	v_mov_b32_e32 v40, v98
	v_mov_b32_e32 v41, v98
	v_mov_b32_e32 v18, v98
	v_mov_b32_e32 v19, v98
	v_mov_b32_e32 v20, v98
	v_mov_b32_e32 v21, v98
	v_mov_b32_e32 v70, v98
	v_mov_b32_e32 v71, v98
	v_mov_b32_e32 v72, v98
	v_mov_b32_e32 v73, v98
	v_mov_b32_e32 v114, v98
	v_mov_b32_e32 v115, v98
	v_mov_b32_e32 v116, v98
	v_mov_b32_e32 v117, v98
	v_mov_b32_e32 v58, v98
	v_mov_b32_e32 v59, v98
	v_mov_b32_e32 v60, v98
	v_mov_b32_e32 v61, v98
	v_mov_b32_e32 v46, v98
	v_mov_b32_e32 v47, v98
	v_mov_b32_e32 v48, v98
	v_mov_b32_e32 v49, v98
	v_mov_b32_e32 v90, v98
	v_mov_b32_e32 v91, v98
	v_mov_b32_e32 v92, v98
	v_mov_b32_e32 v93, v98
	v_mov_b32_e32 v122, v98
	v_mov_b32_e32 v123, v98
	v_mov_b32_e32 v124, v98
	v_mov_b32_e32 v125, v98
	v_mov_b32_e32 v78, v98
	v_mov_b32_e32 v79, v98
	v_mov_b32_e32 v80, v98
	v_mov_b32_e32 v81, v98
	v_mov_b32_e32 v74, v98
	v_mov_b32_e32 v75, v98
	v_mov_b32_e32 v76, v98
	v_mov_b32_e32 v77, v98
	v_mov_b32_e32 v94, v98
	v_mov_b32_e32 v95, v98
	v_mov_b32_e32 v96, v98
	v_mov_b32_e32 v97, v98
	s_add_u32 s14, s8, 0x80
	s_addc_u32 s15, s9, 0
	s_mov_b32 s81, m0
	s_mov_b32 m0, s71
	s_nop 0
	global_load_lds_dwordx4 v169, s[14:15]
	s_mov_b32 m0, s81
	s_mov_b32 s81, m0
	s_mov_b32 m0, s72
	s_nop 0
	global_load_lds_dwordx4 v170, s[14:15]
	s_mov_b32 m0, s81
	s_mov_b32 s81, m0
	s_mov_b32 m0, s73
	s_nop 0
	global_load_lds_dwordx4 v174, s[14:15]
	s_mov_b32 m0, s81
	s_mov_b32 s81, m0
	s_mov_b32 m0, s74
	s_nop 0
	global_load_lds_dwordx4 v175, s[14:15]
	s_mov_b32 m0, s81
	s_mov_b32 s81, m0
	s_mov_b32 m0, s75
	s_nop 0
	global_load_lds_dwordx4 v176, s[14:15]
	s_mov_b32 m0, s81
	s_mov_b32 s81, m0
	s_mov_b32 m0, s76
	s_nop 0
	global_load_lds_dwordx4 v177, s[14:15]
	s_mov_b32 m0, s81
	s_mov_b32 s81, m0
	s_mov_b32 m0, s77
	s_nop 0
	global_load_lds_dwordx4 v191, s[14:15]
	s_mov_b32 m0, s81
	s_mov_b32 s81, m0
	s_mov_b32 m0, s78
	s_nop 0
	global_load_lds_dwordx4 v192, s[14:15]
	s_mov_b32 m0, s81
.LBB0_885:
	s_waitcnt vmcnt(12)
	s_min_u32 s10, s46, 12
	ds_read_b64_tr_b16 v[196:197], v171
	ds_read_b64_tr_b16 v[198:199], v171 offset:1024
	ds_read_b128 v[200:203], v172
	ds_read_b128 v[204:207], v172 offset:2048
	ds_read_b128 v[208:211], v172 offset:4096
	ds_read_b128 v[212:215], v172 offset:6144
	s_cmp_lt_u32 s46, 13
	s_cselect_b64 vcc, -1, 0
	s_lshl_b32 s10, s10, 17
	s_add_u32 s47, s22, s10
	s_addc_u32 s80, s23, 0
	s_add_u32 s10, s47, 0x60000
	ds_read_b64_tr_b16 v[216:217], v179
	ds_read_b64_tr_b16 v[218:219], v179 offset:1024
	s_waitcnt lgkmcnt(5)
	v_mfma_f32_16x16x32_bf16 v[94:97], v[196:199], v[200:203], v[94:97]
	s_addc_u32 s11, s80, 0
	s_add_u32 s14, s12, 0x100
	s_min_u32 s14, s14, 0x780
	s_waitcnt lgkmcnt(4)
	v_mfma_f32_16x16x32_bf16 v[74:77], v[196:199], v[204:207], v[74:77]
	s_add_u32 s14, s8, s14
	v_cvt_pk_bf16_f32 v138, v138, v139
	v_cvt_pk_bf16_f32 v139, v140, v141
	s_waitcnt lgkmcnt(3)
	v_mfma_f32_16x16x32_bf16 v[78:81], v[196:199], v[208:211], v[78:81]
	v_cndmask_b32_e32 v220, 0, v168, vcc
	s_addc_u32 s15, s9, 0
	ds_write_b64 v186, v[138:139] offset:16384
	s_waitcnt lgkmcnt(3)
	v_mfma_f32_16x16x32_bf16 v[122:125], v[196:199], v[212:215], v[122:125]
	ds_read_b64_tr_b16 v[138:139], v180
	ds_read_b64_tr_b16 v[140:141], v180 offset:1024
	s_waitcnt lgkmcnt(3)
	v_mfma_f32_16x16x32_bf16 v[90:93], v[216:219], v[200:203], v[90:93]
	v_cvt_pk_bf16_f32 v134, v134, v135
	v_cvt_pk_bf16_f32 v135, v136, v137
	ds_write_b64 v193, v[134:135] offset:16640
	v_mfma_f32_16x16x32_bf16 v[46:49], v[216:219], v[204:207], v[46:49]
	v_mfma_f32_16x16x32_bf16 v[58:61], v[216:219], v[208:211], v[58:61]
	v_mfma_f32_16x16x32_bf16 v[114:117], v[216:219], v[212:215], v[114:117]
	ds_read_b64_tr_b16 v[134:135], v181
	ds_read_b64_tr_b16 v[136:137], v181 offset:1024
	s_waitcnt lgkmcnt(3)
	v_mfma_f32_16x16x32_bf16 v[70:73], v[138:141], v[200:203], v[70:73]
	v_cvt_pk_bf16_f32 v142, v142, v143
	v_cvt_pk_bf16_f32 v143, v144, v145
	ds_write_b64 v194, v[142:143] offset:16896
	v_mfma_f32_16x16x32_bf16 v[18:21], v[138:141], v[204:207], v[18:21]
	v_mfma_f32_16x16x32_bf16 v[38:41], v[138:141], v[208:211], v[38:41]
	v_mfma_f32_16x16x32_bf16 v[106:109], v[138:141], v[212:215], v[106:109]
	ds_read_b64_tr_b16 v[138:139], v182
	ds_read_b64_tr_b16 v[140:141], v182 offset:1024
	s_waitcnt lgkmcnt(3)
	v_mfma_f32_16x16x32_bf16 v[42:45], v[134:137], v[200:203], v[42:45]
	v_cvt_pk_bf16_f32 v130, v130, v131
	v_cvt_pk_bf16_f32 v131, v132, v133
	ds_write_b64 v195, v[130:131] offset:17152
	v_mfma_f32_16x16x32_bf16 v[6:9], v[134:137], v[204:207], v[6:9]
	v_mfma_f32_16x16x32_bf16 v[22:25], v[134:137], v[208:211], v[22:25]
	v_mfma_f32_16x16x32_bf16 v[102:105], v[134:137], v[212:215], v[102:105]
	ds_read_b64_tr_b16 v[130:131], v183
	ds_read_b64_tr_b16 v[132:133], v183 offset:1024
	s_waitcnt lgkmcnt(3)
	v_mfma_f32_16x16x32_bf16 v[86:89], v[138:141], v[200:203], v[86:89]
	v_mfma_f32_16x16x32_bf16 v[54:57], v[138:141], v[204:207], v[54:57]
	v_mfma_f32_16x16x32_bf16 v[82:85], v[138:141], v[208:211], v[82:85]
	v_mfma_f32_16x16x32_bf16 v[126:129], v[138:141], v[212:215], v[126:129]
	ds_read_b64_tr_b16 v[134:135], v184
	ds_read_b64_tr_b16 v[136:137], v184 offset:1024
	s_waitcnt lgkmcnt(2)
	v_mfma_f32_16x16x32_bf16 v[62:65], v[130:133], v[200:203], v[62:65]
	v_mfma_f32_16x16x32_bf16 v[34:37], v[130:133], v[204:207], v[34:37]
	v_mfma_f32_16x16x32_bf16 v[66:69], v[130:133], v[208:211], v[66:69]
	v_mfma_f32_16x16x32_bf16 v[118:121], v[130:133], v[212:215], v[118:121]
	ds_read_b64_tr_b16 v[130:131], v185
	ds_read_b64_tr_b16 v[132:133], v185 offset:1024
	s_waitcnt lgkmcnt(2)
	v_mfma_f32_16x16x32_bf16 v[30:33], v[134:137], v[200:203], v[30:33]
	v_mfma_f32_16x16x32_bf16 v[14:17], v[134:137], v[204:207], v[14:17]
	v_mfma_f32_16x16x32_bf16 v[50:53], v[134:137], v[208:211], v[50:53]
	v_mfma_f32_16x16x32_bf16 v[110:113], v[134:137], v[212:215], v[110:113]
	s_waitcnt lgkmcnt(0)
	v_mfma_f32_16x16x32_bf16 v[10:13], v[130:133], v[200:203], v[10:13]
	ds_read_b64_tr_b16 v[134:135], v171 offset:8192
	ds_read_b64_tr_b16 v[136:137], v171 offset:9216
	v_mfma_f32_16x16x32_bf16 v[2:5], v[130:133], v[204:207], v[2:5]
	v_mfma_f32_16x16x32_bf16 v[26:29], v[130:133], v[208:211], v[26:29]
	ds_read_b128 v[196:199], v178
	ds_read_b128 v[200:203], v178 offset:2048
	ds_read_b128 v[204:207], v178 offset:4096
	ds_read_b128 v[208:211], v178 offset:6144
	v_mfma_f32_16x16x32_bf16 v[98:101], v[130:133], v[212:215], v[98:101]
	ds_read_b64_tr_b16 v[130:131], v179 offset:8192
	ds_read_b64_tr_b16 v[132:133], v179 offset:9216
	s_waitcnt lgkmcnt(5)
	v_mfma_f32_16x16x32_bf16 v[94:97], v[134:137], v[196:199], v[94:97]
	s_waitcnt lgkmcnt(4)
	v_mfma_f32_16x16x32_bf16 v[74:77], v[134:137], v[200:203], v[74:77]
	s_waitcnt lgkmcnt(3)
	v_mfma_f32_16x16x32_bf16 v[78:81], v[134:137], v[204:207], v[78:81]
	s_waitcnt lgkmcnt(2)
	v_mfma_f32_16x16x32_bf16 v[122:125], v[134:137], v[208:211], v[122:125]
	s_mov_b32 s81, m0
	s_mov_b32 m0, s67
	s_nop 0
	global_load_lds_dwordx4 v169, s[14:15]
	s_mov_b32 m0, s81
	ds_read_b64_tr_b16 v[134:135], v180 offset:8192
	ds_read_b64_tr_b16 v[136:137], v180 offset:9216
	s_waitcnt lgkmcnt(2)
	v_mfma_f32_16x16x32_bf16 v[90:93], v[130:133], v[196:199], v[90:93]
	s_mov_b32 s81, m0
	s_mov_b32 m0, s68
	s_nop 0
	global_load_lds_dwordx4 v170, s[14:15]
	s_mov_b32 m0, s81
	v_mfma_f32_16x16x32_bf16 v[46:49], v[130:133], v[200:203], v[46:49]
	v_mfma_f32_16x16x32_bf16 v[58:61], v[130:133], v[204:207], v[58:61]
	v_mfma_f32_16x16x32_bf16 v[114:117], v[130:133], v[208:211], v[114:117]
	ds_read_b64_tr_b16 v[130:131], v181 offset:8192
	ds_read_b64_tr_b16 v[132:133], v181 offset:9216
	s_waitcnt lgkmcnt(2)
	v_mfma_f32_16x16x32_bf16 v[70:73], v[134:137], v[196:199], v[70:73]
	s_mov_b32 s81, m0
	s_mov_b32 m0, s48
	s_nop 0
	global_load_lds_dwordx4 v174, s[14:15]
	s_mov_b32 m0, s81
	v_mfma_f32_16x16x32_bf16 v[18:21], v[134:137], v[200:203], v[18:21]
	v_mfma_f32_16x16x32_bf16 v[38:41], v[134:137], v[204:207], v[38:41]
	v_mfma_f32_16x16x32_bf16 v[106:109], v[134:137], v[208:211], v[106:109]
	ds_read_b64_tr_b16 v[134:135], v182 offset:8192
	ds_read_b64_tr_b16 v[136:137], v182 offset:9216
	s_waitcnt lgkmcnt(2)
	v_mfma_f32_16x16x32_bf16 v[42:45], v[130:133], v[196:199], v[42:45]
	s_mov_b32 s81, m0
	s_mov_b32 m0, s49
	s_nop 0
	global_load_lds_dwordx4 v175, s[14:15]
	s_mov_b32 m0, s81
	v_mfma_f32_16x16x32_bf16 v[6:9], v[130:133], v[200:203], v[6:9]
	v_mfma_f32_16x16x32_bf16 v[22:25], v[130:133], v[204:207], v[22:25]
	v_mfma_f32_16x16x32_bf16 v[102:105], v[130:133], v[208:211], v[102:105]
	ds_read_b64_tr_b16 v[130:131], v183 offset:8192
	ds_read_b64_tr_b16 v[132:133], v183 offset:9216
	s_waitcnt lgkmcnt(2)
	v_mfma_f32_16x16x32_bf16 v[86:89], v[134:137], v[196:199], v[86:89]
	s_mov_b32 s81, m0
	s_mov_b32 m0, s50
	s_nop 0
	global_load_lds_dwordx4 v176, s[14:15]
	s_mov_b32 m0, s81
	global_load_dwordx4 v[138:141], v220, s[10:11]
	v_mfma_f32_16x16x32_bf16 v[54:57], v[134:137], v[200:203], v[54:57]
	v_mfma_f32_16x16x32_bf16 v[82:85], v[134:137], v[204:207], v[82:85]
	v_mfma_f32_16x16x32_bf16 v[126:129], v[134:137], v[208:211], v[126:129]
	ds_read_b64_tr_b16 v[212:213], v184 offset:8192
	ds_read_b64_tr_b16 v[214:215], v184 offset:9216
	s_waitcnt lgkmcnt(2)
	v_mfma_f32_16x16x32_bf16 v[62:65], v[130:133], v[196:199], v[62:65]
	s_mov_b32 s81, m0
	s_mov_b32 m0, s51
	s_nop 0
	global_load_lds_dwordx4 v177, s[14:15]
	s_mov_b32 m0, s81
	global_load_dwordx4 v[134:137], v220, s[10:11] offset:2048
	v_mfma_f32_16x16x32_bf16 v[34:37], v[130:133], v[200:203], v[34:37]
	v_mfma_f32_16x16x32_bf16 v[66:69], v[130:133], v[204:207], v[66:69]
	v_mfma_f32_16x16x32_bf16 v[118:121], v[130:133], v[208:211], v[118:121]
	ds_read_b64_tr_b16 v[216:217], v185 offset:8192
	ds_read_b64_tr_b16 v[218:219], v185 offset:9216
	s_waitcnt lgkmcnt(2)
	v_mfma_f32_16x16x32_bf16 v[30:33], v[212:215], v[196:199], v[30:33]
	s_mov_b32 s81, m0
	s_mov_b32 m0, s69
	s_nop 0
	global_load_lds_dwordx4 v191, s[14:15]
	s_mov_b32 m0, s81
	s_add_u32 s10, s47, 0x61000
	s_addc_u32 s11, s80, 0
	global_load_dwordx4 v[142:145], v220, s[10:11]
	v_mfma_f32_16x16x32_bf16 v[14:17], v[212:215], v[200:203], v[14:17]
	v_mfma_f32_16x16x32_bf16 v[50:53], v[212:215], v[204:207], v[50:53]
	v_mfma_f32_16x16x32_bf16 v[110:113], v[212:215], v[208:211], v[110:113]
	s_waitcnt lgkmcnt(0)
	v_mfma_f32_16x16x32_bf16 v[10:13], v[216:219], v[196:199], v[10:13]
	s_mov_b32 s81, m0
	s_mov_b32 m0, s70
	s_nop 0
	global_load_lds_dwordx4 v192, s[14:15]
	s_mov_b32 m0, s81
	global_load_dwordx4 v[130:133], v220, s[10:11] offset:2048
	v_mfma_f32_16x16x32_bf16 v[2:5], v[216:219], v[200:203], v[2:5]
	v_mfma_f32_16x16x32_bf16 v[26:29], v[216:219], v[204:207], v[26:29]
	v_mfma_f32_16x16x32_bf16 v[98:101], v[216:219], v[208:211], v[98:101]
	s_min_u32 s10, s46, 11
	s_add_i32 s80, s46, 2
	s_cmp_lt_u32 s46, 12
	s_cselect_b64 vcc, -1, 0
	s_lshl_b32 s10, s10, 17
	s_waitcnt lgkmcnt(0)
	s_barrier
	s_add_u32 s81, s22, s10
	s_waitcnt vmcnt(12)
	s_addc_u32 s82, s23, 0
	ds_read_b64_tr_b16 v[196:197], v171 offset:16384
	ds_read_b64_tr_b16 v[198:199], v171 offset:17408
	s_add_u32 s14, s81, 0x80000
	ds_read_b128 v[200:203], v172 offset:8192
	ds_read_b128 v[204:207], v172 offset:10240
	ds_read_b128 v[208:211], v172 offset:12288
	ds_read_b128 v[212:215], v172 offset:14336
	s_addc_u32 s15, s82, 0
	s_add_u32 s12, s12, 0x100
	s_addc_u32 s13, s13, 0
	s_cmp_lt_u32 s46, 14
	ds_read_b64_tr_b16 v[216:217], v179 offset:16384
	ds_read_b64_tr_b16 v[218:219], v179 offset:17408
	s_cselect_b64 s[10:11], -1, 0
	s_waitcnt lgkmcnt(5)
	v_mfma_f32_16x16x32_bf16 v[94:97], v[196:199], v[200:203], v[94:97]
	v_cndmask_b32_e32 v220, 0, v168, vcc
	s_and_b64 vcc, s[10:11], exec
	s_add_i32 s46, s12, 0x80
	s_min_u32 s46, s46, 0x780
	s_waitcnt lgkmcnt(4)
	v_mfma_f32_16x16x32_bf16 v[74:77], v[196:199], v[204:207], v[74:77]
	s_add_u32 s46, s8, s46
	v_cvt_pk_bf16_f32 v154, v154, v155
	v_cvt_pk_bf16_f32 v155, v156, v157
	s_waitcnt lgkmcnt(3)
	v_mfma_f32_16x16x32_bf16 v[78:81], v[196:199], v[208:211], v[78:81]
	s_addc_u32 s47, s9, 0
	ds_write_b64 v186, v[154:155]
	s_waitcnt lgkmcnt(3)
	v_mfma_f32_16x16x32_bf16 v[122:125], v[196:199], v[212:215], v[122:125]
	ds_read_b64_tr_b16 v[154:155], v180 offset:16384
	ds_read_b64_tr_b16 v[156:157], v180 offset:17408
	s_waitcnt lgkmcnt(3)
	v_mfma_f32_16x16x32_bf16 v[90:93], v[216:219], v[200:203], v[90:93]
	v_cvt_pk_bf16_f32 v150, v150, v151
	v_cvt_pk_bf16_f32 v151, v152, v153
	ds_write_b64 v193, v[150:151] offset:256
	v_mfma_f32_16x16x32_bf16 v[46:49], v[216:219], v[204:207], v[46:49]
	v_mfma_f32_16x16x32_bf16 v[58:61], v[216:219], v[208:211], v[58:61]
	v_mfma_f32_16x16x32_bf16 v[114:117], v[216:219], v[212:215], v[114:117]
	ds_read_b64_tr_b16 v[150:151], v181 offset:16384
	ds_read_b64_tr_b16 v[152:153], v181 offset:17408
	s_waitcnt lgkmcnt(3)
	v_mfma_f32_16x16x32_bf16 v[70:73], v[154:157], v[200:203], v[70:73]
	v_cvt_pk_bf16_f32 v158, v158, v159
	v_cvt_pk_bf16_f32 v159, v160, v161
	ds_write_b64 v194, v[158:159] offset:512
	v_mfma_f32_16x16x32_bf16 v[18:21], v[154:157], v[204:207], v[18:21]
	v_mfma_f32_16x16x32_bf16 v[38:41], v[154:157], v[208:211], v[38:41]
	v_mfma_f32_16x16x32_bf16 v[106:109], v[154:157], v[212:215], v[106:109]
	ds_read_b64_tr_b16 v[154:155], v182 offset:16384
	ds_read_b64_tr_b16 v[156:157], v182 offset:17408
	s_waitcnt lgkmcnt(3)
	v_mfma_f32_16x16x32_bf16 v[42:45], v[150:153], v[200:203], v[42:45]
	v_cvt_pk_bf16_f32 v146, v146, v147
	v_cvt_pk_bf16_f32 v147, v148, v149
	ds_write_b64 v195, v[146:147] offset:768
	v_mfma_f32_16x16x32_bf16 v[6:9], v[150:153], v[204:207], v[6:9]
	v_mfma_f32_16x16x32_bf16 v[22:25], v[150:153], v[208:211], v[22:25]
	v_mfma_f32_16x16x32_bf16 v[102:105], v[150:153], v[212:215], v[102:105]
	ds_read_b64_tr_b16 v[146:147], v183 offset:16384
	ds_read_b64_tr_b16 v[148:149], v183 offset:17408
	s_waitcnt lgkmcnt(3)
	v_mfma_f32_16x16x32_bf16 v[86:89], v[154:157], v[200:203], v[86:89]
	v_mfma_f32_16x16x32_bf16 v[54:57], v[154:157], v[204:207], v[54:57]
	v_mfma_f32_16x16x32_bf16 v[82:85], v[154:157], v[208:211], v[82:85]
	v_mfma_f32_16x16x32_bf16 v[126:129], v[154:157], v[212:215], v[126:129]
	ds_read_b64_tr_b16 v[150:151], v184 offset:16384
	ds_read_b64_tr_b16 v[152:153], v184 offset:17408
	s_waitcnt lgkmcnt(2)
	v_mfma_f32_16x16x32_bf16 v[62:65], v[146:149], v[200:203], v[62:65]
	v_mfma_f32_16x16x32_bf16 v[34:37], v[146:149], v[204:207], v[34:37]
	v_mfma_f32_16x16x32_bf16 v[66:69], v[146:149], v[208:211], v[66:69]
	v_mfma_f32_16x16x32_bf16 v[118:121], v[146:149], v[212:215], v[118:121]
	ds_read_b64_tr_b16 v[146:147], v185 offset:16384
	ds_read_b64_tr_b16 v[148:149], v185 offset:17408
	s_waitcnt lgkmcnt(2)
	v_mfma_f32_16x16x32_bf16 v[30:33], v[150:153], v[200:203], v[30:33]
	v_mfma_f32_16x16x32_bf16 v[14:17], v[150:153], v[204:207], v[14:17]
	v_mfma_f32_16x16x32_bf16 v[50:53], v[150:153], v[208:211], v[50:53]
	v_mfma_f32_16x16x32_bf16 v[110:113], v[150:153], v[212:215], v[110:113]
	s_waitcnt lgkmcnt(0)
	v_mfma_f32_16x16x32_bf16 v[10:13], v[146:149], v[200:203], v[10:13]
	ds_read_b64_tr_b16 v[150:151], v171 offset:24576
	ds_read_b64_tr_b16 v[152:153], v171 offset:25600
	ds_read_b128 v[196:199], v187
	ds_read_b128 v[200:203], v187 offset:2048
	v_mfma_f32_16x16x32_bf16 v[2:5], v[146:149], v[204:207], v[2:5]
	v_mfma_f32_16x16x32_bf16 v[26:29], v[146:149], v[208:211], v[26:29]
	ds_read_b128 v[204:207], v187 offset:4096
	ds_read_b128 v[208:211], v187 offset:6144
	v_mfma_f32_16x16x32_bf16 v[98:101], v[146:149], v[212:215], v[98:101]
	ds_read_b64_tr_b16 v[146:147], v179 offset:24576
	ds_read_b64_tr_b16 v[148:149], v179 offset:25600
	s_waitcnt lgkmcnt(5)
	v_mfma_f32_16x16x32_bf16 v[94:97], v[150:153], v[196:199], v[94:97]
	s_waitcnt lgkmcnt(4)
	v_mfma_f32_16x16x32_bf16 v[74:77], v[150:153], v[200:203], v[74:77]
	s_waitcnt lgkmcnt(3)
	v_mfma_f32_16x16x32_bf16 v[78:81], v[150:153], v[204:207], v[78:81]
	s_waitcnt lgkmcnt(2)
	v_mfma_f32_16x16x32_bf16 v[122:125], v[150:153], v[208:211], v[122:125]
	s_mov_b32 s83, m0
	s_mov_b32 m0, s71
	s_nop 0
	global_load_lds_dwordx4 v169, s[46:47]
	s_mov_b32 m0, s83
	ds_read_b64_tr_b16 v[150:151], v180 offset:24576
	ds_read_b64_tr_b16 v[152:153], v180 offset:25600
	s_waitcnt lgkmcnt(2)
	v_mfma_f32_16x16x32_bf16 v[90:93], v[146:149], v[196:199], v[90:93]
	s_mov_b32 s83, m0
	s_mov_b32 m0, s72
	s_nop 0
	global_load_lds_dwordx4 v170, s[46:47]
	s_mov_b32 m0, s83
	v_mfma_f32_16x16x32_bf16 v[46:49], v[146:149], v[200:203], v[46:49]
	v_mfma_f32_16x16x32_bf16 v[58:61], v[146:149], v[204:207], v[58:61]
	v_mfma_f32_16x16x32_bf16 v[114:117], v[146:149], v[208:211], v[114:117]
	ds_read_b64_tr_b16 v[146:147], v181 offset:24576
	ds_read_b64_tr_b16 v[148:149], v181 offset:25600
	s_waitcnt lgkmcnt(2)
	v_mfma_f32_16x16x32_bf16 v[70:73], v[150:153], v[196:199], v[70:73]
	s_mov_b32 s83, m0
	s_mov_b32 m0, s73
	s_nop 0
	global_load_lds_dwordx4 v174, s[46:47]
	s_mov_b32 m0, s83
	v_mfma_f32_16x16x32_bf16 v[18:21], v[150:153], v[200:203], v[18:21]
	v_mfma_f32_16x16x32_bf16 v[38:41], v[150:153], v[204:207], v[38:41]
	v_mfma_f32_16x16x32_bf16 v[106:109], v[150:153], v[208:211], v[106:109]
	ds_read_b64_tr_b16 v[150:151], v182 offset:24576
	ds_read_b64_tr_b16 v[152:153], v182 offset:25600
	s_waitcnt lgkmcnt(2)
	v_mfma_f32_16x16x32_bf16 v[42:45], v[146:149], v[196:199], v[42:45]
	s_mov_b32 s83, m0
	s_mov_b32 m0, s74
	s_nop 0
	global_load_lds_dwordx4 v175, s[46:47]
	s_mov_b32 m0, s83
	v_mfma_f32_16x16x32_bf16 v[6:9], v[146:149], v[200:203], v[6:9]
	v_mfma_f32_16x16x32_bf16 v[22:25], v[146:149], v[204:207], v[22:25]
	v_mfma_f32_16x16x32_bf16 v[102:105], v[146:149], v[208:211], v[102:105]
	ds_read_b64_tr_b16 v[146:147], v183 offset:24576
	ds_read_b64_tr_b16 v[148:149], v183 offset:25600
	s_waitcnt lgkmcnt(2)
	v_mfma_f32_16x16x32_bf16 v[86:89], v[150:153], v[196:199], v[86:89]
	s_mov_b32 s83, m0
	s_mov_b32 m0, s75
	s_nop 0
	global_load_lds_dwordx4 v176, s[46:47]
	s_mov_b32 m0, s83
	s_cbranch_vccz .Lmy_tl_885_0
	global_load_dwordx4 v[154:157], v220, s[14:15]
.Lmy_tl_885_0:
	v_mfma_f32_16x16x32_bf16 v[54:57], v[150:153], v[200:203], v[54:57]
	v_mfma_f32_16x16x32_bf16 v[82:85], v[150:153], v[204:207], v[82:85]
	v_mfma_f32_16x16x32_bf16 v[126:129], v[150:153], v[208:211], v[126:129]
	ds_read_b64_tr_b16 v[212:213], v184 offset:24576
	ds_read_b64_tr_b16 v[214:215], v184 offset:25600
	s_waitcnt lgkmcnt(2)
	v_mfma_f32_16x16x32_bf16 v[62:65], v[146:149], v[196:199], v[62:65]
	s_mov_b32 s83, m0
	s_mov_b32 m0, s76
	s_nop 0
	global_load_lds_dwordx4 v177, s[46:47]
	s_mov_b32 m0, s83
	s_cbranch_vccz .Lmy_tl_885_1
	global_load_dwordx4 v[150:153], v220, s[14:15] offset:2048
.Lmy_tl_885_1:
	v_mfma_f32_16x16x32_bf16 v[34:37], v[146:149], v[200:203], v[34:37]
	v_mfma_f32_16x16x32_bf16 v[66:69], v[146:149], v[204:207], v[66:69]
	v_mfma_f32_16x16x32_bf16 v[118:121], v[146:149], v[208:211], v[118:121]
	ds_read_b64_tr_b16 v[216:217], v185 offset:24576
	ds_read_b64_tr_b16 v[218:219], v185 offset:25600
	s_waitcnt lgkmcnt(2)
	v_mfma_f32_16x16x32_bf16 v[30:33], v[212:215], v[196:199], v[30:33]
	s_mov_b32 s83, m0
	s_mov_b32 m0, s77
	s_nop 0
	global_load_lds_dwordx4 v191, s[46:47]
	s_mov_b32 m0, s83
	s_add_u32 s10, s81, 0x81000
	s_addc_u32 s11, s82, 0
	s_cbranch_vccz .Lmy_tl_885_2
	global_load_dwordx4 v[158:161], v220, s[10:11]
.Lmy_tl_885_2:
	v_mfma_f32_16x16x32_bf16 v[14:17], v[212:215], v[200:203], v[14:17]
	v_mfma_f32_16x16x32_bf16 v[50:53], v[212:215], v[204:207], v[50:53]
	v_mfma_f32_16x16x32_bf16 v[110:113], v[212:215], v[208:211], v[110:113]
	s_waitcnt lgkmcnt(0)
	v_mfma_f32_16x16x32_bf16 v[10:13], v[216:219], v[196:199], v[10:13]
	s_mov_b32 s83, m0
	s_mov_b32 m0, s78
	s_nop 0
	global_load_lds_dwordx4 v192, s[46:47]
	s_mov_b32 m0, s83
	s_cbranch_vccz .Lmy_tl_885_3
	global_load_dwordx4 v[146:149], v220, s[10:11] offset:2048

.LBB0_887:
	s_and_b64 vcc, exec, s[12:13]
	s_cbranch_vccz .LBB0_891
	s_mov_b32 s10, m0
	s_mov_b32 m0, s67
	s_nop 0
	global_load_lds_dwordx4 v169, s[8:9]
	s_mov_b32 m0, s10
	v_add_u32_e32 v47, v173, v189
	s_mov_b32 s10, m0
	s_mov_b32 m0, s68
	s_nop 0
	global_load_lds_dwordx4 v170, s[8:9]
	s_mov_b32 m0, s10
	s_waitcnt vmcnt(2)
	v_mov_b32_e32 v18, v60
	v_mov_b32_e32 v19, v61
	v_mov_b32_e32 v20, v62
	v_mov_b32_e32 v21, v63
	v_mov_b32_e32 v6, v64
	v_mov_b32_e32 v7, v65
	v_mov_b32_e32 v8, v66
	v_mov_b32_e32 v9, v67
	v_mov_b32_e32 v14, v68
	v_mov_b32_e32 v15, v69
	v_mov_b32_e32 v16, v70
	v_mov_b32_e32 v17, v71
	v_mov_b32_e32 v2, v72
	v_mov_b32_e32 v3, v73
	v_mov_b32_e32 v4, v74
	v_mov_b32_e32 v5, v75
	v_add_u32_e32 v46, v173, v190
	v_cvt_pk_bf16_f32 v10, v228, v229
	v_cvt_pk_bf16_f32 v11, v230, v231
	ds_write_b64 v186, v[10:11]
	v_cvt_pk_bf16_f32 v10, v236, v237
	v_cvt_pk_bf16_f32 v11, v238, v239
	v_cvt_pk_bf16_f32 v12, v232, v233
	v_cvt_pk_bf16_f32 v13, v234, v235
	ds_write_b64 v47, v[10:11] offset:512
	v_cvt_pk_bf16_f32 v10, v240, v241
	v_cvt_pk_bf16_f32 v11, v242, v243
	v_add_u32_e32 v48, v173, v188
	ds_write_b64 v46, v[12:13] offset:256
	ds_write_b64 v48, v[10:11] offset:768
	global_load_dwordx4 v[38:41], v168, s[36:37]
	global_load_dwordx4 v[26:29], v168, s[36:37] offset:2048
	global_load_dwordx4 v[34:37], v168, s[38:39]
	global_load_dwordx4 v[22:25], v168, s[38:39] offset:2048
	s_waitcnt lgkmcnt(0)
	s_barrier
	v_mov_b32_e32 v10, 0
	s_add_i32 s46, s67, 0x2000
	s_add_i32 s47, s67, 0x2400
	s_mov_b32 s48, 0
	s_mov_b64 s[12:13], 0
	v_mov_b32_e32 v11, v10
	v_mov_b32_e32 v12, v10
	v_mov_b32_e32 v13, v10
	v_mov_b32_e32 v30, v10
	v_mov_b32_e32 v31, v10
	v_mov_b32_e32 v32, v10
	v_mov_b32_e32 v33, v10
	v_mov_b32_e32 v62, v10
	v_mov_b32_e32 v63, v10
	v_mov_b32_e32 v64, v10
	v_mov_b32_e32 v65, v10
	v_mov_b32_e32 v86, v10
	v_mov_b32_e32 v87, v10
	v_mov_b32_e32 v88, v10
	v_mov_b32_e32 v89, v10
	v_mov_b32_e32 v42, v10
	v_mov_b32_e32 v43, v10
	v_mov_b32_e32 v44, v10
	v_mov_b32_e32 v45, v10
	v_mov_b32_e32 v70, v10
	v_mov_b32_e32 v71, v10
	v_mov_b32_e32 v72, v10
	v_mov_b32_e32 v73, v10
	v_mov_b32_e32 v90, v10
	v_mov_b32_e32 v91, v10
	v_mov_b32_e32 v92, v10
	v_mov_b32_e32 v93, v10
	v_mov_b32_e32 v94, v10
	v_mov_b32_e32 v95, v10
	v_mov_b32_e32 v96, v10
	v_mov_b32_e32 v97, v10
	s_add_u32 s14, s8, 0x80
	s_addc_u32 s15, s9, 0
	s_mov_b32 s51, m0
	s_mov_b32 m0, s46
	s_nop 0
	global_load_lds_dwordx4 v169, s[14:15]
	s_mov_b32 m0, s51
	s_mov_b32 s51, m0
	s_mov_b32 m0, s47
	s_nop 0
	global_load_lds_dwordx4 v170, s[14:15]
	s_mov_b32 m0, s51
.LBB0_889:
	s_cmp_lt_u32 s48, 13
	s_cselect_b64 vcc, -1, 0
	s_min_u32 s10, s48, 12
	s_lshl_b32 s10, s10, 17
	s_add_u32 s49, s22, s10
	s_waitcnt vmcnt(6)
	s_addc_u32 s50, s23, 0
	ds_read_b128 v[50:53], v172
	ds_read_b64_tr_b16 v[54:55], v171
	ds_read_b64_tr_b16 v[56:57], v171 offset:1024
	s_add_u32 s10, s49, 0x60000
	ds_read_b64_tr_b16 v[58:59], v179
	ds_read_b64_tr_b16 v[60:61], v179 offset:1024
	s_addc_u32 s11, s50, 0
	s_add_u32 s14, s12, 0x100
	s_min_u32 s14, s14, 0x780
	s_add_u32 s14, s8, s14
	v_cvt_pk_bf16_f32 v18, v18, v19
	v_cvt_pk_bf16_f32 v19, v20, v21
	v_cndmask_b32_e32 v49, 0, v168, vcc
	s_addc_u32 s15, s9, 0
	s_waitcnt lgkmcnt(2)
	v_mfma_f32_16x16x32_bf16 v[54:57], v[54:57], v[50:53], v[94:97]
	ds_write_b64 v186, v[18:19] offset:16384
	ds_read_b64_tr_b16 v[18:19], v180
	ds_read_b64_tr_b16 v[20:21], v180 offset:1024
	v_cvt_pk_bf16_f32 v6, v6, v7
	v_cvt_pk_bf16_f32 v7, v8, v9
	s_waitcnt lgkmcnt(3)
	v_mfma_f32_16x16x32_bf16 v[58:61], v[58:61], v[50:53], v[90:93]
	ds_write_b64 v46, v[6:7] offset:16640
	ds_read_b64_tr_b16 v[6:7], v181
	ds_read_b64_tr_b16 v[8:9], v181 offset:1024
	s_waitcnt lgkmcnt(3)
	v_mfma_f32_16x16x32_bf16 v[18:21], v[18:21], v[50:53], v[70:73]
	v_cvt_pk_bf16_f32 v14, v14, v15
	v_cvt_pk_bf16_f32 v15, v16, v17
	ds_write_b64 v47, v[14:15] offset:16896
	ds_read_b64_tr_b16 v[14:15], v182
	ds_read_b64_tr_b16 v[16:17], v182 offset:1024
	s_waitcnt lgkmcnt(3)
	v_mfma_f32_16x16x32_bf16 v[6:9], v[6:9], v[50:53], v[42:45]
	v_cvt_pk_bf16_f32 v2, v2, v3
	v_cvt_pk_bf16_f32 v3, v4, v5
	ds_write_b64 v48, v[2:3] offset:17152
	ds_read_b64_tr_b16 v[2:3], v183
	ds_read_b64_tr_b16 v[4:5], v183 offset:1024
	s_waitcnt lgkmcnt(3)
	v_mfma_f32_16x16x32_bf16 v[14:17], v[14:17], v[50:53], v[86:89]
	ds_read_b64_tr_b16 v[42:43], v184
	ds_read_b64_tr_b16 v[44:45], v184 offset:1024
	s_waitcnt lgkmcnt(2)
	v_mfma_f32_16x16x32_bf16 v[2:5], v[2:5], v[50:53], v[62:65]
	s_nop 2
	ds_read_b64_tr_b16 v[62:63], v185
	ds_read_b64_tr_b16 v[64:65], v185 offset:1024
	s_waitcnt lgkmcnt(2)
	v_mfma_f32_16x16x32_bf16 v[30:33], v[42:45], v[50:53], v[30:33]
	ds_read_b64_tr_b16 v[42:43], v171 offset:8192
	ds_read_b64_tr_b16 v[44:45], v171 offset:9216
	ds_read_b128 v[66:69], v178
	s_waitcnt lgkmcnt(3)
	v_mfma_f32_16x16x32_bf16 v[10:13], v[62:65], v[50:53], v[10:13]
	ds_read_b64_tr_b16 v[50:51], v179 offset:8192
	ds_read_b64_tr_b16 v[52:53], v179 offset:9216
	s_waitcnt lgkmcnt(2)
	v_mfma_f32_16x16x32_bf16 v[42:45], v[42:45], v[66:69], v[54:57]
	s_mov_b32 s51, m0
	s_mov_b32 m0, s67
	s_nop 0
	global_load_lds_dwordx4 v169, s[14:15]
	s_mov_b32 m0, s51
	s_nop 2
	ds_read_b64_tr_b16 v[54:55], v180 offset:8192
	ds_read_b64_tr_b16 v[56:57], v180 offset:9216
	s_waitcnt lgkmcnt(2)
	v_mfma_f32_16x16x32_bf16 v[50:53], v[50:53], v[66:69], v[58:61]
	s_mov_b32 s51, m0
	s_mov_b32 m0, s68
	s_nop 0
	global_load_lds_dwordx4 v170, s[14:15]
	s_mov_b32 m0, s51
	s_nop 2
	ds_read_b64_tr_b16 v[58:59], v181 offset:8192
	ds_read_b64_tr_b16 v[60:61], v181 offset:9216
	s_waitcnt lgkmcnt(2)
	v_mfma_f32_16x16x32_bf16 v[54:57], v[54:57], v[66:69], v[18:21]
	s_nop 2
	ds_read_b64_tr_b16 v[18:19], v182 offset:8192
	ds_read_b64_tr_b16 v[20:21], v182 offset:9216
	s_waitcnt lgkmcnt(2)
	v_mfma_f32_16x16x32_bf16 v[58:61], v[58:61], v[66:69], v[6:9]
	s_nop 2
	ds_read_b64_tr_b16 v[6:7], v183 offset:8192
	ds_read_b64_tr_b16 v[8:9], v183 offset:9216
	s_waitcnt lgkmcnt(2)
	v_mfma_f32_16x16x32_bf16 v[62:65], v[18:21], v[66:69], v[14:17]
	global_load_dwordx4 v[18:21], v49, s[10:11]
	s_nop 2
	ds_read_b64_tr_b16 v[14:15], v184 offset:8192
	ds_read_b64_tr_b16 v[16:17], v184 offset:9216
	s_waitcnt lgkmcnt(2)
	v_mfma_f32_16x16x32_bf16 v[70:73], v[6:9], v[66:69], v[2:5]
	global_load_dwordx4 v[6:9], v49, s[10:11] offset:2048
	ds_read_b64_tr_b16 v[74:75], v185 offset:8192
	ds_read_b64_tr_b16 v[76:77], v185 offset:9216
	s_waitcnt lgkmcnt(2)
	v_mfma_f32_16x16x32_bf16 v[30:33], v[14:17], v[66:69], v[30:33]
	s_add_u32 s10, s49, 0x61000
	s_addc_u32 s11, s50, 0
	global_load_dwordx4 v[14:17], v49, s[10:11]
	s_waitcnt lgkmcnt(0)
	v_mfma_f32_16x16x32_bf16 v[10:13], v[74:77], v[66:69], v[10:13]
	global_load_dwordx4 v[2:5], v49, s[10:11] offset:2048
	s_add_i32 s49, s48, 2
	s_cmp_lt_u32 s48, 12
	s_cselect_b64 vcc, -1, 0
	s_min_u32 s10, s48, 11
	s_lshl_b32 s10, s10, 17
	s_waitcnt lgkmcnt(0)
	s_barrier
	s_add_u32 s69, s22, s10
	s_waitcnt vmcnt(6)
	s_addc_u32 s70, s23, 0
	s_add_u32 s14, s69, 0x80000
	ds_read_b64_tr_b16 v[66:67], v171 offset:16384
	ds_read_b64_tr_b16 v[68:69], v171 offset:17408
	ds_read_b128 v[74:77], v172 offset:8192
	s_addc_u32 s15, s70, 0
	s_add_u32 s12, s12, 0x100
	s_addc_u32 s13, s13, 0
	s_cmp_lt_u32 s48, 14
	ds_read_b64_tr_b16 v[78:79], v179 offset:16384
	ds_read_b64_tr_b16 v[80:81], v179 offset:17408
	s_cselect_b64 s[10:11], -1, 0
	s_waitcnt lgkmcnt(2)
	v_mfma_f32_16x16x32_bf16 v[42:45], v[66:69], v[74:77], v[42:45]
	v_cndmask_b32_e32 v49, 0, v168, vcc
	s_and_b64 vcc, s[10:11], exec
	s_add_i32 s48, s12, 0x80
	s_min_u32 s48, s48, 0x780
	s_add_u32 s50, s8, s48
	v_cvt_pk_bf16_f32 v38, v38, v39
	v_cvt_pk_bf16_f32 v39, v40, v41
	s_addc_u32 s51, s9, 0
	ds_write_b64 v186, v[38:39]
	ds_read_b64_tr_b16 v[38:39], v180 offset:16384
	ds_read_b64_tr_b16 v[40:41], v180 offset:17408
	v_cvt_pk_bf16_f32 v26, v26, v27
	v_cvt_pk_bf16_f32 v27, v28, v29
	s_waitcnt lgkmcnt(3)
	v_mfma_f32_16x16x32_bf16 v[50:53], v[78:81], v[74:77], v[50:53]
	ds_write_b64 v46, v[26:27] offset:256
	ds_read_b64_tr_b16 v[26:27], v181 offset:16384
	ds_read_b64_tr_b16 v[28:29], v181 offset:17408
	s_waitcnt lgkmcnt(3)
	v_mfma_f32_16x16x32_bf16 v[38:41], v[38:41], v[74:77], v[54:57]
	v_cvt_pk_bf16_f32 v34, v34, v35
	v_cvt_pk_bf16_f32 v35, v36, v37
	ds_write_b64 v47, v[34:35] offset:512
	ds_read_b64_tr_b16 v[34:35], v182 offset:16384
	ds_read_b64_tr_b16 v[36:37], v182 offset:17408
	s_waitcnt lgkmcnt(3)
	v_mfma_f32_16x16x32_bf16 v[26:29], v[26:29], v[74:77], v[58:61]
	v_cvt_pk_bf16_f32 v22, v22, v23
	v_cvt_pk_bf16_f32 v23, v24, v25
	ds_write_b64 v48, v[22:23] offset:768
	ds_read_b64_tr_b16 v[22:23], v183 offset:16384
	ds_read_b64_tr_b16 v[24:25], v183 offset:17408
	s_waitcnt lgkmcnt(3)
	v_mfma_f32_16x16x32_bf16 v[34:37], v[34:37], v[74:77], v[62:65]
	ds_read_b64_tr_b16 v[54:55], v184 offset:16384
	ds_read_b64_tr_b16 v[56:57], v184 offset:17408
	s_waitcnt lgkmcnt(2)
	v_mfma_f32_16x16x32_bf16 v[22:25], v[22:25], v[74:77], v[70:73]
	ds_read_b64_tr_b16 v[58:59], v185 offset:16384
	ds_read_b64_tr_b16 v[60:61], v185 offset:17408
	s_waitcnt lgkmcnt(2)
	v_mfma_f32_16x16x32_bf16 v[30:33], v[54:57], v[74:77], v[30:33]
	ds_read_b64_tr_b16 v[54:55], v171 offset:24576
	ds_read_b64_tr_b16 v[56:57], v171 offset:25600
	ds_read_b128 v[66:69], v187
	s_waitcnt lgkmcnt(3)
	v_mfma_f32_16x16x32_bf16 v[10:13], v[58:61], v[74:77], v[10:13]
	ds_read_b64_tr_b16 v[58:59], v179 offset:24576
	ds_read_b64_tr_b16 v[60:61], v179 offset:25600
	s_waitcnt lgkmcnt(2)
	v_mfma_f32_16x16x32_bf16 v[94:97], v[54:57], v[66:69], v[42:45]
	s_mov_b32 s48, m0
	s_mov_b32 m0, s46
	s_nop 0
	global_load_lds_dwordx4 v169, s[50:51]
	s_mov_b32 m0, s48
	s_nop 2
	ds_read_b64_tr_b16 v[42:43], v180 offset:24576
	ds_read_b64_tr_b16 v[44:45], v180 offset:25600
	s_waitcnt lgkmcnt(2)
	v_mfma_f32_16x16x32_bf16 v[90:93], v[58:61], v[66:69], v[50:53]
	s_mov_b32 s48, m0
	s_mov_b32 m0, s47
	s_nop 0
	global_load_lds_dwordx4 v170, s[50:51]
	s_mov_b32 m0, s48
	s_nop 2
	ds_read_b64_tr_b16 v[50:51], v181 offset:24576
	ds_read_b64_tr_b16 v[52:53], v181 offset:25600
	s_waitcnt lgkmcnt(2)
	v_mfma_f32_16x16x32_bf16 v[70:73], v[42:45], v[66:69], v[38:41]
	s_nop 2
	ds_read_b64_tr_b16 v[38:39], v182 offset:24576
	ds_read_b64_tr_b16 v[40:41], v182 offset:25600
	s_waitcnt lgkmcnt(2)
	v_mfma_f32_16x16x32_bf16 v[42:45], v[50:53], v[66:69], v[26:29]
	s_nop 2
	ds_read_b64_tr_b16 v[26:27], v183 offset:24576
	ds_read_b64_tr_b16 v[28:29], v183 offset:25600
	s_waitcnt lgkmcnt(2)
	v_mfma_f32_16x16x32_bf16 v[86:89], v[38:41], v[66:69], v[34:37]
	s_cbranch_vccz .Lmy_tl_889_0
	global_load_dwordx4 v[38:41], v49, s[14:15]
